# GELU epilogue rescheduled (4 interleaved chains), EpiResid x-row loads prefetched 5 steps ahead with counted vmcnt, barrier leaders poll arrival counter
# speedup vs baseline: 1.0234x; 1.0234x over previous
.LBB0_209:
	s_or_b64 exec, exec, s[6:7]
	s_getreg_b32 s0, hwreg(HW_REG_HW_ID, 0, 6)
	s_lshl_b32 s0, s0, 2
	s_and_b32 s0, s0, 0xfc
	s_add_i32 s0, s0, 0
	s_add_i32 s0, s0, 0x25c00
	v_mov_b32_e32 v0, s0
	ds_read_b32 v0, v0
	s_waitcnt lgkmcnt(0)
	v_readfirstlane_b32 s0, v0
	v_mbcnt_lo_u32_b32 v0, -1, 0
	v_mbcnt_hi_u32_b32 v0, -1, v0
	s_nop 1
	v_lshl_add_u32 v0, s0, 6, v0
	s_nop 0
	v_cmp_eq_u32_e32 vcc, 0, v0
	s_and_saveexec_b64 s[0:1], vcc
	s_cbranch_execz .LBB0_239
	s_add_i32 s3, 0, 0x24808
	v_mov_b32_e32 v0, s3
	s_add_i32 s3, 0, 0x2480c
	v_mov_b32_e32 v1, s3
	ds_read_b32 v0, v0
	ds_read_b32 v1, v1
	s_waitcnt lgkmcnt(0)
	v_cmp_eq_u32_e32 vcc, 0, v1
	s_cbranch_vccnz .LBB0_220
	v_mov_b32_e32 v1, 0x3000
	s_add_i32 s3, 0, 0x24804
	v_mov_b32_e32 v3, s3
	ds_read_b32 v3, v3
	global_load_dword v1, v1, s[94:95] offset:1024 sc1
	s_waitcnt lgkmcnt(0)
	v_mul_lo_u32 v0, v0, v3
	s_add_u32 s6, s94, 0x3400
	s_addc_u32 s7, s95, 0
	s_waitcnt vmcnt(0)
	v_cmp_ge_u32_e32 vcc, v1, v0
	s_cbranch_vccnz .LBB0_225
	s_mov_b32 s3, 1
	v_mov_b32_e32 v1, 0
	s_branch .LBB0_214

.LBB0_216:
	global_load_dword v2, v1, s[6:7] sc1
	s_add_i32 s3, s3, 1
	s_mov_b64 s[10:11], -1
	s_waitcnt vmcnt(0)
	v_cmp_ge_u32_e64 s[8:9], v2, v0
	s_branch .LBB0_213

.LBB0_680:
	s_or_b64 exec, exec, s[4:5]
	s_getreg_b32 s0, hwreg(HW_REG_HW_ID, 0, 6)
	s_lshl_b32 s0, s0, 2
	s_and_b32 s0, s0, 0xfc
	s_add_i32 s0, s0, 0
	s_add_i32 s0, s0, 0x25c00
	v_mov_b32_e32 v0, s0
	ds_read_b32 v0, v0
	s_waitcnt lgkmcnt(0)
	v_readfirstlane_b32 s0, v0
	v_mbcnt_lo_u32_b32 v0, -1, 0
	v_mbcnt_hi_u32_b32 v0, -1, v0
	s_nop 1
	v_lshl_add_u32 v0, s0, 6, v0
	s_nop 0
	v_cmp_eq_u32_e32 vcc, 0, v0
	s_and_saveexec_b64 s[0:1], vcc
	s_cbranch_execz .LBB0_710
	s_add_i32 s3, 0, 0x24808
	v_mov_b32_e32 v0, s3
	s_add_i32 s3, 0, 0x2480c
	v_mov_b32_e32 v1, s3
	ds_read_b32 v0, v0
	ds_read_b32 v1, v1
	s_waitcnt lgkmcnt(0)
	v_cmp_eq_u32_e32 vcc, 0, v1
	s_cbranch_vccnz .LBB0_691
	v_mov_b32_e32 v1, 0x3000
	s_add_i32 s3, 0, 0x24804
	v_mov_b32_e32 v3, s3
	ds_read_b32 v3, v3
	global_load_dword v1, v1, s[94:95] offset:1024 sc1
	s_waitcnt lgkmcnt(0)
	v_mul_lo_u32 v0, v0, v3
	s_add_u32 s4, s94, 0x3400
	s_addc_u32 s5, s95, 0
	s_waitcnt vmcnt(0)
	v_cmp_ge_u32_e32 vcc, v1, v0
	s_cbranch_vccnz .LBB0_696
	s_mov_b32 s3, 1
	v_mov_b32_e32 v1, 0
	s_branch .LBB0_685

.LBB0_687:
	global_load_dword v2, v1, s[4:5] sc1
	s_add_i32 s3, s3, 1
	s_mov_b64 s[10:11], -1
	s_waitcnt vmcnt(0)
	v_cmp_ge_u32_e64 s[8:9], v2, v0
	s_branch .LBB0_684

.LBB0_728:
	s_mov_b32 s15, 0
	v_mbcnt_lo_u32_b32 v152, -1, 0
	v_mbcnt_hi_u32_b32 v152, -1, v152
	s_lshl_b32 s15, s53, 8
	v_readlane_b32 s56, v249, 18
	v_lshrrev_b32_e32 v130, 1, v152
	v_and_or_b32 v130, v130, 24, s15
	s_lshr_b32 s15, s22, 5
	s_mul_i32 s24, s15, 0x1800
	s_ashr_i32 s25, s24, 31
	s_lshl_b64 s[24:25], s[24:25], 2
	s_add_u32 s26, s41, s24
	s_addc_u32 s27, s42, s25
	s_add_u32 s28, s96, s24
	v_or_b32_e32 v130, s45, v130
	s_addc_u32 s29, s97, s25
	v_ashrrev_i32_e32 v131, 31, v130
	s_add_u32 s24, s28, 0x1000
	v_lshlrev_b64 v[132:133], 2, v[130:131]
	s_addc_u32 s25, s29, 0
	v_lshl_add_u64 v[150:151], s[26:27], 0, v[132:133]
	v_lshl_add_u64 v[146:147], s[24:25], 0, v[132:133]
	s_lshl_b32 s15, s22, 8
	global_load_dwordx4 v[138:141], v[150:151], off offset:16
	global_load_dwordx4 v[134:137], v[150:151], off
	global_load_dwordx4 v[142:145], v[146:147], off
	s_nop 0
	global_load_dwordx4 v[146:149], v[146:147], off offset:16
	s_add_i32 s15, s15, s44
	v_and_or_b32 v152, v152, 15, s15
	v_ashrrev_i32_e32 v153, 31, v152
	v_lshlrev_b64 v[162:163], 10, v[152:153]
	v_lshl_add_u64 v[162:163], v[162:163], 0, v[130:131]
	v_lshl_add_u64 v[200:201], s[28:29], 0, v[132:133]
	v_lshlrev_b64 v[212:213], 1, v[162:163]
	v_readlane_b32 s62, v249, 24
	v_readlane_b32 s63, v249, 25
	global_load_dwordx4 v[154:157], v[200:201], off offset:16
	global_load_dwordx4 v[158:161], v[200:201], off
	v_lshl_add_u64 v[214:215], s[90:91], 0, v[212:213]
	v_mov_b32_e32 v246, v212
	v_lshl_add_u64 v[132:133], s[62:63], 0, v[132:133]
	global_load_dwordx4 v[162:165], v[214:215], off
	global_load_dwordx4 v[230:233], v246, s[90:91] offset:256
	v_add_u32_e32 v247, 0x8000, v246
	global_load_dwordx4 v[234:237], v247, s[90:91]
	v_add_u32_e32 v247, 0x8000, v246
	global_load_dwordx4 v[238:241], v247, s[90:91] offset:256
	v_add_u32_e32 v247, 0x10000, v246
	global_load_dwordx4 v[242:245], v247, s[90:91]
	v_add_u32_e32 v247, 0x10000, v246
	global_load_dwordx4 v[226:229], v247, s[90:91] offset:256
	global_load_dwordx4 v[166:169], v[132:133], off
	global_load_dwordx4 v[170:173], v[132:133], off offset:16
	v_or_b32_e32 v204, 0x80, v130
	v_ashrrev_i32_e32 v205, 31, v204
	global_load_dwordx4 v[180:183], v[132:133], off offset:528
	global_load_dwordx4 v[184:187], v[132:133], off offset:512
	global_load_dwordx4 v[188:191], v[150:151], off offset:528
	global_load_dwordx4 v[192:195], v[150:151], off offset:512
	global_load_dwordx4 v[196:199], v[200:201], off offset:528
	s_nop 0
	global_load_dwordx4 v[200:203], v[200:201], off offset:512
	v_lshl_add_u64 v[132:133], v[204:205], 2, s[24:25]
	global_load_dwordx4 v[204:207], v[132:133], off offset:16
	global_load_dwordx4 v[208:211], v[132:133], off
	s_and_b64 vcc, exec, s[0:1]
	s_mov_b64 s[0:1], -1
	v_readlane_b32 s57, v249, 19
	v_readlane_b32 s58, v249, 20
	v_readlane_b32 s59, v249, 21
	v_readlane_b32 s60, v249, 22
	v_readlane_b32 s61, v249, 23
	v_readlane_b32 s64, v249, 26
	v_readlane_b32 s65, v249, 27
	v_readlane_b32 s66, v249, 28
	v_readlane_b32 s67, v249, 29
	v_readlane_b32 s68, v249, 30
	v_readlane_b32 s69, v249, 31
	v_readlane_b32 s70, v249, 32
	v_readlane_b32 s71, v249, 33
	s_waitcnt vmcnt(0)
	v_pk_add_f32 v[138:139], v[138:139], 1.0 op_sel_hi:[1,0]
	v_pk_add_f32 v[132:133], v[136:137], 1.0 op_sel_hi:[1,0]
	v_pk_add_f32 v[136:137], v[134:135], 1.0 op_sel_hi:[1,0]
	v_pk_add_f32 v[134:135], v[140:141], 1.0 op_sel_hi:[1,0]
	v_add_f32_e32 v140, 1.0, v142
	v_add_f32_e32 v141, 1.0, v143
	v_add_f32_e32 v142, 1.0, v144
	v_add_f32_e32 v143, 1.0, v145
	v_add_f32_e32 v144, 1.0, v146
	v_add_f32_e32 v145, 1.0, v147
	v_add_f32_e32 v146, 1.0, v148
	v_add_f32_e32 v147, 1.0, v149
	v_rcp_f32_e32 v140, v140
	v_rcp_f32_e32 v141, v141
	v_rcp_f32_e32 v142, v142
	v_rcp_f32_e32 v143, v143
	v_rcp_f32_e32 v144, v144
	v_rcp_f32_e32 v145, v145
	v_rcp_f32_e32 v146, v146
	v_rcp_f32_e32 v147, v147
	v_pk_mul_f32 v[140:141], v[140:141], s[12:13] op_sel_hi:[1,0]
	v_pk_mul_f32 v[142:143], v[142:143], s[12:13] op_sel_hi:[1,0]
	v_pk_mul_f32 v[144:145], v[144:145], s[12:13] op_sel_hi:[1,0]
	v_pk_mul_f32 v[146:147], v[146:147], s[12:13] op_sel_hi:[1,0]
	v_pk_mul_f32 v[148:149], v[160:161], v[142:143]
	v_pk_mul_f32 v[150:151], v[158:159], v[140:141]
	v_pk_mul_f32 v[156:157], v[156:157], v[146:147]
	v_pk_mul_f32 v[158:159], v[154:155], v[144:145]
	v_lshlrev_b32_e32 v160, 16, v162
	v_and_b32_e32 v161, 0xffff0000, v162
	v_lshlrev_b32_e32 v162, 16, v163
	v_and_b32_e32 v163, 0xffff0000, v163
	v_lshlrev_b32_e32 v216, 16, v164
	v_and_b32_e32 v217, 0xffff0000, v164
	v_lshlrev_b32_e32 v164, 16, v165
	v_and_b32_e32 v165, 0xffff0000, v165
	v_pk_fma_f32 v[148:149], v[168:169], v[132:133], v[148:149] neg_lo:[0,0,1] neg_hi:[0,0,1]
	v_pk_fma_f32 v[154:155], v[166:167], v[136:137], v[150:151] neg_lo:[0,0,1] neg_hi:[0,0,1]
	v_pk_fma_f32 v[150:151], v[172:173], v[134:135], v[156:157] neg_lo:[0,0,1] neg_hi:[0,0,1]
	v_pk_fma_f32 v[156:157], v[170:171], v[138:139], v[158:159] neg_lo:[0,0,1] neg_hi:[0,0,1]
	v_pk_fma_f32 v[158:159], v[140:141], v[160:161], v[154:155]
	v_pk_fma_f32 v[160:161], v[142:143], v[162:163], v[148:149]
	v_pk_fma_f32 v[162:163], v[144:145], v[216:217], v[156:157]
	v_pk_fma_f32 v[164:165], v[146:147], v[164:165], v[150:151]
	v_pk_fma_f32 v[124:125], v[124:125], v[136:137], v[158:159]
	v_pk_fma_f32 v[126:127], v[126:127], v[132:133], v[160:161]
	v_pk_fma_f32 v[158:159], v[120:121], v[138:139], v[162:163]
	v_pk_fma_f32 v[160:161], v[122:123], v[134:135], v[164:165]
	v_cvt_pk_bf16_f32 v120, v124, v125
	v_cvt_pk_bf16_f32 v121, v126, v127
	v_cvt_pk_bf16_f32 v122, v158, v159
	v_cvt_pk_bf16_f32 v123, v160, v161
	v_lshl_add_u64 v[216:217], s[76:77], 0, v[212:213]
	global_store_dwordx4 v[216:217], v[120:123], off
	v_add_f32_e32 v153, 1.0, v208
	v_add_f32_e32 v159, 1.0, v209
	v_add_f32_e32 v160, 1.0, v210
	v_add_f32_e32 v161, 1.0, v211
	v_add_f32_e32 v162, 1.0, v204
	v_add_f32_e32 v163, 1.0, v205
	v_add_f32_e32 v164, 1.0, v206
	v_add_f32_e32 v165, 1.0, v207
	v_rcp_f32_e32 v158, v153
	v_rcp_f32_e32 v159, v159
	v_rcp_f32_e32 v160, v160
	v_rcp_f32_e32 v161, v161
	v_rcp_f32_e32 v162, v162
	v_rcp_f32_e32 v163, v163
	v_rcp_f32_e32 v168, v164
	v_rcp_f32_e32 v169, v165
	v_or_b32_e32 v120, 16, v152
	v_ashrrev_i32_e32 v121, 31, v120
	v_lshlrev_b64 v[120:121], 10, v[120:121]
	v_lshl_add_u64 v[120:121], v[120:121], 0, v[130:131]
	v_pk_mul_f32 v[166:167], v[158:159], s[12:13] op_sel_hi:[1,0]
	v_pk_mul_f32 v[164:165], v[160:161], s[12:13] op_sel_hi:[1,0]
	v_pk_mul_f32 v[160:161], v[162:163], s[12:13] op_sel_hi:[1,0]
	v_pk_mul_f32 v[158:159], v[168:169], s[12:13] op_sel_hi:[1,0]
	v_lshlrev_b64 v[218:219], 1, v[120:121]
	v_pk_add_f32 v[122:123], v[194:195], 1.0 op_sel_hi:[1,0]
	v_pk_add_f32 v[124:125], v[192:193], 1.0 op_sel_hi:[1,0]
	v_pk_add_f32 v[120:121], v[190:191], 1.0 op_sel_hi:[1,0]
	v_pk_add_f32 v[126:127], v[188:189], 1.0 op_sel_hi:[1,0]
	v_pk_mul_f32 v[162:163], v[202:203], v[164:165]
	v_pk_mul_f32 v[168:169], v[200:201], v[166:167]
	v_pk_mul_f32 v[188:189], v[198:199], v[158:159]
	v_pk_mul_f32 v[190:191], v[196:197], v[160:161]
	v_pk_fma_f32 v[170:171], v[186:187], v[122:123], v[162:163] neg_lo:[0,0,1] neg_hi:[0,0,1]
	v_pk_fma_f32 v[172:173], v[184:185], v[124:125], v[168:169] neg_lo:[0,0,1] neg_hi:[0,0,1]
	v_pk_fma_f32 v[162:163], v[182:183], v[120:121], v[188:189] neg_lo:[0,0,1] neg_hi:[0,0,1]
	v_pk_fma_f32 v[168:169], v[180:181], v[126:127], v[190:191] neg_lo:[0,0,1] neg_hi:[0,0,1]
	v_lshl_add_u64 v[220:221], s[90:91], 0, v[218:219]
	s_waitcnt vmcnt(9)
	v_mov_b32_e32 v212, v230
	v_mov_b32_e32 v213, v231
	v_mov_b32_e32 v214, v232
	v_mov_b32_e32 v215, v233
	v_add_u32_e32 v247, 0x18000, v246
	global_load_dwordx4 v[230:233], v247, s[90:91]
	v_lshlrev_b32_e32 v180, 16, v212
	v_and_b32_e32 v181, 0xffff0000, v212
	v_lshlrev_b32_e32 v182, 16, v213
	v_and_b32_e32 v183, 0xffff0000, v213
	v_lshlrev_b32_e32 v184, 16, v214
	v_and_b32_e32 v185, 0xffff0000, v214
	v_lshlrev_b32_e32 v186, 16, v215
	v_and_b32_e32 v187, 0xffff0000, v215
	v_pk_fma_f32 v[180:181], v[166:167], v[180:181], v[172:173]
	v_pk_fma_f32 v[182:183], v[164:165], v[182:183], v[170:171]
	v_pk_fma_f32 v[184:185], v[160:161], v[184:185], v[168:169]
	v_pk_fma_f32 v[186:187], v[158:159], v[186:187], v[162:163]
	v_pk_fma_f32 v[116:117], v[116:117], v[124:125], v[180:181]
	v_pk_fma_f32 v[118:119], v[118:119], v[122:123], v[182:183]
	v_pk_fma_f32 v[180:181], v[112:113], v[126:127], v[184:185]
	v_pk_fma_f32 v[182:183], v[114:115], v[120:121], v[186:187]
	v_cvt_pk_bf16_f32 v112, v116, v117
	v_cvt_pk_bf16_f32 v113, v118, v119
	v_cvt_pk_bf16_f32 v114, v180, v181
	v_cvt_pk_bf16_f32 v115, v182, v183
	global_store_dwordx4 v[216:217], v[112:115], off offset:256
	v_lshl_add_u64 v[116:117], s[76:77], 0, v[218:219]
	s_waitcnt vmcnt(9)
	v_mov_b32_e32 v112, v234
	v_mov_b32_e32 v113, v235
	v_mov_b32_e32 v114, v236
	v_mov_b32_e32 v115, v237
	v_add_u32_e32 v247, 0x18000, v246
	global_load_dwordx4 v[234:237], v247, s[90:91] offset:256
	v_lshlrev_b32_e32 v118, 16, v112
	v_and_b32_e32 v119, 0xffff0000, v112
	v_lshlrev_b32_e32 v112, 16, v113
	v_and_b32_e32 v113, 0xffff0000, v113
	v_lshlrev_b32_e32 v180, 16, v114
	v_and_b32_e32 v181, 0xffff0000, v114
	v_lshlrev_b32_e32 v114, 16, v115
	v_and_b32_e32 v115, 0xffff0000, v115
	v_pk_fma_f32 v[118:119], v[140:141], v[118:119], v[154:155]
	v_pk_fma_f32 v[112:113], v[142:143], v[112:113], v[148:149]
	v_pk_fma_f32 v[180:181], v[144:145], v[180:181], v[156:157]
	v_pk_fma_f32 v[114:115], v[146:147], v[114:115], v[150:151]
	v_pk_fma_f32 v[108:109], v[108:109], v[136:137], v[118:119]
	v_pk_fma_f32 v[110:111], v[110:111], v[132:133], v[112:113]
	v_pk_fma_f32 v[112:113], v[104:105], v[138:139], v[180:181]
	v_pk_fma_f32 v[114:115], v[106:107], v[134:135], v[114:115]
	v_cvt_pk_bf16_f32 v104, v108, v109
	v_cvt_pk_bf16_f32 v105, v110, v111
	v_cvt_pk_bf16_f32 v106, v112, v113
	v_cvt_pk_bf16_f32 v107, v114, v115
	global_store_dwordx4 v[116:117], v[104:107], off
	v_or_b32_e32 v108, 32, v152
	v_ashrrev_i32_e32 v109, 31, v108
	v_lshlrev_b64 v[108:109], 10, v[108:109]
	v_lshl_add_u64 v[108:109], v[108:109], 0, v[130:131]
	v_lshlrev_b64 v[108:109], 1, v[108:109]
	v_lshl_add_u64 v[110:111], s[90:91], 0, v[108:109]
	s_waitcnt vmcnt(9)
	v_mov_b32_e32 v104, v238
	v_mov_b32_e32 v105, v239
	v_mov_b32_e32 v106, v240
	v_mov_b32_e32 v107, v241
	v_add_u32_e32 v247, 0x40000, v246
	global_load_dwordx4 v[238:241], v247, s[90:91]
	v_lshlrev_b32_e32 v112, 16, v104
	v_and_b32_e32 v113, 0xffff0000, v104
	v_lshlrev_b32_e32 v104, 16, v105
	v_and_b32_e32 v105, 0xffff0000, v105
	v_lshlrev_b32_e32 v114, 16, v106
	v_and_b32_e32 v115, 0xffff0000, v106
	v_lshlrev_b32_e32 v106, 16, v107
	v_and_b32_e32 v107, 0xffff0000, v107
	v_pk_fma_f32 v[112:113], v[166:167], v[112:113], v[172:173]
	v_pk_fma_f32 v[104:105], v[164:165], v[104:105], v[170:171]
	v_pk_fma_f32 v[114:115], v[160:161], v[114:115], v[168:169]
	v_pk_fma_f32 v[106:107], v[158:159], v[106:107], v[162:163]
	v_pk_fma_f32 v[100:101], v[100:101], v[124:125], v[112:113]
	v_pk_fma_f32 v[102:103], v[102:103], v[122:123], v[104:105]
	v_pk_fma_f32 v[104:105], v[96:97], v[126:127], v[114:115]
	v_pk_fma_f32 v[106:107], v[98:99], v[120:121], v[106:107]
	v_cvt_pk_bf16_f32 v96, v100, v101
	v_cvt_pk_bf16_f32 v97, v102, v103
	v_cvt_pk_bf16_f32 v98, v104, v105
	v_cvt_pk_bf16_f32 v99, v106, v107
	global_store_dwordx4 v[116:117], v[96:99], off offset:256
	v_lshl_add_u64 v[100:101], s[76:77], 0, v[108:109]
	s_waitcnt vmcnt(9)
	v_mov_b32_e32 v96, v242
	v_mov_b32_e32 v97, v243
	v_mov_b32_e32 v98, v244
	v_mov_b32_e32 v99, v245
	v_add_u32_e32 v247, 0x40000, v246
	global_load_dwordx4 v[242:245], v247, s[90:91] offset:256
	v_lshlrev_b32_e32 v102, 16, v96
	v_and_b32_e32 v103, 0xffff0000, v96
	v_lshlrev_b32_e32 v96, 16, v97
	v_and_b32_e32 v97, 0xffff0000, v97
	v_lshlrev_b32_e32 v104, 16, v98
	v_and_b32_e32 v105, 0xffff0000, v98
	v_lshlrev_b32_e32 v98, 16, v99
	v_and_b32_e32 v99, 0xffff0000, v99
	v_pk_fma_f32 v[102:103], v[140:141], v[102:103], v[154:155]
	v_pk_fma_f32 v[96:97], v[142:143], v[96:97], v[148:149]
	v_pk_fma_f32 v[104:105], v[144:145], v[104:105], v[156:157]
	v_pk_fma_f32 v[98:99], v[146:147], v[98:99], v[150:151]
	v_pk_fma_f32 v[92:93], v[92:93], v[136:137], v[102:103]
	v_pk_fma_f32 v[94:95], v[94:95], v[132:133], v[96:97]
	v_pk_fma_f32 v[96:97], v[88:89], v[138:139], v[104:105]
	v_pk_fma_f32 v[98:99], v[90:91], v[134:135], v[98:99]
	v_cvt_pk_bf16_f32 v88, v92, v93
	v_cvt_pk_bf16_f32 v89, v94, v95
	v_cvt_pk_bf16_f32 v90, v96, v97
	v_cvt_pk_bf16_f32 v91, v98, v99
	global_store_dwordx4 v[100:101], v[88:91], off
	v_or_b32_e32 v92, 48, v152
	v_ashrrev_i32_e32 v93, 31, v92
	v_lshlrev_b64 v[92:93], 10, v[92:93]
	v_lshl_add_u64 v[92:93], v[92:93], 0, v[130:131]
	v_lshlrev_b64 v[92:93], 1, v[92:93]
	v_lshl_add_u64 v[94:95], s[90:91], 0, v[92:93]
	s_waitcnt vmcnt(9)
	v_mov_b32_e32 v88, v226
	v_mov_b32_e32 v89, v227
	v_mov_b32_e32 v90, v228
	v_mov_b32_e32 v91, v229
	v_add_u32_e32 v247, 0x48000, v246
	global_load_dwordx4 v[226:229], v247, s[90:91]
	v_lshlrev_b32_e32 v96, 16, v88
	v_and_b32_e32 v97, 0xffff0000, v88
	v_lshlrev_b32_e32 v88, 16, v89
	v_and_b32_e32 v89, 0xffff0000, v89
	v_lshlrev_b32_e32 v98, 16, v90
	v_and_b32_e32 v99, 0xffff0000, v90
	v_lshlrev_b32_e32 v90, 16, v91
	v_and_b32_e32 v91, 0xffff0000, v91
	v_pk_fma_f32 v[96:97], v[166:167], v[96:97], v[172:173]
	v_pk_fma_f32 v[88:89], v[164:165], v[88:89], v[170:171]
	v_pk_fma_f32 v[98:99], v[160:161], v[98:99], v[168:169]
	v_pk_fma_f32 v[90:91], v[158:159], v[90:91], v[162:163]
	v_pk_fma_f32 v[84:85], v[84:85], v[124:125], v[96:97]
	v_pk_fma_f32 v[86:87], v[86:87], v[122:123], v[88:89]
	v_pk_fma_f32 v[88:89], v[80:81], v[126:127], v[98:99]
	v_pk_fma_f32 v[90:91], v[82:83], v[120:121], v[90:91]
	v_cvt_pk_bf16_f32 v80, v84, v85
	v_cvt_pk_bf16_f32 v81, v86, v87
	v_cvt_pk_bf16_f32 v82, v88, v89
	v_cvt_pk_bf16_f32 v83, v90, v91
	global_store_dwordx4 v[100:101], v[80:83], off offset:256
	v_lshl_add_u64 v[84:85], s[76:77], 0, v[92:93]
	s_waitcnt vmcnt(9)
	v_mov_b32_e32 v80, v230
	v_mov_b32_e32 v81, v231
	v_mov_b32_e32 v82, v232
	v_mov_b32_e32 v83, v233
	v_add_u32_e32 v247, 0x48000, v246
	global_load_dwordx4 v[230:233], v247, s[90:91] offset:256
	v_lshlrev_b32_e32 v86, 16, v80
	v_and_b32_e32 v87, 0xffff0000, v80
	v_lshlrev_b32_e32 v80, 16, v81
	v_and_b32_e32 v81, 0xffff0000, v81
	v_lshlrev_b32_e32 v88, 16, v82
	v_and_b32_e32 v89, 0xffff0000, v82
	v_lshlrev_b32_e32 v82, 16, v83
	v_and_b32_e32 v83, 0xffff0000, v83
	v_pk_fma_f32 v[86:87], v[140:141], v[86:87], v[154:155]
	v_pk_fma_f32 v[80:81], v[142:143], v[80:81], v[148:149]
	v_pk_fma_f32 v[88:89], v[144:145], v[88:89], v[156:157]
	v_pk_fma_f32 v[82:83], v[146:147], v[82:83], v[150:151]
	v_pk_fma_f32 v[76:77], v[76:77], v[136:137], v[86:87]
	v_pk_fma_f32 v[78:79], v[78:79], v[132:133], v[80:81]
	v_pk_fma_f32 v[80:81], v[72:73], v[138:139], v[88:89]
	v_pk_fma_f32 v[82:83], v[74:75], v[134:135], v[82:83]
	v_cvt_pk_bf16_f32 v72, v76, v77
	v_cvt_pk_bf16_f32 v73, v78, v79
	v_cvt_pk_bf16_f32 v74, v80, v81
	v_cvt_pk_bf16_f32 v75, v82, v83
	global_store_dwordx4 v[84:85], v[72:75], off
	v_add_u32_e32 v76, 0x80, v152
	v_ashrrev_i32_e32 v77, 31, v76
	v_lshlrev_b64 v[76:77], 10, v[76:77]
	v_lshl_add_u64 v[76:77], v[76:77], 0, v[130:131]
	v_lshlrev_b64 v[76:77], 1, v[76:77]
	v_lshl_add_u64 v[78:79], s[90:91], 0, v[76:77]
	s_waitcnt vmcnt(9)
	v_mov_b32_e32 v72, v234
	v_mov_b32_e32 v73, v235
	v_mov_b32_e32 v74, v236
	v_mov_b32_e32 v75, v237
	v_add_u32_e32 v247, 0x50000, v246
	global_load_dwordx4 v[234:237], v247, s[90:91]
	v_lshlrev_b32_e32 v80, 16, v72
	v_and_b32_e32 v81, 0xffff0000, v72
	v_lshlrev_b32_e32 v72, 16, v73
	v_and_b32_e32 v73, 0xffff0000, v73
	v_lshlrev_b32_e32 v82, 16, v74
	v_and_b32_e32 v83, 0xffff0000, v74
	v_lshlrev_b32_e32 v74, 16, v75
	v_and_b32_e32 v75, 0xffff0000, v75
	v_pk_fma_f32 v[80:81], v[166:167], v[80:81], v[172:173]
	v_pk_fma_f32 v[72:73], v[164:165], v[72:73], v[170:171]
	v_pk_fma_f32 v[82:83], v[160:161], v[82:83], v[168:169]
	v_pk_fma_f32 v[74:75], v[158:159], v[74:75], v[162:163]
	v_pk_fma_f32 v[68:69], v[68:69], v[124:125], v[80:81]
	v_pk_fma_f32 v[70:71], v[70:71], v[122:123], v[72:73]
	v_pk_fma_f32 v[72:73], v[64:65], v[126:127], v[82:83]
	v_pk_fma_f32 v[74:75], v[66:67], v[120:121], v[74:75]
	v_cvt_pk_bf16_f32 v64, v68, v69
	v_cvt_pk_bf16_f32 v65, v70, v71
	v_cvt_pk_bf16_f32 v66, v72, v73
	v_cvt_pk_bf16_f32 v67, v74, v75
	global_store_dwordx4 v[84:85], v[64:67], off offset:256
	v_lshl_add_u64 v[68:69], s[76:77], 0, v[76:77]
	s_waitcnt vmcnt(9)
	v_mov_b32_e32 v64, v238
	v_mov_b32_e32 v65, v239
	v_mov_b32_e32 v66, v240
	v_mov_b32_e32 v67, v241
	v_add_u32_e32 v247, 0x50000, v246
	global_load_dwordx4 v[238:241], v247, s[90:91] offset:256
	v_lshlrev_b32_e32 v70, 16, v64
	v_and_b32_e32 v71, 0xffff0000, v64
	v_lshlrev_b32_e32 v64, 16, v65
	v_and_b32_e32 v65, 0xffff0000, v65
	v_lshlrev_b32_e32 v72, 16, v66
	v_and_b32_e32 v73, 0xffff0000, v66
	v_lshlrev_b32_e32 v66, 16, v67
	v_and_b32_e32 v67, 0xffff0000, v67
	v_pk_fma_f32 v[70:71], v[140:141], v[70:71], v[154:155]
	v_pk_fma_f32 v[64:65], v[142:143], v[64:65], v[148:149]
	v_pk_fma_f32 v[72:73], v[144:145], v[72:73], v[156:157]
	v_pk_fma_f32 v[66:67], v[146:147], v[66:67], v[150:151]
	v_pk_fma_f32 v[60:61], v[60:61], v[136:137], v[70:71]
	v_pk_fma_f32 v[62:63], v[62:63], v[132:133], v[64:65]
	v_pk_fma_f32 v[64:65], v[56:57], v[138:139], v[72:73]
	v_pk_fma_f32 v[66:67], v[58:59], v[134:135], v[66:67]
	v_cvt_pk_bf16_f32 v56, v60, v61
	v_cvt_pk_bf16_f32 v57, v62, v63
	v_cvt_pk_bf16_f32 v58, v64, v65
	v_cvt_pk_bf16_f32 v59, v66, v67
	global_store_dwordx4 v[68:69], v[56:59], off
	v_add_u32_e32 v60, 0x90, v152
	v_ashrrev_i32_e32 v61, 31, v60
	v_lshlrev_b64 v[60:61], 10, v[60:61]
	v_lshl_add_u64 v[60:61], v[60:61], 0, v[130:131]
	v_lshlrev_b64 v[60:61], 1, v[60:61]
	v_lshl_add_u64 v[62:63], s[90:91], 0, v[60:61]
	s_waitcnt vmcnt(9)
	v_mov_b32_e32 v56, v242
	v_mov_b32_e32 v57, v243
	v_mov_b32_e32 v58, v244
	v_mov_b32_e32 v59, v245
	v_add_u32_e32 v247, 0x58000, v246
	global_load_dwordx4 v[242:245], v247, s[90:91]
	v_lshlrev_b32_e32 v64, 16, v56
	v_and_b32_e32 v65, 0xffff0000, v56
	v_lshlrev_b32_e32 v56, 16, v57
	v_and_b32_e32 v57, 0xffff0000, v57
	v_lshlrev_b32_e32 v66, 16, v58
	v_and_b32_e32 v67, 0xffff0000, v58
	v_lshlrev_b32_e32 v58, 16, v59
	v_and_b32_e32 v59, 0xffff0000, v59
	v_pk_fma_f32 v[64:65], v[166:167], v[64:65], v[172:173]
	v_pk_fma_f32 v[56:57], v[164:165], v[56:57], v[170:171]
	v_pk_fma_f32 v[66:67], v[160:161], v[66:67], v[168:169]
	v_pk_fma_f32 v[58:59], v[158:159], v[58:59], v[162:163]
	v_pk_fma_f32 v[52:53], v[52:53], v[124:125], v[64:65]
	v_pk_fma_f32 v[54:55], v[54:55], v[122:123], v[56:57]
	v_pk_fma_f32 v[56:57], v[48:49], v[126:127], v[66:67]
	v_pk_fma_f32 v[58:59], v[50:51], v[120:121], v[58:59]
	v_cvt_pk_bf16_f32 v48, v52, v53
	v_cvt_pk_bf16_f32 v49, v54, v55
	v_cvt_pk_bf16_f32 v50, v56, v57
	v_cvt_pk_bf16_f32 v51, v58, v59
	global_store_dwordx4 v[68:69], v[48:51], off offset:256
	v_lshl_add_u64 v[52:53], s[76:77], 0, v[60:61]
	s_waitcnt vmcnt(9)
	v_mov_b32_e32 v48, v226
	v_mov_b32_e32 v49, v227
	v_mov_b32_e32 v50, v228
	v_mov_b32_e32 v51, v229
	v_add_u32_e32 v247, 0x58000, v246
	global_load_dwordx4 v[226:229], v247, s[90:91] offset:256
	v_lshlrev_b32_e32 v54, 16, v48
	v_and_b32_e32 v55, 0xffff0000, v48
	v_lshlrev_b32_e32 v48, 16, v49
	v_and_b32_e32 v49, 0xffff0000, v49
	v_lshlrev_b32_e32 v56, 16, v50
	v_and_b32_e32 v57, 0xffff0000, v50
	v_lshlrev_b32_e32 v50, 16, v51
	v_and_b32_e32 v51, 0xffff0000, v51
	v_pk_fma_f32 v[54:55], v[140:141], v[54:55], v[154:155]
	v_pk_fma_f32 v[48:49], v[142:143], v[48:49], v[148:149]
	v_pk_fma_f32 v[56:57], v[144:145], v[56:57], v[156:157]
	v_pk_fma_f32 v[50:51], v[146:147], v[50:51], v[150:151]
	v_pk_fma_f32 v[44:45], v[44:45], v[136:137], v[54:55]
	v_pk_fma_f32 v[46:47], v[46:47], v[132:133], v[48:49]
	v_pk_fma_f32 v[48:49], v[40:41], v[138:139], v[56:57]
	v_pk_fma_f32 v[50:51], v[42:43], v[134:135], v[50:51]
	v_cvt_pk_bf16_f32 v40, v44, v45
	v_cvt_pk_bf16_f32 v41, v46, v47
	v_cvt_pk_bf16_f32 v42, v48, v49
	v_cvt_pk_bf16_f32 v43, v50, v51
	global_store_dwordx4 v[52:53], v[40:43], off
	v_add_u32_e32 v44, 0xa0, v152
	v_ashrrev_i32_e32 v45, 31, v44
	v_lshlrev_b64 v[44:45], 10, v[44:45]
	v_lshl_add_u64 v[44:45], v[44:45], 0, v[130:131]
	v_lshlrev_b64 v[44:45], 1, v[44:45]
	v_lshl_add_u64 v[46:47], s[90:91], 0, v[44:45]
	s_waitcnt vmcnt(9)
	v_mov_b32_e32 v40, v230
	v_mov_b32_e32 v41, v231
	v_mov_b32_e32 v42, v232
	v_mov_b32_e32 v43, v233
	v_lshlrev_b32_e32 v48, 16, v40
	v_and_b32_e32 v49, 0xffff0000, v40
	v_lshlrev_b32_e32 v40, 16, v41
	v_and_b32_e32 v41, 0xffff0000, v41
	v_lshlrev_b32_e32 v50, 16, v42
	v_and_b32_e32 v51, 0xffff0000, v42
	v_lshlrev_b32_e32 v42, 16, v43
	v_and_b32_e32 v43, 0xffff0000, v43
	v_pk_fma_f32 v[48:49], v[166:167], v[48:49], v[172:173]
	v_pk_fma_f32 v[40:41], v[164:165], v[40:41], v[170:171]
	v_pk_fma_f32 v[50:51], v[160:161], v[50:51], v[168:169]
	v_pk_fma_f32 v[42:43], v[158:159], v[42:43], v[162:163]
	v_pk_fma_f32 v[36:37], v[36:37], v[124:125], v[48:49]
	v_pk_fma_f32 v[38:39], v[38:39], v[122:123], v[40:41]
	v_pk_fma_f32 v[40:41], v[32:33], v[126:127], v[50:51]
	v_pk_fma_f32 v[42:43], v[34:35], v[120:121], v[42:43]
	v_cvt_pk_bf16_f32 v32, v36, v37
	v_cvt_pk_bf16_f32 v33, v38, v39
	v_cvt_pk_bf16_f32 v34, v40, v41
	v_cvt_pk_bf16_f32 v35, v42, v43
	global_store_dwordx4 v[52:53], v[32:35], off offset:256
	v_lshl_add_u64 v[36:37], s[76:77], 0, v[44:45]
	s_waitcnt vmcnt(8)
	v_mov_b32_e32 v32, v234
	v_mov_b32_e32 v33, v235
	v_mov_b32_e32 v34, v236
	v_mov_b32_e32 v35, v237
	v_lshlrev_b32_e32 v38, 16, v32
	v_and_b32_e32 v39, 0xffff0000, v32
	v_lshlrev_b32_e32 v32, 16, v33
	v_and_b32_e32 v33, 0xffff0000, v33
	v_lshlrev_b32_e32 v40, 16, v34
	v_and_b32_e32 v41, 0xffff0000, v34
	v_lshlrev_b32_e32 v34, 16, v35
	v_and_b32_e32 v35, 0xffff0000, v35
	v_pk_fma_f32 v[38:39], v[140:141], v[38:39], v[154:155]
	v_pk_fma_f32 v[32:33], v[142:143], v[32:33], v[148:149]
	v_pk_fma_f32 v[40:41], v[144:145], v[40:41], v[156:157]
	v_pk_fma_f32 v[34:35], v[146:147], v[34:35], v[150:151]
	v_pk_fma_f32 v[28:29], v[28:29], v[136:137], v[38:39]
	v_pk_fma_f32 v[30:31], v[30:31], v[132:133], v[32:33]
	v_pk_fma_f32 v[32:33], v[24:25], v[138:139], v[40:41]
	v_pk_fma_f32 v[34:35], v[26:27], v[134:135], v[34:35]
	v_cvt_pk_bf16_f32 v24, v28, v29
	v_cvt_pk_bf16_f32 v25, v30, v31
	v_cvt_pk_bf16_f32 v26, v32, v33
	v_cvt_pk_bf16_f32 v27, v34, v35
	global_store_dwordx4 v[36:37], v[24:27], off
	v_add_u32_e32 v28, 0xb0, v152
	v_ashrrev_i32_e32 v29, 31, v28
	v_lshlrev_b64 v[28:29], 10, v[28:29]
	v_lshl_add_u64 v[28:29], v[28:29], 0, v[130:131]
	v_lshlrev_b64 v[28:29], 1, v[28:29]
	v_lshl_add_u64 v[30:31], s[90:91], 0, v[28:29]
	s_waitcnt vmcnt(7)
	v_mov_b32_e32 v24, v238
	v_mov_b32_e32 v25, v239
	v_mov_b32_e32 v26, v240
	v_mov_b32_e32 v27, v241
	v_lshlrev_b32_e32 v32, 16, v24
	v_and_b32_e32 v33, 0xffff0000, v24
	v_lshlrev_b32_e32 v24, 16, v25
	v_and_b32_e32 v25, 0xffff0000, v25
	v_lshlrev_b32_e32 v34, 16, v26
	v_and_b32_e32 v35, 0xffff0000, v26
	v_lshlrev_b32_e32 v26, 16, v27
	v_and_b32_e32 v27, 0xffff0000, v27
	v_pk_fma_f32 v[32:33], v[166:167], v[32:33], v[172:173]
	v_pk_fma_f32 v[24:25], v[164:165], v[24:25], v[170:171]
	v_pk_fma_f32 v[34:35], v[160:161], v[34:35], v[168:169]
	v_pk_fma_f32 v[26:27], v[158:159], v[26:27], v[162:163]
	v_pk_fma_f32 v[20:21], v[20:21], v[124:125], v[32:33]
	v_pk_fma_f32 v[22:23], v[22:23], v[122:123], v[24:25]
	v_pk_fma_f32 v[24:25], v[16:17], v[126:127], v[34:35]
	v_pk_fma_f32 v[26:27], v[18:19], v[120:121], v[26:27]
	v_cvt_pk_bf16_f32 v16, v20, v21
	v_cvt_pk_bf16_f32 v17, v22, v23
	v_cvt_pk_bf16_f32 v18, v24, v25
	v_cvt_pk_bf16_f32 v19, v26, v27
	global_store_dwordx4 v[36:37], v[16:19], off offset:256
	v_lshl_add_u64 v[20:21], s[76:77], 0, v[28:29]
	s_waitcnt vmcnt(6)
	v_mov_b32_e32 v16, v242
	v_mov_b32_e32 v17, v243
	v_mov_b32_e32 v18, v244
	v_mov_b32_e32 v19, v245
	v_lshlrev_b32_e32 v22, 16, v16
	v_and_b32_e32 v23, 0xffff0000, v16
	v_lshlrev_b32_e32 v16, 16, v17
	v_and_b32_e32 v17, 0xffff0000, v17
	v_lshlrev_b32_e32 v24, 16, v18
	v_and_b32_e32 v25, 0xffff0000, v18
	v_lshlrev_b32_e32 v18, 16, v19
	v_and_b32_e32 v19, 0xffff0000, v19
	v_pk_fma_f32 v[22:23], v[140:141], v[22:23], v[154:155]
	v_pk_fma_f32 v[16:17], v[142:143], v[16:17], v[148:149]
	v_pk_fma_f32 v[24:25], v[144:145], v[24:25], v[156:157]
	v_pk_fma_f32 v[18:19], v[146:147], v[18:19], v[150:151]
	v_pk_fma_f32 v[12:13], v[12:13], v[136:137], v[22:23]
	v_pk_fma_f32 v[14:15], v[14:15], v[132:133], v[16:17]
	v_pk_fma_f32 v[16:17], v[8:9], v[138:139], v[24:25]
	v_pk_fma_f32 v[18:19], v[10:11], v[134:135], v[18:19]
	v_cvt_pk_bf16_f32 v8, v12, v13
	v_cvt_pk_bf16_f32 v9, v14, v15
	v_cvt_pk_bf16_f32 v10, v16, v17
	v_cvt_pk_bf16_f32 v11, v18, v19
	global_store_dwordx4 v[20:21], v[8:11], off
	s_waitcnt vmcnt(5)
	v_mov_b32_e32 v8, v226
	v_mov_b32_e32 v9, v227
	v_mov_b32_e32 v10, v228
	v_mov_b32_e32 v11, v229
	v_lshlrev_b32_e32 v12, 16, v8
	v_and_b32_e32 v13, 0xffff0000, v8
	v_lshlrev_b32_e32 v8, 16, v9
	v_and_b32_e32 v9, 0xffff0000, v9
	v_lshlrev_b32_e32 v14, 16, v10
	v_and_b32_e32 v15, 0xffff0000, v10
	v_lshlrev_b32_e32 v10, 16, v11
	v_and_b32_e32 v11, 0xffff0000, v11
	v_pk_fma_f32 v[12:13], v[166:167], v[12:13], v[172:173]
	v_pk_fma_f32 v[8:9], v[164:165], v[8:9], v[170:171]
	v_pk_fma_f32 v[14:15], v[160:161], v[14:15], v[168:169]
	v_pk_fma_f32 v[10:11], v[158:159], v[10:11], v[162:163]
	v_pk_fma_f32 v[4:5], v[4:5], v[124:125], v[12:13]
	v_pk_fma_f32 v[6:7], v[6:7], v[122:123], v[8:9]
	v_pk_fma_f32 v[8:9], v[0:1], v[126:127], v[14:15]
	v_pk_fma_f32 v[10:11], v[2:3], v[120:121], v[10:11]
	v_cvt_pk_bf16_f32 v0, v4, v5
	v_cvt_pk_bf16_f32 v1, v6, v7
	v_cvt_pk_bf16_f32 v2, v8, v9
	v_cvt_pk_bf16_f32 v3, v10, v11
	global_store_dwordx4 v[20:21], v[0:3], off offset:256
	s_cbranch_vccnz .LBB0_717
	s_andn2_b64 vcc, exec, s[6:7]
	s_cbranch_vccnz .LBB0_716
	s_barrier
	s_branch .LBB0_716

.LBB0_1044:
	s_or_b64 exec, exec, s[12:13]
	s_getreg_b32 s0, hwreg(HW_REG_HW_ID, 0, 6)
	s_lshl_b32 s0, s0, 2
	s_and_b32 s0, s0, 0xfc
	s_add_i32 s0, s0, 0
	s_add_i32 s0, s0, 0x25c00
	v_mov_b32_e32 v0, s0
	ds_read_b32 v0, v0
	s_waitcnt lgkmcnt(0)
	v_readfirstlane_b32 s0, v0
	v_mbcnt_lo_u32_b32 v0, -1, 0
	v_mbcnt_hi_u32_b32 v0, -1, v0
	s_nop 1
	v_lshl_add_u32 v0, s0, 6, v0
	s_nop 0
	v_cmp_eq_u32_e32 vcc, 0, v0
	s_and_saveexec_b64 s[0:1], vcc
	s_cbranch_execz .LBB0_1074
	s_add_i32 s3, 0, 0x24808
	v_mov_b32_e32 v0, s3
	s_add_i32 s3, 0, 0x2480c
	v_mov_b32_e32 v1, s3
	ds_read_b32 v0, v0
	ds_read_b32 v1, v1
	s_waitcnt lgkmcnt(0)
	v_cmp_eq_u32_e32 vcc, 0, v1
	s_cbranch_vccnz .LBB0_1055
	v_mov_b32_e32 v1, 0x3000
	s_add_i32 s3, 0, 0x24804
	v_mov_b32_e32 v3, s3
	ds_read_b32 v3, v3
	global_load_dword v1, v1, s[94:95] offset:1024 sc1
	s_waitcnt lgkmcnt(0)
	v_mul_lo_u32 v0, v0, v3
	s_add_u32 s12, s94, 0x3400
	s_addc_u32 s13, s95, 0
	s_waitcnt vmcnt(0)
	v_cmp_ge_u32_e32 vcc, v1, v0
	s_cbranch_vccnz .LBB0_1060
	s_mov_b32 s3, 1
	v_mov_b32_e32 v1, 0
	s_branch .LBB0_1049

.LBB0_1051:
	global_load_dword v2, v1, s[12:13] sc1
	s_add_i32 s3, s3, 1
	s_mov_b64 s[16:17], -1
	s_waitcnt vmcnt(0)
	v_cmp_ge_u32_e64 s[14:15], v2, v0
	s_branch .LBB0_1048

.LBB0_1566:
	global_load_dword v2, v1, s[6:7] sc1
	s_add_i32 s3, s3, 1
	s_mov_b64 s[12:13], -1
	s_waitcnt vmcnt(0)
	v_cmp_ge_u32_e64 s[10:11], v2, v0
	s_branch .LBB0_1563

.LBB0_1772:
	s_mov_b32 s5, 0
	v_mbcnt_lo_u32_b32 v147, -1, 0
	v_mbcnt_hi_u32_b32 v147, -1, v147
	s_lshl_b32 s5, s4, 8
	v_readlane_b32 s80, v249, 18
	v_bfe_u32 v58, v147, 4, 2
	v_lshlrev_b32_e32 v146, 3, v58
	v_or_b32_e32 v56, s41, v146
	v_or_b32_e32 v56, s5, v56
	v_ashrrev_i32_e32 v57, 31, v56
	v_readlane_b32 s90, v249, 28
	v_readlane_b32 s91, v249, 29
	v_cmp_eq_u32_e64 s[6:7], 0, v58
	s_add_i32 s51, s5, 0xfffff800
	v_lshl_add_u64 v[60:61], v[56:57], 2, s[90:91]
	global_load_dwordx4 v[76:79], v[60:61], off
	global_load_dwordx4 v[68:71], v[60:61], off offset:16
	global_load_dwordx4 v[56:59], v[60:61], off offset:528
	s_nop 0
	global_load_dwordx4 v[60:63], v[60:61], off offset:512
	s_cmp_gt_i32 s4, 7
	v_readlane_b32 s81, v249, 19
	v_readlane_b32 s82, v249, 20
	v_readlane_b32 s83, v249, 21
	v_readlane_b32 s84, v249, 22
	v_readlane_b32 s85, v249, 23
	v_readlane_b32 s86, v249, 24
	v_readlane_b32 s87, v249, 25
	s_cselect_b64 s[70:71], -1, 0
	s_and_b64 s[72:73], s[70:71], exec
	s_mov_b32 s53, 0x16500000
	v_readlane_b32 s80, v249, 55
	s_cselect_b32 s53, s53, 0x12500000
	v_readlane_b32 s86, v249, 61
	s_cselect_b32 s5, s51, s5
	v_readlane_b32 s87, v249, 62
	s_add_u32 s72, s86, s53
	s_addc_u32 s73, s87, 0
	s_lshl_b32 s51, s68, 8
	s_or_b32 s5, s41, s5
	s_add_i32 s51, s51, s39
	v_or_b32_e32 v146, s5, v146
	v_and_or_b32 v148, v147, 15, s51
	v_ashrrev_i32_e32 v147, 31, v146
	v_ashrrev_i32_e32 v149, 31, v148
	v_lshl_add_u64 v[146:147], v[146:147], 1, s[72:73]
	v_lshlrev_b64 v[160:161], 12, v[148:149]
	v_lshl_add_u64 v[164:165], v[146:147], 0, v[160:161]
	v_mov_b64_e32 v[150:151], s[24:25]
	s_lshl_b32 s53, s4, 2
	s_sub_i32 s68, s53, 32
	s_ashr_i32 s69, s68, 31
	s_or_b64 s[68:69], s[68:69], s[14:15]
	s_cmp_lt_i32 s4, 8
	v_readlane_b32 s88, v249, 26
	v_readlane_b32 s89, v249, 27
	v_readlane_b32 s92, v249, 30
	v_readlane_b32 s93, v249, 31
	v_readlane_b32 s94, v249, 32
	v_readlane_b32 s95, v249, 33
	v_readlane_b32 s81, v249, 56
	v_readlane_b32 s82, v249, 57
	v_readlane_b32 s83, v249, 58
	v_readlane_b32 s84, v249, 59
	v_readlane_b32 s85, v249, 60
	s_waitcnt vmcnt(0)
	v_readlane_b32 s90, v249, 63
	v_readlane_b32 s91, v248, 0
	s_mov_b64 s[94:95], s[46:47]
	v_mov_b32_e32 v192, v148
	v_ashrrev_i32_e32 v193, 31, v192
	v_lshlrev_b64 v[194:195], 12, v[192:193]
	v_lshl_add_u64 v[196:197], v[146:147], 0, v[194:195]
	v_pk_add_f32 v[140:141], v[140:141], v[76:77]
	v_pk_add_f32 v[142:143], v[142:143], v[78:79]
	v_pk_add_f32 v[136:137], v[136:137], v[68:69]
	v_pk_add_f32 v[138:139], v[138:139], v[70:71]
	v_med3_f32 v160, v140, s78, v158
	v_med3_f32 v161, v141, s78, v158
	v_med3_f32 v162, v142, s78, v158
	v_med3_f32 v163, v143, s78, v158
	v_med3_f32 v164, v136, s78, v158
	v_med3_f32 v165, v137, s78, v158
	v_med3_f32 v166, v138, s78, v158
	v_med3_f32 v167, v139, s78, v158
	v_pk_mul_f32 v[168:169], v[160:161], v[160:161]
	v_pk_mul_f32 v[170:171], v[162:163], v[162:163]
	v_pk_mul_f32 v[172:173], v[164:165], v[164:165]
	v_pk_mul_f32 v[174:175], v[166:167], v[166:167]
	v_pk_fma_f32 v[168:169], v[168:169], s[20:21], -1.0 op_sel_hi:[1,0,0]
	v_pk_fma_f32 v[170:171], v[170:171], s[20:21], -1.0 op_sel_hi:[1,0,0]
	v_pk_fma_f32 v[172:173], v[172:173], s[20:21], -1.0 op_sel_hi:[1,0,0]
	v_pk_fma_f32 v[174:175], v[174:175], s[20:21], -1.0 op_sel_hi:[1,0,0]
	v_pk_fma_f32 v[176:177], v[168:169], s[22:23], v[150:151] op_sel_hi:[1,0,0] neg_lo:[1,0,0] neg_hi:[1,0,0]
	v_pk_fma_f32 v[178:179], v[170:171], s[22:23], v[150:151] op_sel_hi:[1,0,0] neg_lo:[1,0,0] neg_hi:[1,0,0]
	v_pk_fma_f32 v[180:181], v[172:173], s[22:23], v[150:151] op_sel_hi:[1,0,0] neg_lo:[1,0,0] neg_hi:[1,0,0]
	v_pk_fma_f32 v[182:183], v[174:175], s[22:23], v[150:151] op_sel_hi:[1,0,0] neg_lo:[1,0,0] neg_hi:[1,0,0]
	v_pk_fma_f32 v[176:177], v[168:169], v[176:177], s[26:27] op_sel_hi:[1,1,0]
	v_pk_fma_f32 v[178:179], v[170:171], v[178:179], s[26:27] op_sel_hi:[1,1,0]
	v_pk_fma_f32 v[180:181], v[172:173], v[180:181], s[26:27] op_sel_hi:[1,1,0]
	v_pk_fma_f32 v[182:183], v[174:175], v[182:183], s[26:27] op_sel_hi:[1,1,0]
	v_pk_fma_f32 v[176:177], v[168:169], v[176:177], s[28:29] op_sel_hi:[1,1,0]
	v_pk_fma_f32 v[178:179], v[170:171], v[178:179], s[28:29] op_sel_hi:[1,1,0]
	v_pk_fma_f32 v[180:181], v[172:173], v[180:181], s[28:29] op_sel_hi:[1,1,0]
	v_pk_fma_f32 v[182:183], v[174:175], v[182:183], s[28:29] op_sel_hi:[1,1,0]
	v_pk_fma_f32 v[176:177], v[168:169], v[176:177], s[30:31] op_sel_hi:[1,1,0]
	v_pk_fma_f32 v[178:179], v[170:171], v[178:179], s[30:31] op_sel_hi:[1,1,0]
	v_pk_fma_f32 v[180:181], v[172:173], v[180:181], s[30:31] op_sel_hi:[1,1,0]
	v_pk_fma_f32 v[182:183], v[174:175], v[182:183], s[30:31] op_sel_hi:[1,1,0]
	v_pk_fma_f32 v[176:177], v[168:169], v[176:177], s[34:35] op_sel_hi:[1,1,0]
	v_pk_fma_f32 v[178:179], v[170:171], v[178:179], s[34:35] op_sel_hi:[1,1,0]
	v_pk_fma_f32 v[180:181], v[172:173], v[180:181], s[34:35] op_sel_hi:[1,1,0]
	v_pk_fma_f32 v[182:183], v[174:175], v[182:183], s[34:35] op_sel_hi:[1,1,0]
	v_pk_fma_f32 v[176:177], v[168:169], v[176:177], s[36:37] op_sel_hi:[1,1,0]
	v_pk_fma_f32 v[178:179], v[170:171], v[178:179], s[36:37] op_sel_hi:[1,1,0]
	v_pk_fma_f32 v[180:181], v[172:173], v[180:181], s[36:37] op_sel_hi:[1,1,0]
	v_pk_fma_f32 v[182:183], v[174:175], v[182:183], s[36:37] op_sel_hi:[1,1,0]
	v_pk_fma_f32 v[176:177], v[168:169], v[176:177], s[38:39] op_sel_hi:[1,1,0]
	v_pk_fma_f32 v[178:179], v[170:171], v[178:179], s[38:39] op_sel_hi:[1,1,0]
	v_pk_fma_f32 v[180:181], v[172:173], v[180:181], s[38:39] op_sel_hi:[1,1,0]
	v_pk_fma_f32 v[182:183], v[174:175], v[182:183], s[38:39] op_sel_hi:[1,1,0]
	v_pk_fma_f32 v[176:177], v[168:169], v[176:177], s[40:41] op_sel_hi:[1,1,0]
	v_pk_fma_f32 v[178:179], v[170:171], v[178:179], s[40:41] op_sel_hi:[1,1,0]
	v_pk_fma_f32 v[180:181], v[172:173], v[180:181], s[40:41] op_sel_hi:[1,1,0]
	v_pk_fma_f32 v[182:183], v[174:175], v[182:183], s[40:41] op_sel_hi:[1,1,0]
	v_pk_fma_f32 v[176:177], v[168:169], v[176:177], s[42:43] op_sel_hi:[1,1,0]
	v_pk_fma_f32 v[178:179], v[170:171], v[178:179], s[42:43] op_sel_hi:[1,1,0]
	v_pk_fma_f32 v[180:181], v[172:173], v[180:181], s[42:43] op_sel_hi:[1,1,0]
	v_pk_fma_f32 v[182:183], v[174:175], v[182:183], s[42:43] op_sel_hi:[1,1,0]
	v_pk_fma_f32 v[176:177], v[168:169], v[176:177], s[44:45] op_sel_hi:[1,1,0]
	v_pk_fma_f32 v[178:179], v[170:171], v[178:179], s[44:45] op_sel_hi:[1,1,0]
	v_pk_fma_f32 v[180:181], v[172:173], v[180:181], s[44:45] op_sel_hi:[1,1,0]
	v_pk_fma_f32 v[182:183], v[174:175], v[182:183], s[44:45] op_sel_hi:[1,1,0]
	v_pk_fma_f32 v[168:169], v[168:169], v[176:177], s[48:49] op_sel_hi:[1,1,0]
	v_pk_fma_f32 v[170:171], v[170:171], v[178:179], s[48:49] op_sel_hi:[1,1,0]
	v_pk_fma_f32 v[172:173], v[172:173], v[180:181], s[48:49] op_sel_hi:[1,1,0]
	v_pk_fma_f32 v[174:175], v[174:175], v[182:183], s[48:49] op_sel_hi:[1,1,0]
	v_pk_fma_f32 v[160:161], v[160:161], v[168:169], 0.5 op_sel_hi:[1,1,0]
	v_pk_fma_f32 v[162:163], v[162:163], v[170:171], 0.5 op_sel_hi:[1,1,0]
	v_pk_fma_f32 v[164:165], v[164:165], v[172:173], 0.5 op_sel_hi:[1,1,0]
	v_pk_fma_f32 v[166:167], v[166:167], v[174:175], 0.5 op_sel_hi:[1,1,0]
	v_pk_mul_f32 v[140:141], v[140:141], v[160:161]
	v_pk_mul_f32 v[142:143], v[142:143], v[162:163]
	v_pk_mul_f32 v[136:137], v[136:137], v[164:165]
	v_pk_mul_f32 v[138:139], v[138:139], v[166:167]
	v_cvt_pk_bf16_f32 v184, v140, v141
	v_cvt_pk_bf16_f32 v185, v142, v143
	v_cvt_pk_bf16_f32 v186, v136, v137
	v_cvt_pk_bf16_f32 v187, v138, v139
	global_store_dwordx4 v[196:197], v[184:187], off
	v_pk_add_f32 v[132:133], v[132:133], v[60:61]
	v_pk_add_f32 v[134:135], v[134:135], v[62:63]
	v_pk_add_f32 v[128:129], v[128:129], v[56:57]
	v_pk_add_f32 v[130:131], v[130:131], v[58:59]
	v_med3_f32 v160, v132, s78, v158
	v_med3_f32 v161, v133, s78, v158
	v_med3_f32 v162, v134, s78, v158
	v_med3_f32 v163, v135, s78, v158
	v_med3_f32 v164, v128, s78, v158
	v_med3_f32 v165, v129, s78, v158
	v_med3_f32 v166, v130, s78, v158
	v_med3_f32 v167, v131, s78, v158
	v_pk_mul_f32 v[168:169], v[160:161], v[160:161]
	v_pk_mul_f32 v[170:171], v[162:163], v[162:163]
	v_pk_mul_f32 v[172:173], v[164:165], v[164:165]
	v_pk_mul_f32 v[174:175], v[166:167], v[166:167]
	v_pk_fma_f32 v[168:169], v[168:169], s[20:21], -1.0 op_sel_hi:[1,0,0]
	v_pk_fma_f32 v[170:171], v[170:171], s[20:21], -1.0 op_sel_hi:[1,0,0]
	v_pk_fma_f32 v[172:173], v[172:173], s[20:21], -1.0 op_sel_hi:[1,0,0]
	v_pk_fma_f32 v[174:175], v[174:175], s[20:21], -1.0 op_sel_hi:[1,0,0]
	v_pk_fma_f32 v[176:177], v[168:169], s[22:23], v[150:151] op_sel_hi:[1,0,0] neg_lo:[1,0,0] neg_hi:[1,0,0]
	v_pk_fma_f32 v[178:179], v[170:171], s[22:23], v[150:151] op_sel_hi:[1,0,0] neg_lo:[1,0,0] neg_hi:[1,0,0]
	v_pk_fma_f32 v[180:181], v[172:173], s[22:23], v[150:151] op_sel_hi:[1,0,0] neg_lo:[1,0,0] neg_hi:[1,0,0]
	v_pk_fma_f32 v[182:183], v[174:175], s[22:23], v[150:151] op_sel_hi:[1,0,0] neg_lo:[1,0,0] neg_hi:[1,0,0]
	v_pk_fma_f32 v[176:177], v[168:169], v[176:177], s[26:27] op_sel_hi:[1,1,0]
	v_pk_fma_f32 v[178:179], v[170:171], v[178:179], s[26:27] op_sel_hi:[1,1,0]
	v_pk_fma_f32 v[180:181], v[172:173], v[180:181], s[26:27] op_sel_hi:[1,1,0]
	v_pk_fma_f32 v[182:183], v[174:175], v[182:183], s[26:27] op_sel_hi:[1,1,0]
	v_pk_fma_f32 v[176:177], v[168:169], v[176:177], s[28:29] op_sel_hi:[1,1,0]
	v_pk_fma_f32 v[178:179], v[170:171], v[178:179], s[28:29] op_sel_hi:[1,1,0]
	v_pk_fma_f32 v[180:181], v[172:173], v[180:181], s[28:29] op_sel_hi:[1,1,0]
	v_pk_fma_f32 v[182:183], v[174:175], v[182:183], s[28:29] op_sel_hi:[1,1,0]
	v_pk_fma_f32 v[176:177], v[168:169], v[176:177], s[30:31] op_sel_hi:[1,1,0]
	v_pk_fma_f32 v[178:179], v[170:171], v[178:179], s[30:31] op_sel_hi:[1,1,0]
	v_pk_fma_f32 v[180:181], v[172:173], v[180:181], s[30:31] op_sel_hi:[1,1,0]
	v_pk_fma_f32 v[182:183], v[174:175], v[182:183], s[30:31] op_sel_hi:[1,1,0]
	v_pk_fma_f32 v[176:177], v[168:169], v[176:177], s[34:35] op_sel_hi:[1,1,0]
	v_pk_fma_f32 v[178:179], v[170:171], v[178:179], s[34:35] op_sel_hi:[1,1,0]
	v_pk_fma_f32 v[180:181], v[172:173], v[180:181], s[34:35] op_sel_hi:[1,1,0]
	v_pk_fma_f32 v[182:183], v[174:175], v[182:183], s[34:35] op_sel_hi:[1,1,0]
	v_pk_fma_f32 v[176:177], v[168:169], v[176:177], s[36:37] op_sel_hi:[1,1,0]
	v_pk_fma_f32 v[178:179], v[170:171], v[178:179], s[36:37] op_sel_hi:[1,1,0]
	v_pk_fma_f32 v[180:181], v[172:173], v[180:181], s[36:37] op_sel_hi:[1,1,0]
	v_pk_fma_f32 v[182:183], v[174:175], v[182:183], s[36:37] op_sel_hi:[1,1,0]
	v_pk_fma_f32 v[176:177], v[168:169], v[176:177], s[38:39] op_sel_hi:[1,1,0]
	v_pk_fma_f32 v[178:179], v[170:171], v[178:179], s[38:39] op_sel_hi:[1,1,0]
	v_pk_fma_f32 v[180:181], v[172:173], v[180:181], s[38:39] op_sel_hi:[1,1,0]
	v_pk_fma_f32 v[182:183], v[174:175], v[182:183], s[38:39] op_sel_hi:[1,1,0]
	v_pk_fma_f32 v[176:177], v[168:169], v[176:177], s[40:41] op_sel_hi:[1,1,0]
	v_pk_fma_f32 v[178:179], v[170:171], v[178:179], s[40:41] op_sel_hi:[1,1,0]
	v_pk_fma_f32 v[180:181], v[172:173], v[180:181], s[40:41] op_sel_hi:[1,1,0]
	v_pk_fma_f32 v[182:183], v[174:175], v[182:183], s[40:41] op_sel_hi:[1,1,0]
	v_pk_fma_f32 v[176:177], v[168:169], v[176:177], s[42:43] op_sel_hi:[1,1,0]
	v_pk_fma_f32 v[178:179], v[170:171], v[178:179], s[42:43] op_sel_hi:[1,1,0]
	v_pk_fma_f32 v[180:181], v[172:173], v[180:181], s[42:43] op_sel_hi:[1,1,0]
	v_pk_fma_f32 v[182:183], v[174:175], v[182:183], s[42:43] op_sel_hi:[1,1,0]
	v_pk_fma_f32 v[176:177], v[168:169], v[176:177], s[44:45] op_sel_hi:[1,1,0]
	v_pk_fma_f32 v[178:179], v[170:171], v[178:179], s[44:45] op_sel_hi:[1,1,0]
	v_pk_fma_f32 v[180:181], v[172:173], v[180:181], s[44:45] op_sel_hi:[1,1,0]
	v_pk_fma_f32 v[182:183], v[174:175], v[182:183], s[44:45] op_sel_hi:[1,1,0]
	v_pk_fma_f32 v[168:169], v[168:169], v[176:177], s[48:49] op_sel_hi:[1,1,0]
	v_pk_fma_f32 v[170:171], v[170:171], v[178:179], s[48:49] op_sel_hi:[1,1,0]
	v_pk_fma_f32 v[172:173], v[172:173], v[180:181], s[48:49] op_sel_hi:[1,1,0]
	v_pk_fma_f32 v[174:175], v[174:175], v[182:183], s[48:49] op_sel_hi:[1,1,0]
	v_pk_fma_f32 v[160:161], v[160:161], v[168:169], 0.5 op_sel_hi:[1,1,0]
	v_pk_fma_f32 v[162:163], v[162:163], v[170:171], 0.5 op_sel_hi:[1,1,0]
	v_pk_fma_f32 v[164:165], v[164:165], v[172:173], 0.5 op_sel_hi:[1,1,0]
	v_pk_fma_f32 v[166:167], v[166:167], v[174:175], 0.5 op_sel_hi:[1,1,0]
	v_pk_mul_f32 v[132:133], v[132:133], v[160:161]
	v_pk_mul_f32 v[134:135], v[134:135], v[162:163]
	v_pk_mul_f32 v[128:129], v[128:129], v[164:165]
	v_pk_mul_f32 v[130:131], v[130:131], v[166:167]
	v_cvt_pk_bf16_f32 v188, v132, v133
	v_cvt_pk_bf16_f32 v189, v134, v135
	v_cvt_pk_bf16_f32 v190, v128, v129
	v_cvt_pk_bf16_f32 v191, v130, v131
	global_store_dwordx4 v[196:197], v[188:191], off offset:256
	s_and_b64 vcc, exec, s[70:71]
	s_cbranch_vccz .Lg9_nostat_0
	v_pk_mul_f32 v[168:169], v[140:141], v[140:141]
	v_pk_mul_f32 v[170:171], v[142:143], v[142:143]
	v_pk_mul_f32 v[172:173], v[136:137], v[136:137]
	v_pk_mul_f32 v[174:175], v[138:139], v[138:139]
	v_pk_mul_f32 v[176:177], v[132:133], v[132:133]
	v_pk_mul_f32 v[178:179], v[134:135], v[134:135]
	v_pk_mul_f32 v[180:181], v[128:129], v[128:129]
	v_pk_mul_f32 v[182:183], v[130:131], v[130:131]
	v_add_f32_e32 v160, v140, v141
	v_add_f32_e32 v161, v142, v143
	v_add_f32_e32 v162, v136, v137
	v_add_f32_e32 v163, v138, v139
	v_add_f32_e32 v164, v132, v133
	v_add_f32_e32 v165, v134, v135
	v_add_f32_e32 v166, v128, v129
	v_add_f32_e32 v167, v130, v131
	v_add_f32_e32 v160, v160, v161
	v_add_f32_e32 v164, v164, v165
	v_add_f32_e32 v160, v160, v162
	v_add_f32_e32 v164, v164, v166
	v_add_f32_e32 v160, v160, v163
	v_add_f32_e32 v164, v164, v167
	v_add_f32_e32 v168, v168, v169
	v_add_f32_e32 v170, v170, v171
	v_add_f32_e32 v172, v172, v173
	v_add_f32_e32 v174, v174, v175
	v_add_f32_e32 v176, v176, v177
	v_add_f32_e32 v178, v178, v179
	v_add_f32_e32 v180, v180, v181
	v_add_f32_e32 v182, v182, v183
	v_add_f32_e32 v198, v160, v164
	v_add_f32_e32 v168, v168, v170
	v_add_f32_e32 v176, v176, v178
	v_mov_b32_e32 v199, v198
	v_add_f32_e32 v168, v168, v172
	v_add_f32_e32 v176, v176, v180
	s_nop 1
	v_permlane16_swap_b32 v199, v198
	s_nop 1
	v_add_f32_e32 v168, v168, v174
	v_add_f32_e32 v176, v176, v182
	v_add_f32_e32 v198, v199, v198
	v_add_f32_e32 v200, v168, v176
	v_mov_b32_e32 v202, v198
	v_mov_b32_e32 v201, v200
	s_nop 1
	v_permlane32_swap_b32 v202, v198
	s_nop 1
	s_nop 1
	v_permlane16_swap_b32 v201, v200
	s_nop 1
	v_add_f32_e32 v199, v201, v200
	v_mov_b32_e32 v203, v199
	s_nop 1
	v_permlane32_swap_b32 v203, v199
	s_nop 1
	s_and_saveexec_b64 s[4:5], s[6:7]
	v_lshlrev_b64 v[194:195], 8, v[192:193]
	v_lshl_add_u64 v[194:195], s[16:17], 0, v[194:195]
	v_lshl_add_u64 v[194:195], s[68:69], 3, v[194:195]
	v_pk_add_f32 v[200:201], v[202:203], v[198:199]
	global_store_dwordx2 v[194:195], v[200:201], off
	s_or_b64 exec, exec, s[4:5]
.Lg9_nostat_0:
	v_add_u32_e32 v192, 0x10, v148
	v_ashrrev_i32_e32 v193, 31, v192
	v_lshlrev_b64 v[194:195], 12, v[192:193]
	v_lshl_add_u64 v[196:197], v[146:147], 0, v[194:195]
	v_pk_add_f32 v[124:125], v[124:125], v[76:77]
	v_pk_add_f32 v[126:127], v[126:127], v[78:79]
	v_pk_add_f32 v[120:121], v[120:121], v[68:69]
	v_pk_add_f32 v[122:123], v[122:123], v[70:71]
	v_med3_f32 v160, v124, s78, v158
	v_med3_f32 v161, v125, s78, v158
	v_med3_f32 v162, v126, s78, v158
	v_med3_f32 v163, v127, s78, v158
	v_med3_f32 v164, v120, s78, v158
	v_med3_f32 v165, v121, s78, v158
	v_med3_f32 v166, v122, s78, v158
	v_med3_f32 v167, v123, s78, v158
	v_pk_mul_f32 v[168:169], v[160:161], v[160:161]
	v_pk_mul_f32 v[170:171], v[162:163], v[162:163]
	v_pk_mul_f32 v[172:173], v[164:165], v[164:165]
	v_pk_mul_f32 v[174:175], v[166:167], v[166:167]
	v_pk_fma_f32 v[168:169], v[168:169], s[20:21], -1.0 op_sel_hi:[1,0,0]
	v_pk_fma_f32 v[170:171], v[170:171], s[20:21], -1.0 op_sel_hi:[1,0,0]
	v_pk_fma_f32 v[172:173], v[172:173], s[20:21], -1.0 op_sel_hi:[1,0,0]
	v_pk_fma_f32 v[174:175], v[174:175], s[20:21], -1.0 op_sel_hi:[1,0,0]
	v_pk_fma_f32 v[176:177], v[168:169], s[22:23], v[150:151] op_sel_hi:[1,0,0] neg_lo:[1,0,0] neg_hi:[1,0,0]
	v_pk_fma_f32 v[178:179], v[170:171], s[22:23], v[150:151] op_sel_hi:[1,0,0] neg_lo:[1,0,0] neg_hi:[1,0,0]
	v_pk_fma_f32 v[180:181], v[172:173], s[22:23], v[150:151] op_sel_hi:[1,0,0] neg_lo:[1,0,0] neg_hi:[1,0,0]
	v_pk_fma_f32 v[182:183], v[174:175], s[22:23], v[150:151] op_sel_hi:[1,0,0] neg_lo:[1,0,0] neg_hi:[1,0,0]
	v_pk_fma_f32 v[176:177], v[168:169], v[176:177], s[26:27] op_sel_hi:[1,1,0]
	v_pk_fma_f32 v[178:179], v[170:171], v[178:179], s[26:27] op_sel_hi:[1,1,0]
	v_pk_fma_f32 v[180:181], v[172:173], v[180:181], s[26:27] op_sel_hi:[1,1,0]
	v_pk_fma_f32 v[182:183], v[174:175], v[182:183], s[26:27] op_sel_hi:[1,1,0]
	v_pk_fma_f32 v[176:177], v[168:169], v[176:177], s[28:29] op_sel_hi:[1,1,0]
	v_pk_fma_f32 v[178:179], v[170:171], v[178:179], s[28:29] op_sel_hi:[1,1,0]
	v_pk_fma_f32 v[180:181], v[172:173], v[180:181], s[28:29] op_sel_hi:[1,1,0]
	v_pk_fma_f32 v[182:183], v[174:175], v[182:183], s[28:29] op_sel_hi:[1,1,0]
	v_pk_fma_f32 v[176:177], v[168:169], v[176:177], s[30:31] op_sel_hi:[1,1,0]
	v_pk_fma_f32 v[178:179], v[170:171], v[178:179], s[30:31] op_sel_hi:[1,1,0]
	v_pk_fma_f32 v[180:181], v[172:173], v[180:181], s[30:31] op_sel_hi:[1,1,0]
	v_pk_fma_f32 v[182:183], v[174:175], v[182:183], s[30:31] op_sel_hi:[1,1,0]
	v_pk_fma_f32 v[176:177], v[168:169], v[176:177], s[34:35] op_sel_hi:[1,1,0]
	v_pk_fma_f32 v[178:179], v[170:171], v[178:179], s[34:35] op_sel_hi:[1,1,0]
	v_pk_fma_f32 v[180:181], v[172:173], v[180:181], s[34:35] op_sel_hi:[1,1,0]
	v_pk_fma_f32 v[182:183], v[174:175], v[182:183], s[34:35] op_sel_hi:[1,1,0]
	v_pk_fma_f32 v[176:177], v[168:169], v[176:177], s[36:37] op_sel_hi:[1,1,0]
	v_pk_fma_f32 v[178:179], v[170:171], v[178:179], s[36:37] op_sel_hi:[1,1,0]
	v_pk_fma_f32 v[180:181], v[172:173], v[180:181], s[36:37] op_sel_hi:[1,1,0]
	v_pk_fma_f32 v[182:183], v[174:175], v[182:183], s[36:37] op_sel_hi:[1,1,0]
	v_pk_fma_f32 v[176:177], v[168:169], v[176:177], s[38:39] op_sel_hi:[1,1,0]
	v_pk_fma_f32 v[178:179], v[170:171], v[178:179], s[38:39] op_sel_hi:[1,1,0]
	v_pk_fma_f32 v[180:181], v[172:173], v[180:181], s[38:39] op_sel_hi:[1,1,0]
	v_pk_fma_f32 v[182:183], v[174:175], v[182:183], s[38:39] op_sel_hi:[1,1,0]
	v_pk_fma_f32 v[176:177], v[168:169], v[176:177], s[40:41] op_sel_hi:[1,1,0]
	v_pk_fma_f32 v[178:179], v[170:171], v[178:179], s[40:41] op_sel_hi:[1,1,0]
	v_pk_fma_f32 v[180:181], v[172:173], v[180:181], s[40:41] op_sel_hi:[1,1,0]
	v_pk_fma_f32 v[182:183], v[174:175], v[182:183], s[40:41] op_sel_hi:[1,1,0]
	v_pk_fma_f32 v[176:177], v[168:169], v[176:177], s[42:43] op_sel_hi:[1,1,0]
	v_pk_fma_f32 v[178:179], v[170:171], v[178:179], s[42:43] op_sel_hi:[1,1,0]
	v_pk_fma_f32 v[180:181], v[172:173], v[180:181], s[42:43] op_sel_hi:[1,1,0]
	v_pk_fma_f32 v[182:183], v[174:175], v[182:183], s[42:43] op_sel_hi:[1,1,0]
	v_pk_fma_f32 v[176:177], v[168:169], v[176:177], s[44:45] op_sel_hi:[1,1,0]
	v_pk_fma_f32 v[178:179], v[170:171], v[178:179], s[44:45] op_sel_hi:[1,1,0]
	v_pk_fma_f32 v[180:181], v[172:173], v[180:181], s[44:45] op_sel_hi:[1,1,0]
	v_pk_fma_f32 v[182:183], v[174:175], v[182:183], s[44:45] op_sel_hi:[1,1,0]
	v_pk_fma_f32 v[168:169], v[168:169], v[176:177], s[48:49] op_sel_hi:[1,1,0]
	v_pk_fma_f32 v[170:171], v[170:171], v[178:179], s[48:49] op_sel_hi:[1,1,0]
	v_pk_fma_f32 v[172:173], v[172:173], v[180:181], s[48:49] op_sel_hi:[1,1,0]
	v_pk_fma_f32 v[174:175], v[174:175], v[182:183], s[48:49] op_sel_hi:[1,1,0]
	v_pk_fma_f32 v[160:161], v[160:161], v[168:169], 0.5 op_sel_hi:[1,1,0]
	v_pk_fma_f32 v[162:163], v[162:163], v[170:171], 0.5 op_sel_hi:[1,1,0]
	v_pk_fma_f32 v[164:165], v[164:165], v[172:173], 0.5 op_sel_hi:[1,1,0]
	v_pk_fma_f32 v[166:167], v[166:167], v[174:175], 0.5 op_sel_hi:[1,1,0]
	v_pk_mul_f32 v[124:125], v[124:125], v[160:161]
	v_pk_mul_f32 v[126:127], v[126:127], v[162:163]
	v_pk_mul_f32 v[120:121], v[120:121], v[164:165]
	v_pk_mul_f32 v[122:123], v[122:123], v[166:167]
	v_cvt_pk_bf16_f32 v184, v124, v125
	v_cvt_pk_bf16_f32 v185, v126, v127
	v_cvt_pk_bf16_f32 v186, v120, v121
	v_cvt_pk_bf16_f32 v187, v122, v123
	global_store_dwordx4 v[196:197], v[184:187], off
	v_pk_add_f32 v[116:117], v[116:117], v[60:61]
	v_pk_add_f32 v[118:119], v[118:119], v[62:63]
	v_pk_add_f32 v[112:113], v[112:113], v[56:57]
	v_pk_add_f32 v[114:115], v[114:115], v[58:59]
	v_med3_f32 v160, v116, s78, v158
	v_med3_f32 v161, v117, s78, v158
	v_med3_f32 v162, v118, s78, v158
	v_med3_f32 v163, v119, s78, v158
	v_med3_f32 v164, v112, s78, v158
	v_med3_f32 v165, v113, s78, v158
	v_med3_f32 v166, v114, s78, v158
	v_med3_f32 v167, v115, s78, v158
	v_pk_mul_f32 v[168:169], v[160:161], v[160:161]
	v_pk_mul_f32 v[170:171], v[162:163], v[162:163]
	v_pk_mul_f32 v[172:173], v[164:165], v[164:165]
	v_pk_mul_f32 v[174:175], v[166:167], v[166:167]
	v_pk_fma_f32 v[168:169], v[168:169], s[20:21], -1.0 op_sel_hi:[1,0,0]
	v_pk_fma_f32 v[170:171], v[170:171], s[20:21], -1.0 op_sel_hi:[1,0,0]
	v_pk_fma_f32 v[172:173], v[172:173], s[20:21], -1.0 op_sel_hi:[1,0,0]
	v_pk_fma_f32 v[174:175], v[174:175], s[20:21], -1.0 op_sel_hi:[1,0,0]
	v_pk_fma_f32 v[176:177], v[168:169], s[22:23], v[150:151] op_sel_hi:[1,0,0] neg_lo:[1,0,0] neg_hi:[1,0,0]
	v_pk_fma_f32 v[178:179], v[170:171], s[22:23], v[150:151] op_sel_hi:[1,0,0] neg_lo:[1,0,0] neg_hi:[1,0,0]
	v_pk_fma_f32 v[180:181], v[172:173], s[22:23], v[150:151] op_sel_hi:[1,0,0] neg_lo:[1,0,0] neg_hi:[1,0,0]
	v_pk_fma_f32 v[182:183], v[174:175], s[22:23], v[150:151] op_sel_hi:[1,0,0] neg_lo:[1,0,0] neg_hi:[1,0,0]
	v_pk_fma_f32 v[176:177], v[168:169], v[176:177], s[26:27] op_sel_hi:[1,1,0]
	v_pk_fma_f32 v[178:179], v[170:171], v[178:179], s[26:27] op_sel_hi:[1,1,0]
	v_pk_fma_f32 v[180:181], v[172:173], v[180:181], s[26:27] op_sel_hi:[1,1,0]
	v_pk_fma_f32 v[182:183], v[174:175], v[182:183], s[26:27] op_sel_hi:[1,1,0]
	v_pk_fma_f32 v[176:177], v[168:169], v[176:177], s[28:29] op_sel_hi:[1,1,0]
	v_pk_fma_f32 v[178:179], v[170:171], v[178:179], s[28:29] op_sel_hi:[1,1,0]
	v_pk_fma_f32 v[180:181], v[172:173], v[180:181], s[28:29] op_sel_hi:[1,1,0]
	v_pk_fma_f32 v[182:183], v[174:175], v[182:183], s[28:29] op_sel_hi:[1,1,0]
	v_pk_fma_f32 v[176:177], v[168:169], v[176:177], s[30:31] op_sel_hi:[1,1,0]
	v_pk_fma_f32 v[178:179], v[170:171], v[178:179], s[30:31] op_sel_hi:[1,1,0]
	v_pk_fma_f32 v[180:181], v[172:173], v[180:181], s[30:31] op_sel_hi:[1,1,0]
	v_pk_fma_f32 v[182:183], v[174:175], v[182:183], s[30:31] op_sel_hi:[1,1,0]
	v_pk_fma_f32 v[176:177], v[168:169], v[176:177], s[34:35] op_sel_hi:[1,1,0]
	v_pk_fma_f32 v[178:179], v[170:171], v[178:179], s[34:35] op_sel_hi:[1,1,0]
	v_pk_fma_f32 v[180:181], v[172:173], v[180:181], s[34:35] op_sel_hi:[1,1,0]
	v_pk_fma_f32 v[182:183], v[174:175], v[182:183], s[34:35] op_sel_hi:[1,1,0]
	v_pk_fma_f32 v[176:177], v[168:169], v[176:177], s[36:37] op_sel_hi:[1,1,0]
	v_pk_fma_f32 v[178:179], v[170:171], v[178:179], s[36:37] op_sel_hi:[1,1,0]
	v_pk_fma_f32 v[180:181], v[172:173], v[180:181], s[36:37] op_sel_hi:[1,1,0]
	v_pk_fma_f32 v[182:183], v[174:175], v[182:183], s[36:37] op_sel_hi:[1,1,0]
	v_pk_fma_f32 v[176:177], v[168:169], v[176:177], s[38:39] op_sel_hi:[1,1,0]
	v_pk_fma_f32 v[178:179], v[170:171], v[178:179], s[38:39] op_sel_hi:[1,1,0]
	v_pk_fma_f32 v[180:181], v[172:173], v[180:181], s[38:39] op_sel_hi:[1,1,0]
	v_pk_fma_f32 v[182:183], v[174:175], v[182:183], s[38:39] op_sel_hi:[1,1,0]
	v_pk_fma_f32 v[176:177], v[168:169], v[176:177], s[40:41] op_sel_hi:[1,1,0]
	v_pk_fma_f32 v[178:179], v[170:171], v[178:179], s[40:41] op_sel_hi:[1,1,0]
	v_pk_fma_f32 v[180:181], v[172:173], v[180:181], s[40:41] op_sel_hi:[1,1,0]
	v_pk_fma_f32 v[182:183], v[174:175], v[182:183], s[40:41] op_sel_hi:[1,1,0]
	v_pk_fma_f32 v[176:177], v[168:169], v[176:177], s[42:43] op_sel_hi:[1,1,0]
	v_pk_fma_f32 v[178:179], v[170:171], v[178:179], s[42:43] op_sel_hi:[1,1,0]
	v_pk_fma_f32 v[180:181], v[172:173], v[180:181], s[42:43] op_sel_hi:[1,1,0]
	v_pk_fma_f32 v[182:183], v[174:175], v[182:183], s[42:43] op_sel_hi:[1,1,0]
	v_pk_fma_f32 v[176:177], v[168:169], v[176:177], s[44:45] op_sel_hi:[1,1,0]
	v_pk_fma_f32 v[178:179], v[170:171], v[178:179], s[44:45] op_sel_hi:[1,1,0]
	v_pk_fma_f32 v[180:181], v[172:173], v[180:181], s[44:45] op_sel_hi:[1,1,0]
	v_pk_fma_f32 v[182:183], v[174:175], v[182:183], s[44:45] op_sel_hi:[1,1,0]
	v_pk_fma_f32 v[168:169], v[168:169], v[176:177], s[48:49] op_sel_hi:[1,1,0]
	v_pk_fma_f32 v[170:171], v[170:171], v[178:179], s[48:49] op_sel_hi:[1,1,0]
	v_pk_fma_f32 v[172:173], v[172:173], v[180:181], s[48:49] op_sel_hi:[1,1,0]
	v_pk_fma_f32 v[174:175], v[174:175], v[182:183], s[48:49] op_sel_hi:[1,1,0]
	v_pk_fma_f32 v[160:161], v[160:161], v[168:169], 0.5 op_sel_hi:[1,1,0]
	v_pk_fma_f32 v[162:163], v[162:163], v[170:171], 0.5 op_sel_hi:[1,1,0]
	v_pk_fma_f32 v[164:165], v[164:165], v[172:173], 0.5 op_sel_hi:[1,1,0]
	v_pk_fma_f32 v[166:167], v[166:167], v[174:175], 0.5 op_sel_hi:[1,1,0]
	v_pk_mul_f32 v[116:117], v[116:117], v[160:161]
	v_pk_mul_f32 v[118:119], v[118:119], v[162:163]
	v_pk_mul_f32 v[112:113], v[112:113], v[164:165]
	v_pk_mul_f32 v[114:115], v[114:115], v[166:167]
	v_cvt_pk_bf16_f32 v188, v116, v117
	v_cvt_pk_bf16_f32 v189, v118, v119
	v_cvt_pk_bf16_f32 v190, v112, v113
	v_cvt_pk_bf16_f32 v191, v114, v115
	global_store_dwordx4 v[196:197], v[188:191], off offset:256
	s_and_b64 vcc, exec, s[70:71]
	s_cbranch_vccz .Lg9_nostat_1
	v_pk_mul_f32 v[168:169], v[124:125], v[124:125]
	v_pk_mul_f32 v[170:171], v[126:127], v[126:127]
	v_pk_mul_f32 v[172:173], v[120:121], v[120:121]
	v_pk_mul_f32 v[174:175], v[122:123], v[122:123]
	v_pk_mul_f32 v[176:177], v[116:117], v[116:117]
	v_pk_mul_f32 v[178:179], v[118:119], v[118:119]
	v_pk_mul_f32 v[180:181], v[112:113], v[112:113]
	v_pk_mul_f32 v[182:183], v[114:115], v[114:115]
	v_add_f32_e32 v160, v124, v125
	v_add_f32_e32 v161, v126, v127
	v_add_f32_e32 v162, v120, v121
	v_add_f32_e32 v163, v122, v123
	v_add_f32_e32 v164, v116, v117
	v_add_f32_e32 v165, v118, v119
	v_add_f32_e32 v166, v112, v113
	v_add_f32_e32 v167, v114, v115
	v_add_f32_e32 v160, v160, v161
	v_add_f32_e32 v164, v164, v165
	v_add_f32_e32 v160, v160, v162
	v_add_f32_e32 v164, v164, v166
	v_add_f32_e32 v160, v160, v163
	v_add_f32_e32 v164, v164, v167
	v_add_f32_e32 v168, v168, v169
	v_add_f32_e32 v170, v170, v171
	v_add_f32_e32 v172, v172, v173
	v_add_f32_e32 v174, v174, v175
	v_add_f32_e32 v176, v176, v177
	v_add_f32_e32 v178, v178, v179
	v_add_f32_e32 v180, v180, v181
	v_add_f32_e32 v182, v182, v183
	v_add_f32_e32 v198, v160, v164
	v_add_f32_e32 v168, v168, v170
	v_add_f32_e32 v176, v176, v178
	v_mov_b32_e32 v199, v198
	v_add_f32_e32 v168, v168, v172
	v_add_f32_e32 v176, v176, v180
	s_nop 1
	v_permlane16_swap_b32 v199, v198
	s_nop 1
	v_add_f32_e32 v168, v168, v174
	v_add_f32_e32 v176, v176, v182
	v_add_f32_e32 v198, v199, v198
	v_add_f32_e32 v200, v168, v176
	v_mov_b32_e32 v202, v198
	v_mov_b32_e32 v201, v200
	s_nop 1
	v_permlane32_swap_b32 v202, v198
	s_nop 1
	s_nop 1
	v_permlane16_swap_b32 v201, v200
	s_nop 1
	v_add_f32_e32 v199, v201, v200
	v_mov_b32_e32 v203, v199
	s_nop 1
	v_permlane32_swap_b32 v203, v199
	s_nop 1
	s_and_saveexec_b64 s[4:5], s[6:7]
	v_lshlrev_b64 v[194:195], 8, v[192:193]
	v_lshl_add_u64 v[194:195], s[16:17], 0, v[194:195]
	v_lshl_add_u64 v[194:195], s[68:69], 3, v[194:195]
	v_pk_add_f32 v[200:201], v[202:203], v[198:199]
	global_store_dwordx2 v[194:195], v[200:201], off
	s_or_b64 exec, exec, s[4:5]
.Lg9_nostat_1:
	v_add_u32_e32 v192, 0x20, v148
	v_ashrrev_i32_e32 v193, 31, v192
	v_lshlrev_b64 v[194:195], 12, v[192:193]
	v_lshl_add_u64 v[196:197], v[146:147], 0, v[194:195]
	v_pk_add_f32 v[108:109], v[108:109], v[76:77]
	v_pk_add_f32 v[110:111], v[110:111], v[78:79]
	v_pk_add_f32 v[104:105], v[104:105], v[68:69]
	v_pk_add_f32 v[106:107], v[106:107], v[70:71]
	v_med3_f32 v160, v108, s78, v158
	v_med3_f32 v161, v109, s78, v158
	v_med3_f32 v162, v110, s78, v158
	v_med3_f32 v163, v111, s78, v158
	v_med3_f32 v164, v104, s78, v158
	v_med3_f32 v165, v105, s78, v158
	v_med3_f32 v166, v106, s78, v158
	v_med3_f32 v167, v107, s78, v158
	v_pk_mul_f32 v[168:169], v[160:161], v[160:161]
	v_pk_mul_f32 v[170:171], v[162:163], v[162:163]
	v_pk_mul_f32 v[172:173], v[164:165], v[164:165]
	v_pk_mul_f32 v[174:175], v[166:167], v[166:167]
	v_pk_fma_f32 v[168:169], v[168:169], s[20:21], -1.0 op_sel_hi:[1,0,0]
	v_pk_fma_f32 v[170:171], v[170:171], s[20:21], -1.0 op_sel_hi:[1,0,0]
	v_pk_fma_f32 v[172:173], v[172:173], s[20:21], -1.0 op_sel_hi:[1,0,0]
	v_pk_fma_f32 v[174:175], v[174:175], s[20:21], -1.0 op_sel_hi:[1,0,0]
	v_pk_fma_f32 v[176:177], v[168:169], s[22:23], v[150:151] op_sel_hi:[1,0,0] neg_lo:[1,0,0] neg_hi:[1,0,0]
	v_pk_fma_f32 v[178:179], v[170:171], s[22:23], v[150:151] op_sel_hi:[1,0,0] neg_lo:[1,0,0] neg_hi:[1,0,0]
	v_pk_fma_f32 v[180:181], v[172:173], s[22:23], v[150:151] op_sel_hi:[1,0,0] neg_lo:[1,0,0] neg_hi:[1,0,0]
	v_pk_fma_f32 v[182:183], v[174:175], s[22:23], v[150:151] op_sel_hi:[1,0,0] neg_lo:[1,0,0] neg_hi:[1,0,0]
	v_pk_fma_f32 v[176:177], v[168:169], v[176:177], s[26:27] op_sel_hi:[1,1,0]
	v_pk_fma_f32 v[178:179], v[170:171], v[178:179], s[26:27] op_sel_hi:[1,1,0]
	v_pk_fma_f32 v[180:181], v[172:173], v[180:181], s[26:27] op_sel_hi:[1,1,0]
	v_pk_fma_f32 v[182:183], v[174:175], v[182:183], s[26:27] op_sel_hi:[1,1,0]
	v_pk_fma_f32 v[176:177], v[168:169], v[176:177], s[28:29] op_sel_hi:[1,1,0]
	v_pk_fma_f32 v[178:179], v[170:171], v[178:179], s[28:29] op_sel_hi:[1,1,0]
	v_pk_fma_f32 v[180:181], v[172:173], v[180:181], s[28:29] op_sel_hi:[1,1,0]
	v_pk_fma_f32 v[182:183], v[174:175], v[182:183], s[28:29] op_sel_hi:[1,1,0]
	v_pk_fma_f32 v[176:177], v[168:169], v[176:177], s[30:31] op_sel_hi:[1,1,0]
	v_pk_fma_f32 v[178:179], v[170:171], v[178:179], s[30:31] op_sel_hi:[1,1,0]
	v_pk_fma_f32 v[180:181], v[172:173], v[180:181], s[30:31] op_sel_hi:[1,1,0]
	v_pk_fma_f32 v[182:183], v[174:175], v[182:183], s[30:31] op_sel_hi:[1,1,0]
	v_pk_fma_f32 v[176:177], v[168:169], v[176:177], s[34:35] op_sel_hi:[1,1,0]
	v_pk_fma_f32 v[178:179], v[170:171], v[178:179], s[34:35] op_sel_hi:[1,1,0]
	v_pk_fma_f32 v[180:181], v[172:173], v[180:181], s[34:35] op_sel_hi:[1,1,0]
	v_pk_fma_f32 v[182:183], v[174:175], v[182:183], s[34:35] op_sel_hi:[1,1,0]
	v_pk_fma_f32 v[176:177], v[168:169], v[176:177], s[36:37] op_sel_hi:[1,1,0]
	v_pk_fma_f32 v[178:179], v[170:171], v[178:179], s[36:37] op_sel_hi:[1,1,0]
	v_pk_fma_f32 v[180:181], v[172:173], v[180:181], s[36:37] op_sel_hi:[1,1,0]
	v_pk_fma_f32 v[182:183], v[174:175], v[182:183], s[36:37] op_sel_hi:[1,1,0]
	v_pk_fma_f32 v[176:177], v[168:169], v[176:177], s[38:39] op_sel_hi:[1,1,0]
	v_pk_fma_f32 v[178:179], v[170:171], v[178:179], s[38:39] op_sel_hi:[1,1,0]
	v_pk_fma_f32 v[180:181], v[172:173], v[180:181], s[38:39] op_sel_hi:[1,1,0]
	v_pk_fma_f32 v[182:183], v[174:175], v[182:183], s[38:39] op_sel_hi:[1,1,0]
	v_pk_fma_f32 v[176:177], v[168:169], v[176:177], s[40:41] op_sel_hi:[1,1,0]
	v_pk_fma_f32 v[178:179], v[170:171], v[178:179], s[40:41] op_sel_hi:[1,1,0]
	v_pk_fma_f32 v[180:181], v[172:173], v[180:181], s[40:41] op_sel_hi:[1,1,0]
	v_pk_fma_f32 v[182:183], v[174:175], v[182:183], s[40:41] op_sel_hi:[1,1,0]
	v_pk_fma_f32 v[176:177], v[168:169], v[176:177], s[42:43] op_sel_hi:[1,1,0]
	v_pk_fma_f32 v[178:179], v[170:171], v[178:179], s[42:43] op_sel_hi:[1,1,0]
	v_pk_fma_f32 v[180:181], v[172:173], v[180:181], s[42:43] op_sel_hi:[1,1,0]
	v_pk_fma_f32 v[182:183], v[174:175], v[182:183], s[42:43] op_sel_hi:[1,1,0]
	v_pk_fma_f32 v[176:177], v[168:169], v[176:177], s[44:45] op_sel_hi:[1,1,0]
	v_pk_fma_f32 v[178:179], v[170:171], v[178:179], s[44:45] op_sel_hi:[1,1,0]
	v_pk_fma_f32 v[180:181], v[172:173], v[180:181], s[44:45] op_sel_hi:[1,1,0]
	v_pk_fma_f32 v[182:183], v[174:175], v[182:183], s[44:45] op_sel_hi:[1,1,0]
	v_pk_fma_f32 v[168:169], v[168:169], v[176:177], s[48:49] op_sel_hi:[1,1,0]
	v_pk_fma_f32 v[170:171], v[170:171], v[178:179], s[48:49] op_sel_hi:[1,1,0]
	v_pk_fma_f32 v[172:173], v[172:173], v[180:181], s[48:49] op_sel_hi:[1,1,0]
	v_pk_fma_f32 v[174:175], v[174:175], v[182:183], s[48:49] op_sel_hi:[1,1,0]
	v_pk_fma_f32 v[160:161], v[160:161], v[168:169], 0.5 op_sel_hi:[1,1,0]
	v_pk_fma_f32 v[162:163], v[162:163], v[170:171], 0.5 op_sel_hi:[1,1,0]
	v_pk_fma_f32 v[164:165], v[164:165], v[172:173], 0.5 op_sel_hi:[1,1,0]
	v_pk_fma_f32 v[166:167], v[166:167], v[174:175], 0.5 op_sel_hi:[1,1,0]
	v_pk_mul_f32 v[108:109], v[108:109], v[160:161]
	v_pk_mul_f32 v[110:111], v[110:111], v[162:163]
	v_pk_mul_f32 v[104:105], v[104:105], v[164:165]
	v_pk_mul_f32 v[106:107], v[106:107], v[166:167]
	v_cvt_pk_bf16_f32 v184, v108, v109
	v_cvt_pk_bf16_f32 v185, v110, v111
	v_cvt_pk_bf16_f32 v186, v104, v105
	v_cvt_pk_bf16_f32 v187, v106, v107
	global_store_dwordx4 v[196:197], v[184:187], off
	v_pk_add_f32 v[100:101], v[100:101], v[60:61]
	v_pk_add_f32 v[102:103], v[102:103], v[62:63]
	v_pk_add_f32 v[96:97], v[96:97], v[56:57]
	v_pk_add_f32 v[98:99], v[98:99], v[58:59]
	v_med3_f32 v160, v100, s78, v158
	v_med3_f32 v161, v101, s78, v158
	v_med3_f32 v162, v102, s78, v158
	v_med3_f32 v163, v103, s78, v158
	v_med3_f32 v164, v96, s78, v158
	v_med3_f32 v165, v97, s78, v158
	v_med3_f32 v166, v98, s78, v158
	v_med3_f32 v167, v99, s78, v158
	v_pk_mul_f32 v[168:169], v[160:161], v[160:161]
	v_pk_mul_f32 v[170:171], v[162:163], v[162:163]
	v_pk_mul_f32 v[172:173], v[164:165], v[164:165]
	v_pk_mul_f32 v[174:175], v[166:167], v[166:167]
	v_pk_fma_f32 v[168:169], v[168:169], s[20:21], -1.0 op_sel_hi:[1,0,0]
	v_pk_fma_f32 v[170:171], v[170:171], s[20:21], -1.0 op_sel_hi:[1,0,0]
	v_pk_fma_f32 v[172:173], v[172:173], s[20:21], -1.0 op_sel_hi:[1,0,0]
	v_pk_fma_f32 v[174:175], v[174:175], s[20:21], -1.0 op_sel_hi:[1,0,0]
	v_pk_fma_f32 v[176:177], v[168:169], s[22:23], v[150:151] op_sel_hi:[1,0,0] neg_lo:[1,0,0] neg_hi:[1,0,0]
	v_pk_fma_f32 v[178:179], v[170:171], s[22:23], v[150:151] op_sel_hi:[1,0,0] neg_lo:[1,0,0] neg_hi:[1,0,0]
	v_pk_fma_f32 v[180:181], v[172:173], s[22:23], v[150:151] op_sel_hi:[1,0,0] neg_lo:[1,0,0] neg_hi:[1,0,0]
	v_pk_fma_f32 v[182:183], v[174:175], s[22:23], v[150:151] op_sel_hi:[1,0,0] neg_lo:[1,0,0] neg_hi:[1,0,0]
	v_pk_fma_f32 v[176:177], v[168:169], v[176:177], s[26:27] op_sel_hi:[1,1,0]
	v_pk_fma_f32 v[178:179], v[170:171], v[178:179], s[26:27] op_sel_hi:[1,1,0]
	v_pk_fma_f32 v[180:181], v[172:173], v[180:181], s[26:27] op_sel_hi:[1,1,0]
	v_pk_fma_f32 v[182:183], v[174:175], v[182:183], s[26:27] op_sel_hi:[1,1,0]
	v_pk_fma_f32 v[176:177], v[168:169], v[176:177], s[28:29] op_sel_hi:[1,1,0]
	v_pk_fma_f32 v[178:179], v[170:171], v[178:179], s[28:29] op_sel_hi:[1,1,0]
	v_pk_fma_f32 v[180:181], v[172:173], v[180:181], s[28:29] op_sel_hi:[1,1,0]
	v_pk_fma_f32 v[182:183], v[174:175], v[182:183], s[28:29] op_sel_hi:[1,1,0]
	v_pk_fma_f32 v[176:177], v[168:169], v[176:177], s[30:31] op_sel_hi:[1,1,0]
	v_pk_fma_f32 v[178:179], v[170:171], v[178:179], s[30:31] op_sel_hi:[1,1,0]
	v_pk_fma_f32 v[180:181], v[172:173], v[180:181], s[30:31] op_sel_hi:[1,1,0]
	v_pk_fma_f32 v[182:183], v[174:175], v[182:183], s[30:31] op_sel_hi:[1,1,0]
	v_pk_fma_f32 v[176:177], v[168:169], v[176:177], s[34:35] op_sel_hi:[1,1,0]
	v_pk_fma_f32 v[178:179], v[170:171], v[178:179], s[34:35] op_sel_hi:[1,1,0]
	v_pk_fma_f32 v[180:181], v[172:173], v[180:181], s[34:35] op_sel_hi:[1,1,0]
	v_pk_fma_f32 v[182:183], v[174:175], v[182:183], s[34:35] op_sel_hi:[1,1,0]
	v_pk_fma_f32 v[176:177], v[168:169], v[176:177], s[36:37] op_sel_hi:[1,1,0]
	v_pk_fma_f32 v[178:179], v[170:171], v[178:179], s[36:37] op_sel_hi:[1,1,0]
	v_pk_fma_f32 v[180:181], v[172:173], v[180:181], s[36:37] op_sel_hi:[1,1,0]
	v_pk_fma_f32 v[182:183], v[174:175], v[182:183], s[36:37] op_sel_hi:[1,1,0]
	v_pk_fma_f32 v[176:177], v[168:169], v[176:177], s[38:39] op_sel_hi:[1,1,0]
	v_pk_fma_f32 v[178:179], v[170:171], v[178:179], s[38:39] op_sel_hi:[1,1,0]
	v_pk_fma_f32 v[180:181], v[172:173], v[180:181], s[38:39] op_sel_hi:[1,1,0]
	v_pk_fma_f32 v[182:183], v[174:175], v[182:183], s[38:39] op_sel_hi:[1,1,0]
	v_pk_fma_f32 v[176:177], v[168:169], v[176:177], s[40:41] op_sel_hi:[1,1,0]
	v_pk_fma_f32 v[178:179], v[170:171], v[178:179], s[40:41] op_sel_hi:[1,1,0]
	v_pk_fma_f32 v[180:181], v[172:173], v[180:181], s[40:41] op_sel_hi:[1,1,0]
	v_pk_fma_f32 v[182:183], v[174:175], v[182:183], s[40:41] op_sel_hi:[1,1,0]
	v_pk_fma_f32 v[176:177], v[168:169], v[176:177], s[42:43] op_sel_hi:[1,1,0]
	v_pk_fma_f32 v[178:179], v[170:171], v[178:179], s[42:43] op_sel_hi:[1,1,0]
	v_pk_fma_f32 v[180:181], v[172:173], v[180:181], s[42:43] op_sel_hi:[1,1,0]
	v_pk_fma_f32 v[182:183], v[174:175], v[182:183], s[42:43] op_sel_hi:[1,1,0]
	v_pk_fma_f32 v[176:177], v[168:169], v[176:177], s[44:45] op_sel_hi:[1,1,0]
	v_pk_fma_f32 v[178:179], v[170:171], v[178:179], s[44:45] op_sel_hi:[1,1,0]
	v_pk_fma_f32 v[180:181], v[172:173], v[180:181], s[44:45] op_sel_hi:[1,1,0]
	v_pk_fma_f32 v[182:183], v[174:175], v[182:183], s[44:45] op_sel_hi:[1,1,0]
	v_pk_fma_f32 v[168:169], v[168:169], v[176:177], s[48:49] op_sel_hi:[1,1,0]
	v_pk_fma_f32 v[170:171], v[170:171], v[178:179], s[48:49] op_sel_hi:[1,1,0]
	v_pk_fma_f32 v[172:173], v[172:173], v[180:181], s[48:49] op_sel_hi:[1,1,0]
	v_pk_fma_f32 v[174:175], v[174:175], v[182:183], s[48:49] op_sel_hi:[1,1,0]
	v_pk_fma_f32 v[160:161], v[160:161], v[168:169], 0.5 op_sel_hi:[1,1,0]
	v_pk_fma_f32 v[162:163], v[162:163], v[170:171], 0.5 op_sel_hi:[1,1,0]
	v_pk_fma_f32 v[164:165], v[164:165], v[172:173], 0.5 op_sel_hi:[1,1,0]
	v_pk_fma_f32 v[166:167], v[166:167], v[174:175], 0.5 op_sel_hi:[1,1,0]
	v_pk_mul_f32 v[100:101], v[100:101], v[160:161]
	v_pk_mul_f32 v[102:103], v[102:103], v[162:163]
	v_pk_mul_f32 v[96:97], v[96:97], v[164:165]
	v_pk_mul_f32 v[98:99], v[98:99], v[166:167]
	v_cvt_pk_bf16_f32 v188, v100, v101
	v_cvt_pk_bf16_f32 v189, v102, v103
	v_cvt_pk_bf16_f32 v190, v96, v97
	v_cvt_pk_bf16_f32 v191, v98, v99
	global_store_dwordx4 v[196:197], v[188:191], off offset:256
	s_and_b64 vcc, exec, s[70:71]
	s_cbranch_vccz .Lg9_nostat_2
	v_pk_mul_f32 v[168:169], v[108:109], v[108:109]
	v_pk_mul_f32 v[170:171], v[110:111], v[110:111]
	v_pk_mul_f32 v[172:173], v[104:105], v[104:105]
	v_pk_mul_f32 v[174:175], v[106:107], v[106:107]
	v_pk_mul_f32 v[176:177], v[100:101], v[100:101]
	v_pk_mul_f32 v[178:179], v[102:103], v[102:103]
	v_pk_mul_f32 v[180:181], v[96:97], v[96:97]
	v_pk_mul_f32 v[182:183], v[98:99], v[98:99]
	v_add_f32_e32 v160, v108, v109
	v_add_f32_e32 v161, v110, v111
	v_add_f32_e32 v162, v104, v105
	v_add_f32_e32 v163, v106, v107
	v_add_f32_e32 v164, v100, v101
	v_add_f32_e32 v165, v102, v103
	v_add_f32_e32 v166, v96, v97
	v_add_f32_e32 v167, v98, v99
	v_add_f32_e32 v160, v160, v161
	v_add_f32_e32 v164, v164, v165
	v_add_f32_e32 v160, v160, v162
	v_add_f32_e32 v164, v164, v166
	v_add_f32_e32 v160, v160, v163
	v_add_f32_e32 v164, v164, v167
	v_add_f32_e32 v168, v168, v169
	v_add_f32_e32 v170, v170, v171
	v_add_f32_e32 v172, v172, v173
	v_add_f32_e32 v174, v174, v175
	v_add_f32_e32 v176, v176, v177
	v_add_f32_e32 v178, v178, v179
	v_add_f32_e32 v180, v180, v181
	v_add_f32_e32 v182, v182, v183
	v_add_f32_e32 v198, v160, v164
	v_add_f32_e32 v168, v168, v170
	v_add_f32_e32 v176, v176, v178
	v_mov_b32_e32 v199, v198
	v_add_f32_e32 v168, v168, v172
	v_add_f32_e32 v176, v176, v180
	s_nop 1
	v_permlane16_swap_b32 v199, v198
	s_nop 1
	v_add_f32_e32 v168, v168, v174
	v_add_f32_e32 v176, v176, v182
	v_add_f32_e32 v198, v199, v198
	v_add_f32_e32 v200, v168, v176
	v_mov_b32_e32 v202, v198
	v_mov_b32_e32 v201, v200
	s_nop 1
	v_permlane32_swap_b32 v202, v198
	s_nop 1
	s_nop 1
	v_permlane16_swap_b32 v201, v200
	s_nop 1
	v_add_f32_e32 v199, v201, v200
	v_mov_b32_e32 v203, v199
	s_nop 1
	v_permlane32_swap_b32 v203, v199
	s_nop 1
	s_and_saveexec_b64 s[4:5], s[6:7]
	v_lshlrev_b64 v[194:195], 8, v[192:193]
	v_lshl_add_u64 v[194:195], s[16:17], 0, v[194:195]
	v_lshl_add_u64 v[194:195], s[68:69], 3, v[194:195]
	v_pk_add_f32 v[200:201], v[202:203], v[198:199]
	global_store_dwordx2 v[194:195], v[200:201], off
	s_or_b64 exec, exec, s[4:5]
.Lg9_nostat_2:
	v_add_u32_e32 v192, 0x30, v148
	v_ashrrev_i32_e32 v193, 31, v192
	v_lshlrev_b64 v[194:195], 12, v[192:193]
	v_lshl_add_u64 v[196:197], v[146:147], 0, v[194:195]
	v_pk_add_f32 v[92:93], v[92:93], v[76:77]
	v_pk_add_f32 v[94:95], v[94:95], v[78:79]
	v_pk_add_f32 v[88:89], v[88:89], v[68:69]
	v_pk_add_f32 v[90:91], v[90:91], v[70:71]
	v_med3_f32 v160, v92, s78, v158
	v_med3_f32 v161, v93, s78, v158
	v_med3_f32 v162, v94, s78, v158
	v_med3_f32 v163, v95, s78, v158
	v_med3_f32 v164, v88, s78, v158
	v_med3_f32 v165, v89, s78, v158
	v_med3_f32 v166, v90, s78, v158
	v_med3_f32 v167, v91, s78, v158
	v_pk_mul_f32 v[168:169], v[160:161], v[160:161]
	v_pk_mul_f32 v[170:171], v[162:163], v[162:163]
	v_pk_mul_f32 v[172:173], v[164:165], v[164:165]
	v_pk_mul_f32 v[174:175], v[166:167], v[166:167]
	v_pk_fma_f32 v[168:169], v[168:169], s[20:21], -1.0 op_sel_hi:[1,0,0]
	v_pk_fma_f32 v[170:171], v[170:171], s[20:21], -1.0 op_sel_hi:[1,0,0]
	v_pk_fma_f32 v[172:173], v[172:173], s[20:21], -1.0 op_sel_hi:[1,0,0]
	v_pk_fma_f32 v[174:175], v[174:175], s[20:21], -1.0 op_sel_hi:[1,0,0]
	v_pk_fma_f32 v[176:177], v[168:169], s[22:23], v[150:151] op_sel_hi:[1,0,0] neg_lo:[1,0,0] neg_hi:[1,0,0]
	v_pk_fma_f32 v[178:179], v[170:171], s[22:23], v[150:151] op_sel_hi:[1,0,0] neg_lo:[1,0,0] neg_hi:[1,0,0]
	v_pk_fma_f32 v[180:181], v[172:173], s[22:23], v[150:151] op_sel_hi:[1,0,0] neg_lo:[1,0,0] neg_hi:[1,0,0]
	v_pk_fma_f32 v[182:183], v[174:175], s[22:23], v[150:151] op_sel_hi:[1,0,0] neg_lo:[1,0,0] neg_hi:[1,0,0]
	v_pk_fma_f32 v[176:177], v[168:169], v[176:177], s[26:27] op_sel_hi:[1,1,0]
	v_pk_fma_f32 v[178:179], v[170:171], v[178:179], s[26:27] op_sel_hi:[1,1,0]
	v_pk_fma_f32 v[180:181], v[172:173], v[180:181], s[26:27] op_sel_hi:[1,1,0]
	v_pk_fma_f32 v[182:183], v[174:175], v[182:183], s[26:27] op_sel_hi:[1,1,0]
	v_pk_fma_f32 v[176:177], v[168:169], v[176:177], s[28:29] op_sel_hi:[1,1,0]
	v_pk_fma_f32 v[178:179], v[170:171], v[178:179], s[28:29] op_sel_hi:[1,1,0]
	v_pk_fma_f32 v[180:181], v[172:173], v[180:181], s[28:29] op_sel_hi:[1,1,0]
	v_pk_fma_f32 v[182:183], v[174:175], v[182:183], s[28:29] op_sel_hi:[1,1,0]
	v_pk_fma_f32 v[176:177], v[168:169], v[176:177], s[30:31] op_sel_hi:[1,1,0]
	v_pk_fma_f32 v[178:179], v[170:171], v[178:179], s[30:31] op_sel_hi:[1,1,0]
	v_pk_fma_f32 v[180:181], v[172:173], v[180:181], s[30:31] op_sel_hi:[1,1,0]
	v_pk_fma_f32 v[182:183], v[174:175], v[182:183], s[30:31] op_sel_hi:[1,1,0]
	v_pk_fma_f32 v[176:177], v[168:169], v[176:177], s[34:35] op_sel_hi:[1,1,0]
	v_pk_fma_f32 v[178:179], v[170:171], v[178:179], s[34:35] op_sel_hi:[1,1,0]
	v_pk_fma_f32 v[180:181], v[172:173], v[180:181], s[34:35] op_sel_hi:[1,1,0]
	v_pk_fma_f32 v[182:183], v[174:175], v[182:183], s[34:35] op_sel_hi:[1,1,0]
	v_pk_fma_f32 v[176:177], v[168:169], v[176:177], s[36:37] op_sel_hi:[1,1,0]
	v_pk_fma_f32 v[178:179], v[170:171], v[178:179], s[36:37] op_sel_hi:[1,1,0]
	v_pk_fma_f32 v[180:181], v[172:173], v[180:181], s[36:37] op_sel_hi:[1,1,0]
	v_pk_fma_f32 v[182:183], v[174:175], v[182:183], s[36:37] op_sel_hi:[1,1,0]
	v_pk_fma_f32 v[176:177], v[168:169], v[176:177], s[38:39] op_sel_hi:[1,1,0]
	v_pk_fma_f32 v[178:179], v[170:171], v[178:179], s[38:39] op_sel_hi:[1,1,0]
	v_pk_fma_f32 v[180:181], v[172:173], v[180:181], s[38:39] op_sel_hi:[1,1,0]
	v_pk_fma_f32 v[182:183], v[174:175], v[182:183], s[38:39] op_sel_hi:[1,1,0]
	v_pk_fma_f32 v[176:177], v[168:169], v[176:177], s[40:41] op_sel_hi:[1,1,0]
	v_pk_fma_f32 v[178:179], v[170:171], v[178:179], s[40:41] op_sel_hi:[1,1,0]
	v_pk_fma_f32 v[180:181], v[172:173], v[180:181], s[40:41] op_sel_hi:[1,1,0]
	v_pk_fma_f32 v[182:183], v[174:175], v[182:183], s[40:41] op_sel_hi:[1,1,0]
	v_pk_fma_f32 v[176:177], v[168:169], v[176:177], s[42:43] op_sel_hi:[1,1,0]
	v_pk_fma_f32 v[178:179], v[170:171], v[178:179], s[42:43] op_sel_hi:[1,1,0]
	v_pk_fma_f32 v[180:181], v[172:173], v[180:181], s[42:43] op_sel_hi:[1,1,0]
	v_pk_fma_f32 v[182:183], v[174:175], v[182:183], s[42:43] op_sel_hi:[1,1,0]
	v_pk_fma_f32 v[176:177], v[168:169], v[176:177], s[44:45] op_sel_hi:[1,1,0]
	v_pk_fma_f32 v[178:179], v[170:171], v[178:179], s[44:45] op_sel_hi:[1,1,0]
	v_pk_fma_f32 v[180:181], v[172:173], v[180:181], s[44:45] op_sel_hi:[1,1,0]
	v_pk_fma_f32 v[182:183], v[174:175], v[182:183], s[44:45] op_sel_hi:[1,1,0]
	v_pk_fma_f32 v[168:169], v[168:169], v[176:177], s[48:49] op_sel_hi:[1,1,0]
	v_pk_fma_f32 v[170:171], v[170:171], v[178:179], s[48:49] op_sel_hi:[1,1,0]
	v_pk_fma_f32 v[172:173], v[172:173], v[180:181], s[48:49] op_sel_hi:[1,1,0]
	v_pk_fma_f32 v[174:175], v[174:175], v[182:183], s[48:49] op_sel_hi:[1,1,0]
	v_pk_fma_f32 v[160:161], v[160:161], v[168:169], 0.5 op_sel_hi:[1,1,0]
	v_pk_fma_f32 v[162:163], v[162:163], v[170:171], 0.5 op_sel_hi:[1,1,0]
	v_pk_fma_f32 v[164:165], v[164:165], v[172:173], 0.5 op_sel_hi:[1,1,0]
	v_pk_fma_f32 v[166:167], v[166:167], v[174:175], 0.5 op_sel_hi:[1,1,0]
	v_pk_mul_f32 v[92:93], v[92:93], v[160:161]
	v_pk_mul_f32 v[94:95], v[94:95], v[162:163]
	v_pk_mul_f32 v[88:89], v[88:89], v[164:165]
	v_pk_mul_f32 v[90:91], v[90:91], v[166:167]
	v_cvt_pk_bf16_f32 v184, v92, v93
	v_cvt_pk_bf16_f32 v185, v94, v95
	v_cvt_pk_bf16_f32 v186, v88, v89
	v_cvt_pk_bf16_f32 v187, v90, v91
	global_store_dwordx4 v[196:197], v[184:187], off
	v_pk_add_f32 v[84:85], v[84:85], v[60:61]
	v_pk_add_f32 v[86:87], v[86:87], v[62:63]
	v_pk_add_f32 v[80:81], v[80:81], v[56:57]
	v_pk_add_f32 v[82:83], v[82:83], v[58:59]
	v_med3_f32 v160, v84, s78, v158
	v_med3_f32 v161, v85, s78, v158
	v_med3_f32 v162, v86, s78, v158
	v_med3_f32 v163, v87, s78, v158
	v_med3_f32 v164, v80, s78, v158
	v_med3_f32 v165, v81, s78, v158
	v_med3_f32 v166, v82, s78, v158
	v_med3_f32 v167, v83, s78, v158
	v_pk_mul_f32 v[168:169], v[160:161], v[160:161]
	v_pk_mul_f32 v[170:171], v[162:163], v[162:163]
	v_pk_mul_f32 v[172:173], v[164:165], v[164:165]
	v_pk_mul_f32 v[174:175], v[166:167], v[166:167]
	v_pk_fma_f32 v[168:169], v[168:169], s[20:21], -1.0 op_sel_hi:[1,0,0]
	v_pk_fma_f32 v[170:171], v[170:171], s[20:21], -1.0 op_sel_hi:[1,0,0]
	v_pk_fma_f32 v[172:173], v[172:173], s[20:21], -1.0 op_sel_hi:[1,0,0]
	v_pk_fma_f32 v[174:175], v[174:175], s[20:21], -1.0 op_sel_hi:[1,0,0]
	v_pk_fma_f32 v[176:177], v[168:169], s[22:23], v[150:151] op_sel_hi:[1,0,0] neg_lo:[1,0,0] neg_hi:[1,0,0]
	v_pk_fma_f32 v[178:179], v[170:171], s[22:23], v[150:151] op_sel_hi:[1,0,0] neg_lo:[1,0,0] neg_hi:[1,0,0]
	v_pk_fma_f32 v[180:181], v[172:173], s[22:23], v[150:151] op_sel_hi:[1,0,0] neg_lo:[1,0,0] neg_hi:[1,0,0]
	v_pk_fma_f32 v[182:183], v[174:175], s[22:23], v[150:151] op_sel_hi:[1,0,0] neg_lo:[1,0,0] neg_hi:[1,0,0]
	v_pk_fma_f32 v[176:177], v[168:169], v[176:177], s[26:27] op_sel_hi:[1,1,0]
	v_pk_fma_f32 v[178:179], v[170:171], v[178:179], s[26:27] op_sel_hi:[1,1,0]
	v_pk_fma_f32 v[180:181], v[172:173], v[180:181], s[26:27] op_sel_hi:[1,1,0]
	v_pk_fma_f32 v[182:183], v[174:175], v[182:183], s[26:27] op_sel_hi:[1,1,0]
	v_pk_fma_f32 v[176:177], v[168:169], v[176:177], s[28:29] op_sel_hi:[1,1,0]
	v_pk_fma_f32 v[178:179], v[170:171], v[178:179], s[28:29] op_sel_hi:[1,1,0]
	v_pk_fma_f32 v[180:181], v[172:173], v[180:181], s[28:29] op_sel_hi:[1,1,0]
	v_pk_fma_f32 v[182:183], v[174:175], v[182:183], s[28:29] op_sel_hi:[1,1,0]
	v_pk_fma_f32 v[176:177], v[168:169], v[176:177], s[30:31] op_sel_hi:[1,1,0]
	v_pk_fma_f32 v[178:179], v[170:171], v[178:179], s[30:31] op_sel_hi:[1,1,0]
	v_pk_fma_f32 v[180:181], v[172:173], v[180:181], s[30:31] op_sel_hi:[1,1,0]
	v_pk_fma_f32 v[182:183], v[174:175], v[182:183], s[30:31] op_sel_hi:[1,1,0]
	v_pk_fma_f32 v[176:177], v[168:169], v[176:177], s[34:35] op_sel_hi:[1,1,0]
	v_pk_fma_f32 v[178:179], v[170:171], v[178:179], s[34:35] op_sel_hi:[1,1,0]
	v_pk_fma_f32 v[180:181], v[172:173], v[180:181], s[34:35] op_sel_hi:[1,1,0]
	v_pk_fma_f32 v[182:183], v[174:175], v[182:183], s[34:35] op_sel_hi:[1,1,0]
	v_pk_fma_f32 v[176:177], v[168:169], v[176:177], s[36:37] op_sel_hi:[1,1,0]
	v_pk_fma_f32 v[178:179], v[170:171], v[178:179], s[36:37] op_sel_hi:[1,1,0]
	v_pk_fma_f32 v[180:181], v[172:173], v[180:181], s[36:37] op_sel_hi:[1,1,0]
	v_pk_fma_f32 v[182:183], v[174:175], v[182:183], s[36:37] op_sel_hi:[1,1,0]
	v_pk_fma_f32 v[176:177], v[168:169], v[176:177], s[38:39] op_sel_hi:[1,1,0]
	v_pk_fma_f32 v[178:179], v[170:171], v[178:179], s[38:39] op_sel_hi:[1,1,0]
	v_pk_fma_f32 v[180:181], v[172:173], v[180:181], s[38:39] op_sel_hi:[1,1,0]
	v_pk_fma_f32 v[182:183], v[174:175], v[182:183], s[38:39] op_sel_hi:[1,1,0]
	v_pk_fma_f32 v[176:177], v[168:169], v[176:177], s[40:41] op_sel_hi:[1,1,0]
	v_pk_fma_f32 v[178:179], v[170:171], v[178:179], s[40:41] op_sel_hi:[1,1,0]
	v_pk_fma_f32 v[180:181], v[172:173], v[180:181], s[40:41] op_sel_hi:[1,1,0]
	v_pk_fma_f32 v[182:183], v[174:175], v[182:183], s[40:41] op_sel_hi:[1,1,0]
	v_pk_fma_f32 v[176:177], v[168:169], v[176:177], s[42:43] op_sel_hi:[1,1,0]
	v_pk_fma_f32 v[178:179], v[170:171], v[178:179], s[42:43] op_sel_hi:[1,1,0]
	v_pk_fma_f32 v[180:181], v[172:173], v[180:181], s[42:43] op_sel_hi:[1,1,0]
	v_pk_fma_f32 v[182:183], v[174:175], v[182:183], s[42:43] op_sel_hi:[1,1,0]
	v_pk_fma_f32 v[176:177], v[168:169], v[176:177], s[44:45] op_sel_hi:[1,1,0]
	v_pk_fma_f32 v[178:179], v[170:171], v[178:179], s[44:45] op_sel_hi:[1,1,0]
	v_pk_fma_f32 v[180:181], v[172:173], v[180:181], s[44:45] op_sel_hi:[1,1,0]
	v_pk_fma_f32 v[182:183], v[174:175], v[182:183], s[44:45] op_sel_hi:[1,1,0]
	v_pk_fma_f32 v[168:169], v[168:169], v[176:177], s[48:49] op_sel_hi:[1,1,0]
	v_pk_fma_f32 v[170:171], v[170:171], v[178:179], s[48:49] op_sel_hi:[1,1,0]
	v_pk_fma_f32 v[172:173], v[172:173], v[180:181], s[48:49] op_sel_hi:[1,1,0]
	v_pk_fma_f32 v[174:175], v[174:175], v[182:183], s[48:49] op_sel_hi:[1,1,0]
	v_pk_fma_f32 v[160:161], v[160:161], v[168:169], 0.5 op_sel_hi:[1,1,0]
	v_pk_fma_f32 v[162:163], v[162:163], v[170:171], 0.5 op_sel_hi:[1,1,0]
	v_pk_fma_f32 v[164:165], v[164:165], v[172:173], 0.5 op_sel_hi:[1,1,0]
	v_pk_fma_f32 v[166:167], v[166:167], v[174:175], 0.5 op_sel_hi:[1,1,0]
	v_pk_mul_f32 v[84:85], v[84:85], v[160:161]
	v_pk_mul_f32 v[86:87], v[86:87], v[162:163]
	v_pk_mul_f32 v[80:81], v[80:81], v[164:165]
	v_pk_mul_f32 v[82:83], v[82:83], v[166:167]
	v_cvt_pk_bf16_f32 v188, v84, v85
	v_cvt_pk_bf16_f32 v189, v86, v87
	v_cvt_pk_bf16_f32 v190, v80, v81
	v_cvt_pk_bf16_f32 v191, v82, v83
	global_store_dwordx4 v[196:197], v[188:191], off offset:256
	s_and_b64 vcc, exec, s[70:71]
	s_cbranch_vccz .Lg9_nostat_3
	v_pk_mul_f32 v[168:169], v[92:93], v[92:93]
	v_pk_mul_f32 v[170:171], v[94:95], v[94:95]
	v_pk_mul_f32 v[172:173], v[88:89], v[88:89]
	v_pk_mul_f32 v[174:175], v[90:91], v[90:91]
	v_pk_mul_f32 v[176:177], v[84:85], v[84:85]
	v_pk_mul_f32 v[178:179], v[86:87], v[86:87]
	v_pk_mul_f32 v[180:181], v[80:81], v[80:81]
	v_pk_mul_f32 v[182:183], v[82:83], v[82:83]
	v_add_f32_e32 v160, v92, v93
	v_add_f32_e32 v161, v94, v95
	v_add_f32_e32 v162, v88, v89
	v_add_f32_e32 v163, v90, v91
	v_add_f32_e32 v164, v84, v85
	v_add_f32_e32 v165, v86, v87
	v_add_f32_e32 v166, v80, v81
	v_add_f32_e32 v167, v82, v83
	v_add_f32_e32 v160, v160, v161
	v_add_f32_e32 v164, v164, v165
	v_add_f32_e32 v160, v160, v162
	v_add_f32_e32 v164, v164, v166
	v_add_f32_e32 v160, v160, v163
	v_add_f32_e32 v164, v164, v167
	v_add_f32_e32 v168, v168, v169
	v_add_f32_e32 v170, v170, v171
	v_add_f32_e32 v172, v172, v173
	v_add_f32_e32 v174, v174, v175
	v_add_f32_e32 v176, v176, v177
	v_add_f32_e32 v178, v178, v179
	v_add_f32_e32 v180, v180, v181
	v_add_f32_e32 v182, v182, v183
	v_add_f32_e32 v198, v160, v164
	v_add_f32_e32 v168, v168, v170
	v_add_f32_e32 v176, v176, v178
	v_mov_b32_e32 v199, v198
	v_add_f32_e32 v168, v168, v172
	v_add_f32_e32 v176, v176, v180
	s_nop 1
	v_permlane16_swap_b32 v199, v198
	s_nop 1
	v_add_f32_e32 v168, v168, v174
	v_add_f32_e32 v176, v176, v182
	v_add_f32_e32 v198, v199, v198
	v_add_f32_e32 v200, v168, v176
	v_mov_b32_e32 v202, v198
	v_mov_b32_e32 v201, v200
	s_nop 1
	v_permlane32_swap_b32 v202, v198
	s_nop 1
	s_nop 1
	v_permlane16_swap_b32 v201, v200
	s_nop 1
	v_add_f32_e32 v199, v201, v200
	v_mov_b32_e32 v203, v199
	s_nop 1
	v_permlane32_swap_b32 v203, v199
	s_nop 1
	s_and_saveexec_b64 s[4:5], s[6:7]
	v_lshlrev_b64 v[194:195], 8, v[192:193]
	v_lshl_add_u64 v[194:195], s[16:17], 0, v[194:195]
	v_lshl_add_u64 v[194:195], s[68:69], 3, v[194:195]
	v_pk_add_f32 v[200:201], v[202:203], v[198:199]
	global_store_dwordx2 v[194:195], v[200:201], off
	s_or_b64 exec, exec, s[4:5]
.Lg9_nostat_3:
	v_add_u32_e32 v192, 0x80, v148
	v_ashrrev_i32_e32 v193, 31, v192
	v_lshlrev_b64 v[194:195], 12, v[192:193]
	v_lshl_add_u64 v[196:197], v[146:147], 0, v[194:195]
	v_pk_add_f32 v[72:73], v[72:73], v[76:77]
	v_pk_add_f32 v[74:75], v[74:75], v[78:79]
	v_pk_add_f32 v[64:65], v[64:65], v[68:69]
	v_pk_add_f32 v[66:67], v[66:67], v[70:71]
	v_med3_f32 v160, v72, s78, v158
	v_med3_f32 v161, v73, s78, v158
	v_med3_f32 v162, v74, s78, v158
	v_med3_f32 v163, v75, s78, v158
	v_med3_f32 v164, v64, s78, v158
	v_med3_f32 v165, v65, s78, v158
	v_med3_f32 v166, v66, s78, v158
	v_med3_f32 v167, v67, s78, v158
	v_pk_mul_f32 v[168:169], v[160:161], v[160:161]
	v_pk_mul_f32 v[170:171], v[162:163], v[162:163]
	v_pk_mul_f32 v[172:173], v[164:165], v[164:165]
	v_pk_mul_f32 v[174:175], v[166:167], v[166:167]
	v_pk_fma_f32 v[168:169], v[168:169], s[20:21], -1.0 op_sel_hi:[1,0,0]
	v_pk_fma_f32 v[170:171], v[170:171], s[20:21], -1.0 op_sel_hi:[1,0,0]
	v_pk_fma_f32 v[172:173], v[172:173], s[20:21], -1.0 op_sel_hi:[1,0,0]
	v_pk_fma_f32 v[174:175], v[174:175], s[20:21], -1.0 op_sel_hi:[1,0,0]
	v_pk_fma_f32 v[176:177], v[168:169], s[22:23], v[150:151] op_sel_hi:[1,0,0] neg_lo:[1,0,0] neg_hi:[1,0,0]
	v_pk_fma_f32 v[178:179], v[170:171], s[22:23], v[150:151] op_sel_hi:[1,0,0] neg_lo:[1,0,0] neg_hi:[1,0,0]
	v_pk_fma_f32 v[180:181], v[172:173], s[22:23], v[150:151] op_sel_hi:[1,0,0] neg_lo:[1,0,0] neg_hi:[1,0,0]
	v_pk_fma_f32 v[182:183], v[174:175], s[22:23], v[150:151] op_sel_hi:[1,0,0] neg_lo:[1,0,0] neg_hi:[1,0,0]
	v_pk_fma_f32 v[176:177], v[168:169], v[176:177], s[26:27] op_sel_hi:[1,1,0]
	v_pk_fma_f32 v[178:179], v[170:171], v[178:179], s[26:27] op_sel_hi:[1,1,0]
	v_pk_fma_f32 v[180:181], v[172:173], v[180:181], s[26:27] op_sel_hi:[1,1,0]
	v_pk_fma_f32 v[182:183], v[174:175], v[182:183], s[26:27] op_sel_hi:[1,1,0]
	v_pk_fma_f32 v[176:177], v[168:169], v[176:177], s[28:29] op_sel_hi:[1,1,0]
	v_pk_fma_f32 v[178:179], v[170:171], v[178:179], s[28:29] op_sel_hi:[1,1,0]
	v_pk_fma_f32 v[180:181], v[172:173], v[180:181], s[28:29] op_sel_hi:[1,1,0]
	v_pk_fma_f32 v[182:183], v[174:175], v[182:183], s[28:29] op_sel_hi:[1,1,0]
	v_pk_fma_f32 v[176:177], v[168:169], v[176:177], s[30:31] op_sel_hi:[1,1,0]
	v_pk_fma_f32 v[178:179], v[170:171], v[178:179], s[30:31] op_sel_hi:[1,1,0]
	v_pk_fma_f32 v[180:181], v[172:173], v[180:181], s[30:31] op_sel_hi:[1,1,0]
	v_pk_fma_f32 v[182:183], v[174:175], v[182:183], s[30:31] op_sel_hi:[1,1,0]
	v_pk_fma_f32 v[176:177], v[168:169], v[176:177], s[34:35] op_sel_hi:[1,1,0]
	v_pk_fma_f32 v[178:179], v[170:171], v[178:179], s[34:35] op_sel_hi:[1,1,0]
	v_pk_fma_f32 v[180:181], v[172:173], v[180:181], s[34:35] op_sel_hi:[1,1,0]
	v_pk_fma_f32 v[182:183], v[174:175], v[182:183], s[34:35] op_sel_hi:[1,1,0]
	v_pk_fma_f32 v[176:177], v[168:169], v[176:177], s[36:37] op_sel_hi:[1,1,0]
	v_pk_fma_f32 v[178:179], v[170:171], v[178:179], s[36:37] op_sel_hi:[1,1,0]
	v_pk_fma_f32 v[180:181], v[172:173], v[180:181], s[36:37] op_sel_hi:[1,1,0]
	v_pk_fma_f32 v[182:183], v[174:175], v[182:183], s[36:37] op_sel_hi:[1,1,0]
	v_pk_fma_f32 v[176:177], v[168:169], v[176:177], s[38:39] op_sel_hi:[1,1,0]
	v_pk_fma_f32 v[178:179], v[170:171], v[178:179], s[38:39] op_sel_hi:[1,1,0]
	v_pk_fma_f32 v[180:181], v[172:173], v[180:181], s[38:39] op_sel_hi:[1,1,0]
	v_pk_fma_f32 v[182:183], v[174:175], v[182:183], s[38:39] op_sel_hi:[1,1,0]
	v_pk_fma_f32 v[176:177], v[168:169], v[176:177], s[40:41] op_sel_hi:[1,1,0]
	v_pk_fma_f32 v[178:179], v[170:171], v[178:179], s[40:41] op_sel_hi:[1,1,0]
	v_pk_fma_f32 v[180:181], v[172:173], v[180:181], s[40:41] op_sel_hi:[1,1,0]
	v_pk_fma_f32 v[182:183], v[174:175], v[182:183], s[40:41] op_sel_hi:[1,1,0]
	v_pk_fma_f32 v[176:177], v[168:169], v[176:177], s[42:43] op_sel_hi:[1,1,0]
	v_pk_fma_f32 v[178:179], v[170:171], v[178:179], s[42:43] op_sel_hi:[1,1,0]
	v_pk_fma_f32 v[180:181], v[172:173], v[180:181], s[42:43] op_sel_hi:[1,1,0]
	v_pk_fma_f32 v[182:183], v[174:175], v[182:183], s[42:43] op_sel_hi:[1,1,0]
	v_pk_fma_f32 v[176:177], v[168:169], v[176:177], s[44:45] op_sel_hi:[1,1,0]
	v_pk_fma_f32 v[178:179], v[170:171], v[178:179], s[44:45] op_sel_hi:[1,1,0]
	v_pk_fma_f32 v[180:181], v[172:173], v[180:181], s[44:45] op_sel_hi:[1,1,0]
	v_pk_fma_f32 v[182:183], v[174:175], v[182:183], s[44:45] op_sel_hi:[1,1,0]
	v_pk_fma_f32 v[168:169], v[168:169], v[176:177], s[48:49] op_sel_hi:[1,1,0]
	v_pk_fma_f32 v[170:171], v[170:171], v[178:179], s[48:49] op_sel_hi:[1,1,0]
	v_pk_fma_f32 v[172:173], v[172:173], v[180:181], s[48:49] op_sel_hi:[1,1,0]
	v_pk_fma_f32 v[174:175], v[174:175], v[182:183], s[48:49] op_sel_hi:[1,1,0]
	v_pk_fma_f32 v[160:161], v[160:161], v[168:169], 0.5 op_sel_hi:[1,1,0]
	v_pk_fma_f32 v[162:163], v[162:163], v[170:171], 0.5 op_sel_hi:[1,1,0]
	v_pk_fma_f32 v[164:165], v[164:165], v[172:173], 0.5 op_sel_hi:[1,1,0]
	v_pk_fma_f32 v[166:167], v[166:167], v[174:175], 0.5 op_sel_hi:[1,1,0]
	v_pk_mul_f32 v[72:73], v[72:73], v[160:161]
	v_pk_mul_f32 v[74:75], v[74:75], v[162:163]
	v_pk_mul_f32 v[64:65], v[64:65], v[164:165]
	v_pk_mul_f32 v[66:67], v[66:67], v[166:167]
	v_cvt_pk_bf16_f32 v184, v72, v73
	v_cvt_pk_bf16_f32 v185, v74, v75
	v_cvt_pk_bf16_f32 v186, v64, v65
	v_cvt_pk_bf16_f32 v187, v66, v67
	global_store_dwordx4 v[196:197], v[184:187], off
	v_pk_add_f32 v[52:53], v[52:53], v[60:61]
	v_pk_add_f32 v[54:55], v[54:55], v[62:63]
	v_pk_add_f32 v[48:49], v[48:49], v[56:57]
	v_pk_add_f32 v[50:51], v[50:51], v[58:59]
	v_med3_f32 v160, v52, s78, v158
	v_med3_f32 v161, v53, s78, v158
	v_med3_f32 v162, v54, s78, v158
	v_med3_f32 v163, v55, s78, v158
	v_med3_f32 v164, v48, s78, v158
	v_med3_f32 v165, v49, s78, v158
	v_med3_f32 v166, v50, s78, v158
	v_med3_f32 v167, v51, s78, v158
	v_pk_mul_f32 v[168:169], v[160:161], v[160:161]
	v_pk_mul_f32 v[170:171], v[162:163], v[162:163]
	v_pk_mul_f32 v[172:173], v[164:165], v[164:165]
	v_pk_mul_f32 v[174:175], v[166:167], v[166:167]
	v_pk_fma_f32 v[168:169], v[168:169], s[20:21], -1.0 op_sel_hi:[1,0,0]
	v_pk_fma_f32 v[170:171], v[170:171], s[20:21], -1.0 op_sel_hi:[1,0,0]
	v_pk_fma_f32 v[172:173], v[172:173], s[20:21], -1.0 op_sel_hi:[1,0,0]
	v_pk_fma_f32 v[174:175], v[174:175], s[20:21], -1.0 op_sel_hi:[1,0,0]
	v_pk_fma_f32 v[176:177], v[168:169], s[22:23], v[150:151] op_sel_hi:[1,0,0] neg_lo:[1,0,0] neg_hi:[1,0,0]
	v_pk_fma_f32 v[178:179], v[170:171], s[22:23], v[150:151] op_sel_hi:[1,0,0] neg_lo:[1,0,0] neg_hi:[1,0,0]
	v_pk_fma_f32 v[180:181], v[172:173], s[22:23], v[150:151] op_sel_hi:[1,0,0] neg_lo:[1,0,0] neg_hi:[1,0,0]
	v_pk_fma_f32 v[182:183], v[174:175], s[22:23], v[150:151] op_sel_hi:[1,0,0] neg_lo:[1,0,0] neg_hi:[1,0,0]
	v_pk_fma_f32 v[176:177], v[168:169], v[176:177], s[26:27] op_sel_hi:[1,1,0]
	v_pk_fma_f32 v[178:179], v[170:171], v[178:179], s[26:27] op_sel_hi:[1,1,0]
	v_pk_fma_f32 v[180:181], v[172:173], v[180:181], s[26:27] op_sel_hi:[1,1,0]
	v_pk_fma_f32 v[182:183], v[174:175], v[182:183], s[26:27] op_sel_hi:[1,1,0]
	v_pk_fma_f32 v[176:177], v[168:169], v[176:177], s[28:29] op_sel_hi:[1,1,0]
	v_pk_fma_f32 v[178:179], v[170:171], v[178:179], s[28:29] op_sel_hi:[1,1,0]
	v_pk_fma_f32 v[180:181], v[172:173], v[180:181], s[28:29] op_sel_hi:[1,1,0]
	v_pk_fma_f32 v[182:183], v[174:175], v[182:183], s[28:29] op_sel_hi:[1,1,0]
	v_pk_fma_f32 v[176:177], v[168:169], v[176:177], s[30:31] op_sel_hi:[1,1,0]
	v_pk_fma_f32 v[178:179], v[170:171], v[178:179], s[30:31] op_sel_hi:[1,1,0]
	v_pk_fma_f32 v[180:181], v[172:173], v[180:181], s[30:31] op_sel_hi:[1,1,0]
	v_pk_fma_f32 v[182:183], v[174:175], v[182:183], s[30:31] op_sel_hi:[1,1,0]
	v_pk_fma_f32 v[176:177], v[168:169], v[176:177], s[34:35] op_sel_hi:[1,1,0]
	v_pk_fma_f32 v[178:179], v[170:171], v[178:179], s[34:35] op_sel_hi:[1,1,0]
	v_pk_fma_f32 v[180:181], v[172:173], v[180:181], s[34:35] op_sel_hi:[1,1,0]
	v_pk_fma_f32 v[182:183], v[174:175], v[182:183], s[34:35] op_sel_hi:[1,1,0]
	v_pk_fma_f32 v[176:177], v[168:169], v[176:177], s[36:37] op_sel_hi:[1,1,0]
	v_pk_fma_f32 v[178:179], v[170:171], v[178:179], s[36:37] op_sel_hi:[1,1,0]
	v_pk_fma_f32 v[180:181], v[172:173], v[180:181], s[36:37] op_sel_hi:[1,1,0]
	v_pk_fma_f32 v[182:183], v[174:175], v[182:183], s[36:37] op_sel_hi:[1,1,0]
	v_pk_fma_f32 v[176:177], v[168:169], v[176:177], s[38:39] op_sel_hi:[1,1,0]
	v_pk_fma_f32 v[178:179], v[170:171], v[178:179], s[38:39] op_sel_hi:[1,1,0]
	v_pk_fma_f32 v[180:181], v[172:173], v[180:181], s[38:39] op_sel_hi:[1,1,0]
	v_pk_fma_f32 v[182:183], v[174:175], v[182:183], s[38:39] op_sel_hi:[1,1,0]
	v_pk_fma_f32 v[176:177], v[168:169], v[176:177], s[40:41] op_sel_hi:[1,1,0]
	v_pk_fma_f32 v[178:179], v[170:171], v[178:179], s[40:41] op_sel_hi:[1,1,0]
	v_pk_fma_f32 v[180:181], v[172:173], v[180:181], s[40:41] op_sel_hi:[1,1,0]
	v_pk_fma_f32 v[182:183], v[174:175], v[182:183], s[40:41] op_sel_hi:[1,1,0]
	v_pk_fma_f32 v[176:177], v[168:169], v[176:177], s[42:43] op_sel_hi:[1,1,0]
	v_pk_fma_f32 v[178:179], v[170:171], v[178:179], s[42:43] op_sel_hi:[1,1,0]
	v_pk_fma_f32 v[180:181], v[172:173], v[180:181], s[42:43] op_sel_hi:[1,1,0]
	v_pk_fma_f32 v[182:183], v[174:175], v[182:183], s[42:43] op_sel_hi:[1,1,0]
	v_pk_fma_f32 v[176:177], v[168:169], v[176:177], s[44:45] op_sel_hi:[1,1,0]
	v_pk_fma_f32 v[178:179], v[170:171], v[178:179], s[44:45] op_sel_hi:[1,1,0]
	v_pk_fma_f32 v[180:181], v[172:173], v[180:181], s[44:45] op_sel_hi:[1,1,0]
	v_pk_fma_f32 v[182:183], v[174:175], v[182:183], s[44:45] op_sel_hi:[1,1,0]
	v_pk_fma_f32 v[168:169], v[168:169], v[176:177], s[48:49] op_sel_hi:[1,1,0]
	v_pk_fma_f32 v[170:171], v[170:171], v[178:179], s[48:49] op_sel_hi:[1,1,0]
	v_pk_fma_f32 v[172:173], v[172:173], v[180:181], s[48:49] op_sel_hi:[1,1,0]
	v_pk_fma_f32 v[174:175], v[174:175], v[182:183], s[48:49] op_sel_hi:[1,1,0]
	v_pk_fma_f32 v[160:161], v[160:161], v[168:169], 0.5 op_sel_hi:[1,1,0]
	v_pk_fma_f32 v[162:163], v[162:163], v[170:171], 0.5 op_sel_hi:[1,1,0]
	v_pk_fma_f32 v[164:165], v[164:165], v[172:173], 0.5 op_sel_hi:[1,1,0]
	v_pk_fma_f32 v[166:167], v[166:167], v[174:175], 0.5 op_sel_hi:[1,1,0]
	v_pk_mul_f32 v[52:53], v[52:53], v[160:161]
	v_pk_mul_f32 v[54:55], v[54:55], v[162:163]
	v_pk_mul_f32 v[48:49], v[48:49], v[164:165]
	v_pk_mul_f32 v[50:51], v[50:51], v[166:167]
	v_cvt_pk_bf16_f32 v188, v52, v53
	v_cvt_pk_bf16_f32 v189, v54, v55
	v_cvt_pk_bf16_f32 v190, v48, v49
	v_cvt_pk_bf16_f32 v191, v50, v51
	global_store_dwordx4 v[196:197], v[188:191], off offset:256
	s_and_b64 vcc, exec, s[70:71]
	s_cbranch_vccz .Lg9_nostat_4
	v_pk_mul_f32 v[168:169], v[72:73], v[72:73]
	v_pk_mul_f32 v[170:171], v[74:75], v[74:75]
	v_pk_mul_f32 v[172:173], v[64:65], v[64:65]
	v_pk_mul_f32 v[174:175], v[66:67], v[66:67]
	v_pk_mul_f32 v[176:177], v[52:53], v[52:53]
	v_pk_mul_f32 v[178:179], v[54:55], v[54:55]
	v_pk_mul_f32 v[180:181], v[48:49], v[48:49]
	v_pk_mul_f32 v[182:183], v[50:51], v[50:51]
	v_add_f32_e32 v160, v72, v73
	v_add_f32_e32 v161, v74, v75
	v_add_f32_e32 v162, v64, v65
	v_add_f32_e32 v163, v66, v67
	v_add_f32_e32 v164, v52, v53
	v_add_f32_e32 v165, v54, v55
	v_add_f32_e32 v166, v48, v49
	v_add_f32_e32 v167, v50, v51
	v_add_f32_e32 v160, v160, v161
	v_add_f32_e32 v164, v164, v165
	v_add_f32_e32 v160, v160, v162
	v_add_f32_e32 v164, v164, v166
	v_add_f32_e32 v160, v160, v163
	v_add_f32_e32 v164, v164, v167
	v_add_f32_e32 v168, v168, v169
	v_add_f32_e32 v170, v170, v171
	v_add_f32_e32 v172, v172, v173
	v_add_f32_e32 v174, v174, v175
	v_add_f32_e32 v176, v176, v177
	v_add_f32_e32 v178, v178, v179
	v_add_f32_e32 v180, v180, v181
	v_add_f32_e32 v182, v182, v183
	v_add_f32_e32 v198, v160, v164
	v_add_f32_e32 v168, v168, v170
	v_add_f32_e32 v176, v176, v178
	v_mov_b32_e32 v199, v198
	v_add_f32_e32 v168, v168, v172
	v_add_f32_e32 v176, v176, v180
	s_nop 1
	v_permlane16_swap_b32 v199, v198
	s_nop 1
	v_add_f32_e32 v168, v168, v174
	v_add_f32_e32 v176, v176, v182
	v_add_f32_e32 v198, v199, v198
	v_add_f32_e32 v200, v168, v176
	v_mov_b32_e32 v202, v198
	v_mov_b32_e32 v201, v200
	s_nop 1
	v_permlane32_swap_b32 v202, v198
	s_nop 1
	s_nop 1
	v_permlane16_swap_b32 v201, v200
	s_nop 1
	v_add_f32_e32 v199, v201, v200
	v_mov_b32_e32 v203, v199
	s_nop 1
	v_permlane32_swap_b32 v203, v199
	s_nop 1
	s_and_saveexec_b64 s[4:5], s[6:7]
	v_lshlrev_b64 v[194:195], 8, v[192:193]
	v_lshl_add_u64 v[194:195], s[16:17], 0, v[194:195]
	v_lshl_add_u64 v[194:195], s[68:69], 3, v[194:195]
	v_pk_add_f32 v[200:201], v[202:203], v[198:199]
	global_store_dwordx2 v[194:195], v[200:201], off
	s_or_b64 exec, exec, s[4:5]
.Lg9_nostat_4:
	v_add_u32_e32 v192, 0x90, v148
	v_ashrrev_i32_e32 v193, 31, v192
	v_lshlrev_b64 v[194:195], 12, v[192:193]
	v_lshl_add_u64 v[196:197], v[146:147], 0, v[194:195]
	v_pk_add_f32 v[44:45], v[44:45], v[76:77]
	v_pk_add_f32 v[46:47], v[46:47], v[78:79]
	v_pk_add_f32 v[40:41], v[40:41], v[68:69]
	v_pk_add_f32 v[42:43], v[42:43], v[70:71]
	v_med3_f32 v160, v44, s78, v158
	v_med3_f32 v161, v45, s78, v158
	v_med3_f32 v162, v46, s78, v158
	v_med3_f32 v163, v47, s78, v158
	v_med3_f32 v164, v40, s78, v158
	v_med3_f32 v165, v41, s78, v158
	v_med3_f32 v166, v42, s78, v158
	v_med3_f32 v167, v43, s78, v158
	v_pk_mul_f32 v[168:169], v[160:161], v[160:161]
	v_pk_mul_f32 v[170:171], v[162:163], v[162:163]
	v_pk_mul_f32 v[172:173], v[164:165], v[164:165]
	v_pk_mul_f32 v[174:175], v[166:167], v[166:167]
	v_pk_fma_f32 v[168:169], v[168:169], s[20:21], -1.0 op_sel_hi:[1,0,0]
	v_pk_fma_f32 v[170:171], v[170:171], s[20:21], -1.0 op_sel_hi:[1,0,0]
	v_pk_fma_f32 v[172:173], v[172:173], s[20:21], -1.0 op_sel_hi:[1,0,0]
	v_pk_fma_f32 v[174:175], v[174:175], s[20:21], -1.0 op_sel_hi:[1,0,0]
	v_pk_fma_f32 v[176:177], v[168:169], s[22:23], v[150:151] op_sel_hi:[1,0,0] neg_lo:[1,0,0] neg_hi:[1,0,0]
	v_pk_fma_f32 v[178:179], v[170:171], s[22:23], v[150:151] op_sel_hi:[1,0,0] neg_lo:[1,0,0] neg_hi:[1,0,0]
	v_pk_fma_f32 v[180:181], v[172:173], s[22:23], v[150:151] op_sel_hi:[1,0,0] neg_lo:[1,0,0] neg_hi:[1,0,0]
	v_pk_fma_f32 v[182:183], v[174:175], s[22:23], v[150:151] op_sel_hi:[1,0,0] neg_lo:[1,0,0] neg_hi:[1,0,0]
	v_pk_fma_f32 v[176:177], v[168:169], v[176:177], s[26:27] op_sel_hi:[1,1,0]
	v_pk_fma_f32 v[178:179], v[170:171], v[178:179], s[26:27] op_sel_hi:[1,1,0]
	v_pk_fma_f32 v[180:181], v[172:173], v[180:181], s[26:27] op_sel_hi:[1,1,0]
	v_pk_fma_f32 v[182:183], v[174:175], v[182:183], s[26:27] op_sel_hi:[1,1,0]
	v_pk_fma_f32 v[176:177], v[168:169], v[176:177], s[28:29] op_sel_hi:[1,1,0]
	v_pk_fma_f32 v[178:179], v[170:171], v[178:179], s[28:29] op_sel_hi:[1,1,0]
	v_pk_fma_f32 v[180:181], v[172:173], v[180:181], s[28:29] op_sel_hi:[1,1,0]
	v_pk_fma_f32 v[182:183], v[174:175], v[182:183], s[28:29] op_sel_hi:[1,1,0]
	v_pk_fma_f32 v[176:177], v[168:169], v[176:177], s[30:31] op_sel_hi:[1,1,0]
	v_pk_fma_f32 v[178:179], v[170:171], v[178:179], s[30:31] op_sel_hi:[1,1,0]
	v_pk_fma_f32 v[180:181], v[172:173], v[180:181], s[30:31] op_sel_hi:[1,1,0]
	v_pk_fma_f32 v[182:183], v[174:175], v[182:183], s[30:31] op_sel_hi:[1,1,0]
	v_pk_fma_f32 v[176:177], v[168:169], v[176:177], s[34:35] op_sel_hi:[1,1,0]
	v_pk_fma_f32 v[178:179], v[170:171], v[178:179], s[34:35] op_sel_hi:[1,1,0]
	v_pk_fma_f32 v[180:181], v[172:173], v[180:181], s[34:35] op_sel_hi:[1,1,0]
	v_pk_fma_f32 v[182:183], v[174:175], v[182:183], s[34:35] op_sel_hi:[1,1,0]
	v_pk_fma_f32 v[176:177], v[168:169], v[176:177], s[36:37] op_sel_hi:[1,1,0]
	v_pk_fma_f32 v[178:179], v[170:171], v[178:179], s[36:37] op_sel_hi:[1,1,0]
	v_pk_fma_f32 v[180:181], v[172:173], v[180:181], s[36:37] op_sel_hi:[1,1,0]
	v_pk_fma_f32 v[182:183], v[174:175], v[182:183], s[36:37] op_sel_hi:[1,1,0]
	v_pk_fma_f32 v[176:177], v[168:169], v[176:177], s[38:39] op_sel_hi:[1,1,0]
	v_pk_fma_f32 v[178:179], v[170:171], v[178:179], s[38:39] op_sel_hi:[1,1,0]
	v_pk_fma_f32 v[180:181], v[172:173], v[180:181], s[38:39] op_sel_hi:[1,1,0]
	v_pk_fma_f32 v[182:183], v[174:175], v[182:183], s[38:39] op_sel_hi:[1,1,0]
	v_pk_fma_f32 v[176:177], v[168:169], v[176:177], s[40:41] op_sel_hi:[1,1,0]
	v_pk_fma_f32 v[178:179], v[170:171], v[178:179], s[40:41] op_sel_hi:[1,1,0]
	v_pk_fma_f32 v[180:181], v[172:173], v[180:181], s[40:41] op_sel_hi:[1,1,0]
	v_pk_fma_f32 v[182:183], v[174:175], v[182:183], s[40:41] op_sel_hi:[1,1,0]
	v_pk_fma_f32 v[176:177], v[168:169], v[176:177], s[42:43] op_sel_hi:[1,1,0]
	v_pk_fma_f32 v[178:179], v[170:171], v[178:179], s[42:43] op_sel_hi:[1,1,0]
	v_pk_fma_f32 v[180:181], v[172:173], v[180:181], s[42:43] op_sel_hi:[1,1,0]
	v_pk_fma_f32 v[182:183], v[174:175], v[182:183], s[42:43] op_sel_hi:[1,1,0]
	v_pk_fma_f32 v[176:177], v[168:169], v[176:177], s[44:45] op_sel_hi:[1,1,0]
	v_pk_fma_f32 v[178:179], v[170:171], v[178:179], s[44:45] op_sel_hi:[1,1,0]
	v_pk_fma_f32 v[180:181], v[172:173], v[180:181], s[44:45] op_sel_hi:[1,1,0]
	v_pk_fma_f32 v[182:183], v[174:175], v[182:183], s[44:45] op_sel_hi:[1,1,0]
	v_pk_fma_f32 v[168:169], v[168:169], v[176:177], s[48:49] op_sel_hi:[1,1,0]
	v_pk_fma_f32 v[170:171], v[170:171], v[178:179], s[48:49] op_sel_hi:[1,1,0]
	v_pk_fma_f32 v[172:173], v[172:173], v[180:181], s[48:49] op_sel_hi:[1,1,0]
	v_pk_fma_f32 v[174:175], v[174:175], v[182:183], s[48:49] op_sel_hi:[1,1,0]
	v_pk_fma_f32 v[160:161], v[160:161], v[168:169], 0.5 op_sel_hi:[1,1,0]
	v_pk_fma_f32 v[162:163], v[162:163], v[170:171], 0.5 op_sel_hi:[1,1,0]
	v_pk_fma_f32 v[164:165], v[164:165], v[172:173], 0.5 op_sel_hi:[1,1,0]
	v_pk_fma_f32 v[166:167], v[166:167], v[174:175], 0.5 op_sel_hi:[1,1,0]
	v_pk_mul_f32 v[44:45], v[44:45], v[160:161]
	v_pk_mul_f32 v[46:47], v[46:47], v[162:163]
	v_pk_mul_f32 v[40:41], v[40:41], v[164:165]
	v_pk_mul_f32 v[42:43], v[42:43], v[166:167]
	v_cvt_pk_bf16_f32 v184, v44, v45
	v_cvt_pk_bf16_f32 v185, v46, v47
	v_cvt_pk_bf16_f32 v186, v40, v41
	v_cvt_pk_bf16_f32 v187, v42, v43
	global_store_dwordx4 v[196:197], v[184:187], off
	v_pk_add_f32 v[36:37], v[36:37], v[60:61]
	v_pk_add_f32 v[38:39], v[38:39], v[62:63]
	v_pk_add_f32 v[32:33], v[32:33], v[56:57]
	v_pk_add_f32 v[34:35], v[34:35], v[58:59]
	v_med3_f32 v160, v36, s78, v158
	v_med3_f32 v161, v37, s78, v158
	v_med3_f32 v162, v38, s78, v158
	v_med3_f32 v163, v39, s78, v158
	v_med3_f32 v164, v32, s78, v158
	v_med3_f32 v165, v33, s78, v158
	v_med3_f32 v166, v34, s78, v158
	v_med3_f32 v167, v35, s78, v158
	v_pk_mul_f32 v[168:169], v[160:161], v[160:161]
	v_pk_mul_f32 v[170:171], v[162:163], v[162:163]
	v_pk_mul_f32 v[172:173], v[164:165], v[164:165]
	v_pk_mul_f32 v[174:175], v[166:167], v[166:167]
	v_pk_fma_f32 v[168:169], v[168:169], s[20:21], -1.0 op_sel_hi:[1,0,0]
	v_pk_fma_f32 v[170:171], v[170:171], s[20:21], -1.0 op_sel_hi:[1,0,0]
	v_pk_fma_f32 v[172:173], v[172:173], s[20:21], -1.0 op_sel_hi:[1,0,0]
	v_pk_fma_f32 v[174:175], v[174:175], s[20:21], -1.0 op_sel_hi:[1,0,0]
	v_pk_fma_f32 v[176:177], v[168:169], s[22:23], v[150:151] op_sel_hi:[1,0,0] neg_lo:[1,0,0] neg_hi:[1,0,0]
	v_pk_fma_f32 v[178:179], v[170:171], s[22:23], v[150:151] op_sel_hi:[1,0,0] neg_lo:[1,0,0] neg_hi:[1,0,0]
	v_pk_fma_f32 v[180:181], v[172:173], s[22:23], v[150:151] op_sel_hi:[1,0,0] neg_lo:[1,0,0] neg_hi:[1,0,0]
	v_pk_fma_f32 v[182:183], v[174:175], s[22:23], v[150:151] op_sel_hi:[1,0,0] neg_lo:[1,0,0] neg_hi:[1,0,0]
	v_pk_fma_f32 v[176:177], v[168:169], v[176:177], s[26:27] op_sel_hi:[1,1,0]
	v_pk_fma_f32 v[178:179], v[170:171], v[178:179], s[26:27] op_sel_hi:[1,1,0]
	v_pk_fma_f32 v[180:181], v[172:173], v[180:181], s[26:27] op_sel_hi:[1,1,0]
	v_pk_fma_f32 v[182:183], v[174:175], v[182:183], s[26:27] op_sel_hi:[1,1,0]
	v_pk_fma_f32 v[176:177], v[168:169], v[176:177], s[28:29] op_sel_hi:[1,1,0]
	v_pk_fma_f32 v[178:179], v[170:171], v[178:179], s[28:29] op_sel_hi:[1,1,0]
	v_pk_fma_f32 v[180:181], v[172:173], v[180:181], s[28:29] op_sel_hi:[1,1,0]
	v_pk_fma_f32 v[182:183], v[174:175], v[182:183], s[28:29] op_sel_hi:[1,1,0]
	v_pk_fma_f32 v[176:177], v[168:169], v[176:177], s[30:31] op_sel_hi:[1,1,0]
	v_pk_fma_f32 v[178:179], v[170:171], v[178:179], s[30:31] op_sel_hi:[1,1,0]
	v_pk_fma_f32 v[180:181], v[172:173], v[180:181], s[30:31] op_sel_hi:[1,1,0]
	v_pk_fma_f32 v[182:183], v[174:175], v[182:183], s[30:31] op_sel_hi:[1,1,0]
	v_pk_fma_f32 v[176:177], v[168:169], v[176:177], s[34:35] op_sel_hi:[1,1,0]
	v_pk_fma_f32 v[178:179], v[170:171], v[178:179], s[34:35] op_sel_hi:[1,1,0]
	v_pk_fma_f32 v[180:181], v[172:173], v[180:181], s[34:35] op_sel_hi:[1,1,0]
	v_pk_fma_f32 v[182:183], v[174:175], v[182:183], s[34:35] op_sel_hi:[1,1,0]
	v_pk_fma_f32 v[176:177], v[168:169], v[176:177], s[36:37] op_sel_hi:[1,1,0]
	v_pk_fma_f32 v[178:179], v[170:171], v[178:179], s[36:37] op_sel_hi:[1,1,0]
	v_pk_fma_f32 v[180:181], v[172:173], v[180:181], s[36:37] op_sel_hi:[1,1,0]
	v_pk_fma_f32 v[182:183], v[174:175], v[182:183], s[36:37] op_sel_hi:[1,1,0]
	v_pk_fma_f32 v[176:177], v[168:169], v[176:177], s[38:39] op_sel_hi:[1,1,0]
	v_pk_fma_f32 v[178:179], v[170:171], v[178:179], s[38:39] op_sel_hi:[1,1,0]
	v_pk_fma_f32 v[180:181], v[172:173], v[180:181], s[38:39] op_sel_hi:[1,1,0]
	v_pk_fma_f32 v[182:183], v[174:175], v[182:183], s[38:39] op_sel_hi:[1,1,0]
	v_pk_fma_f32 v[176:177], v[168:169], v[176:177], s[40:41] op_sel_hi:[1,1,0]
	v_pk_fma_f32 v[178:179], v[170:171], v[178:179], s[40:41] op_sel_hi:[1,1,0]
	v_pk_fma_f32 v[180:181], v[172:173], v[180:181], s[40:41] op_sel_hi:[1,1,0]
	v_pk_fma_f32 v[182:183], v[174:175], v[182:183], s[40:41] op_sel_hi:[1,1,0]
	v_pk_fma_f32 v[176:177], v[168:169], v[176:177], s[42:43] op_sel_hi:[1,1,0]
	v_pk_fma_f32 v[178:179], v[170:171], v[178:179], s[42:43] op_sel_hi:[1,1,0]
	v_pk_fma_f32 v[180:181], v[172:173], v[180:181], s[42:43] op_sel_hi:[1,1,0]
	v_pk_fma_f32 v[182:183], v[174:175], v[182:183], s[42:43] op_sel_hi:[1,1,0]
	v_pk_fma_f32 v[176:177], v[168:169], v[176:177], s[44:45] op_sel_hi:[1,1,0]
	v_pk_fma_f32 v[178:179], v[170:171], v[178:179], s[44:45] op_sel_hi:[1,1,0]
	v_pk_fma_f32 v[180:181], v[172:173], v[180:181], s[44:45] op_sel_hi:[1,1,0]
	v_pk_fma_f32 v[182:183], v[174:175], v[182:183], s[44:45] op_sel_hi:[1,1,0]
	v_pk_fma_f32 v[168:169], v[168:169], v[176:177], s[48:49] op_sel_hi:[1,1,0]
	v_pk_fma_f32 v[170:171], v[170:171], v[178:179], s[48:49] op_sel_hi:[1,1,0]
	v_pk_fma_f32 v[172:173], v[172:173], v[180:181], s[48:49] op_sel_hi:[1,1,0]
	v_pk_fma_f32 v[174:175], v[174:175], v[182:183], s[48:49] op_sel_hi:[1,1,0]
	v_pk_fma_f32 v[160:161], v[160:161], v[168:169], 0.5 op_sel_hi:[1,1,0]
	v_pk_fma_f32 v[162:163], v[162:163], v[170:171], 0.5 op_sel_hi:[1,1,0]
	v_pk_fma_f32 v[164:165], v[164:165], v[172:173], 0.5 op_sel_hi:[1,1,0]
	v_pk_fma_f32 v[166:167], v[166:167], v[174:175], 0.5 op_sel_hi:[1,1,0]
	v_pk_mul_f32 v[36:37], v[36:37], v[160:161]
	v_pk_mul_f32 v[38:39], v[38:39], v[162:163]
	v_pk_mul_f32 v[32:33], v[32:33], v[164:165]
	v_pk_mul_f32 v[34:35], v[34:35], v[166:167]
	v_cvt_pk_bf16_f32 v188, v36, v37
	v_cvt_pk_bf16_f32 v189, v38, v39
	v_cvt_pk_bf16_f32 v190, v32, v33
	v_cvt_pk_bf16_f32 v191, v34, v35
	global_store_dwordx4 v[196:197], v[188:191], off offset:256
	s_and_b64 vcc, exec, s[70:71]
	s_cbranch_vccz .Lg9_nostat_5
	v_pk_mul_f32 v[168:169], v[44:45], v[44:45]
	v_pk_mul_f32 v[170:171], v[46:47], v[46:47]
	v_pk_mul_f32 v[172:173], v[40:41], v[40:41]
	v_pk_mul_f32 v[174:175], v[42:43], v[42:43]
	v_pk_mul_f32 v[176:177], v[36:37], v[36:37]
	v_pk_mul_f32 v[178:179], v[38:39], v[38:39]
	v_pk_mul_f32 v[180:181], v[32:33], v[32:33]
	v_pk_mul_f32 v[182:183], v[34:35], v[34:35]
	v_add_f32_e32 v160, v44, v45
	v_add_f32_e32 v161, v46, v47
	v_add_f32_e32 v162, v40, v41
	v_add_f32_e32 v163, v42, v43
	v_add_f32_e32 v164, v36, v37
	v_add_f32_e32 v165, v38, v39
	v_add_f32_e32 v166, v32, v33
	v_add_f32_e32 v167, v34, v35
	v_add_f32_e32 v160, v160, v161
	v_add_f32_e32 v164, v164, v165
	v_add_f32_e32 v160, v160, v162
	v_add_f32_e32 v164, v164, v166
	v_add_f32_e32 v160, v160, v163
	v_add_f32_e32 v164, v164, v167
	v_add_f32_e32 v168, v168, v169
	v_add_f32_e32 v170, v170, v171
	v_add_f32_e32 v172, v172, v173
	v_add_f32_e32 v174, v174, v175
	v_add_f32_e32 v176, v176, v177
	v_add_f32_e32 v178, v178, v179
	v_add_f32_e32 v180, v180, v181
	v_add_f32_e32 v182, v182, v183
	v_add_f32_e32 v198, v160, v164
	v_add_f32_e32 v168, v168, v170
	v_add_f32_e32 v176, v176, v178
	v_mov_b32_e32 v199, v198
	v_add_f32_e32 v168, v168, v172
	v_add_f32_e32 v176, v176, v180
	s_nop 1
	v_permlane16_swap_b32 v199, v198
	s_nop 1
	v_add_f32_e32 v168, v168, v174
	v_add_f32_e32 v176, v176, v182
	v_add_f32_e32 v198, v199, v198
	v_add_f32_e32 v200, v168, v176
	v_mov_b32_e32 v202, v198
	v_mov_b32_e32 v201, v200
	s_nop 1
	v_permlane32_swap_b32 v202, v198
	s_nop 1
	s_nop 1
	v_permlane16_swap_b32 v201, v200
	s_nop 1
	v_add_f32_e32 v199, v201, v200
	v_mov_b32_e32 v203, v199
	s_nop 1
	v_permlane32_swap_b32 v203, v199
	s_nop 1
	s_and_saveexec_b64 s[4:5], s[6:7]
	v_lshlrev_b64 v[194:195], 8, v[192:193]
	v_lshl_add_u64 v[194:195], s[16:17], 0, v[194:195]
	v_lshl_add_u64 v[194:195], s[68:69], 3, v[194:195]
	v_pk_add_f32 v[200:201], v[202:203], v[198:199]
	global_store_dwordx2 v[194:195], v[200:201], off
	s_or_b64 exec, exec, s[4:5]
.Lg9_nostat_5:
	v_add_u32_e32 v192, 0xa0, v148
	v_ashrrev_i32_e32 v193, 31, v192
	v_lshlrev_b64 v[194:195], 12, v[192:193]
	v_lshl_add_u64 v[196:197], v[146:147], 0, v[194:195]
	v_pk_add_f32 v[28:29], v[28:29], v[76:77]
	v_pk_add_f32 v[30:31], v[30:31], v[78:79]
	v_pk_add_f32 v[24:25], v[24:25], v[68:69]
	v_pk_add_f32 v[26:27], v[26:27], v[70:71]
	v_med3_f32 v160, v28, s78, v158
	v_med3_f32 v161, v29, s78, v158
	v_med3_f32 v162, v30, s78, v158
	v_med3_f32 v163, v31, s78, v158
	v_med3_f32 v164, v24, s78, v158
	v_med3_f32 v165, v25, s78, v158
	v_med3_f32 v166, v26, s78, v158
	v_med3_f32 v167, v27, s78, v158
	v_pk_mul_f32 v[168:169], v[160:161], v[160:161]
	v_pk_mul_f32 v[170:171], v[162:163], v[162:163]
	v_pk_mul_f32 v[172:173], v[164:165], v[164:165]
	v_pk_mul_f32 v[174:175], v[166:167], v[166:167]
	v_pk_fma_f32 v[168:169], v[168:169], s[20:21], -1.0 op_sel_hi:[1,0,0]
	v_pk_fma_f32 v[170:171], v[170:171], s[20:21], -1.0 op_sel_hi:[1,0,0]
	v_pk_fma_f32 v[172:173], v[172:173], s[20:21], -1.0 op_sel_hi:[1,0,0]
	v_pk_fma_f32 v[174:175], v[174:175], s[20:21], -1.0 op_sel_hi:[1,0,0]
	v_pk_fma_f32 v[176:177], v[168:169], s[22:23], v[150:151] op_sel_hi:[1,0,0] neg_lo:[1,0,0] neg_hi:[1,0,0]
	v_pk_fma_f32 v[178:179], v[170:171], s[22:23], v[150:151] op_sel_hi:[1,0,0] neg_lo:[1,0,0] neg_hi:[1,0,0]
	v_pk_fma_f32 v[180:181], v[172:173], s[22:23], v[150:151] op_sel_hi:[1,0,0] neg_lo:[1,0,0] neg_hi:[1,0,0]
	v_pk_fma_f32 v[182:183], v[174:175], s[22:23], v[150:151] op_sel_hi:[1,0,0] neg_lo:[1,0,0] neg_hi:[1,0,0]
	v_pk_fma_f32 v[176:177], v[168:169], v[176:177], s[26:27] op_sel_hi:[1,1,0]
	v_pk_fma_f32 v[178:179], v[170:171], v[178:179], s[26:27] op_sel_hi:[1,1,0]
	v_pk_fma_f32 v[180:181], v[172:173], v[180:181], s[26:27] op_sel_hi:[1,1,0]
	v_pk_fma_f32 v[182:183], v[174:175], v[182:183], s[26:27] op_sel_hi:[1,1,0]
	v_pk_fma_f32 v[176:177], v[168:169], v[176:177], s[28:29] op_sel_hi:[1,1,0]
	v_pk_fma_f32 v[178:179], v[170:171], v[178:179], s[28:29] op_sel_hi:[1,1,0]
	v_pk_fma_f32 v[180:181], v[172:173], v[180:181], s[28:29] op_sel_hi:[1,1,0]
	v_pk_fma_f32 v[182:183], v[174:175], v[182:183], s[28:29] op_sel_hi:[1,1,0]
	v_pk_fma_f32 v[176:177], v[168:169], v[176:177], s[30:31] op_sel_hi:[1,1,0]
	v_pk_fma_f32 v[178:179], v[170:171], v[178:179], s[30:31] op_sel_hi:[1,1,0]
	v_pk_fma_f32 v[180:181], v[172:173], v[180:181], s[30:31] op_sel_hi:[1,1,0]
	v_pk_fma_f32 v[182:183], v[174:175], v[182:183], s[30:31] op_sel_hi:[1,1,0]
	v_pk_fma_f32 v[176:177], v[168:169], v[176:177], s[34:35] op_sel_hi:[1,1,0]
	v_pk_fma_f32 v[178:179], v[170:171], v[178:179], s[34:35] op_sel_hi:[1,1,0]
	v_pk_fma_f32 v[180:181], v[172:173], v[180:181], s[34:35] op_sel_hi:[1,1,0]
	v_pk_fma_f32 v[182:183], v[174:175], v[182:183], s[34:35] op_sel_hi:[1,1,0]
	v_pk_fma_f32 v[176:177], v[168:169], v[176:177], s[36:37] op_sel_hi:[1,1,0]
	v_pk_fma_f32 v[178:179], v[170:171], v[178:179], s[36:37] op_sel_hi:[1,1,0]
	v_pk_fma_f32 v[180:181], v[172:173], v[180:181], s[36:37] op_sel_hi:[1,1,0]
	v_pk_fma_f32 v[182:183], v[174:175], v[182:183], s[36:37] op_sel_hi:[1,1,0]
	v_pk_fma_f32 v[176:177], v[168:169], v[176:177], s[38:39] op_sel_hi:[1,1,0]
	v_pk_fma_f32 v[178:179], v[170:171], v[178:179], s[38:39] op_sel_hi:[1,1,0]
	v_pk_fma_f32 v[180:181], v[172:173], v[180:181], s[38:39] op_sel_hi:[1,1,0]
	v_pk_fma_f32 v[182:183], v[174:175], v[182:183], s[38:39] op_sel_hi:[1,1,0]
	v_pk_fma_f32 v[176:177], v[168:169], v[176:177], s[40:41] op_sel_hi:[1,1,0]
	v_pk_fma_f32 v[178:179], v[170:171], v[178:179], s[40:41] op_sel_hi:[1,1,0]
	v_pk_fma_f32 v[180:181], v[172:173], v[180:181], s[40:41] op_sel_hi:[1,1,0]
	v_pk_fma_f32 v[182:183], v[174:175], v[182:183], s[40:41] op_sel_hi:[1,1,0]
	v_pk_fma_f32 v[176:177], v[168:169], v[176:177], s[42:43] op_sel_hi:[1,1,0]
	v_pk_fma_f32 v[178:179], v[170:171], v[178:179], s[42:43] op_sel_hi:[1,1,0]
	v_pk_fma_f32 v[180:181], v[172:173], v[180:181], s[42:43] op_sel_hi:[1,1,0]
	v_pk_fma_f32 v[182:183], v[174:175], v[182:183], s[42:43] op_sel_hi:[1,1,0]
	v_pk_fma_f32 v[176:177], v[168:169], v[176:177], s[44:45] op_sel_hi:[1,1,0]
	v_pk_fma_f32 v[178:179], v[170:171], v[178:179], s[44:45] op_sel_hi:[1,1,0]
	v_pk_fma_f32 v[180:181], v[172:173], v[180:181], s[44:45] op_sel_hi:[1,1,0]
	v_pk_fma_f32 v[182:183], v[174:175], v[182:183], s[44:45] op_sel_hi:[1,1,0]
	v_pk_fma_f32 v[168:169], v[168:169], v[176:177], s[48:49] op_sel_hi:[1,1,0]
	v_pk_fma_f32 v[170:171], v[170:171], v[178:179], s[48:49] op_sel_hi:[1,1,0]
	v_pk_fma_f32 v[172:173], v[172:173], v[180:181], s[48:49] op_sel_hi:[1,1,0]
	v_pk_fma_f32 v[174:175], v[174:175], v[182:183], s[48:49] op_sel_hi:[1,1,0]
	v_pk_fma_f32 v[160:161], v[160:161], v[168:169], 0.5 op_sel_hi:[1,1,0]
	v_pk_fma_f32 v[162:163], v[162:163], v[170:171], 0.5 op_sel_hi:[1,1,0]
	v_pk_fma_f32 v[164:165], v[164:165], v[172:173], 0.5 op_sel_hi:[1,1,0]
	v_pk_fma_f32 v[166:167], v[166:167], v[174:175], 0.5 op_sel_hi:[1,1,0]
	v_pk_mul_f32 v[28:29], v[28:29], v[160:161]
	v_pk_mul_f32 v[30:31], v[30:31], v[162:163]
	v_pk_mul_f32 v[24:25], v[24:25], v[164:165]
	v_pk_mul_f32 v[26:27], v[26:27], v[166:167]
	v_cvt_pk_bf16_f32 v184, v28, v29
	v_cvt_pk_bf16_f32 v185, v30, v31
	v_cvt_pk_bf16_f32 v186, v24, v25
	v_cvt_pk_bf16_f32 v187, v26, v27
	global_store_dwordx4 v[196:197], v[184:187], off
	v_pk_add_f32 v[20:21], v[20:21], v[60:61]
	v_pk_add_f32 v[22:23], v[22:23], v[62:63]
	v_pk_add_f32 v[16:17], v[16:17], v[56:57]
	v_pk_add_f32 v[18:19], v[18:19], v[58:59]
	v_med3_f32 v160, v20, s78, v158
	v_med3_f32 v161, v21, s78, v158
	v_med3_f32 v162, v22, s78, v158
	v_med3_f32 v163, v23, s78, v158
	v_med3_f32 v164, v16, s78, v158
	v_med3_f32 v165, v17, s78, v158
	v_med3_f32 v166, v18, s78, v158
	v_med3_f32 v167, v19, s78, v158
	v_pk_mul_f32 v[168:169], v[160:161], v[160:161]
	v_pk_mul_f32 v[170:171], v[162:163], v[162:163]
	v_pk_mul_f32 v[172:173], v[164:165], v[164:165]
	v_pk_mul_f32 v[174:175], v[166:167], v[166:167]
	v_pk_fma_f32 v[168:169], v[168:169], s[20:21], -1.0 op_sel_hi:[1,0,0]
	v_pk_fma_f32 v[170:171], v[170:171], s[20:21], -1.0 op_sel_hi:[1,0,0]
	v_pk_fma_f32 v[172:173], v[172:173], s[20:21], -1.0 op_sel_hi:[1,0,0]
	v_pk_fma_f32 v[174:175], v[174:175], s[20:21], -1.0 op_sel_hi:[1,0,0]
	v_pk_fma_f32 v[176:177], v[168:169], s[22:23], v[150:151] op_sel_hi:[1,0,0] neg_lo:[1,0,0] neg_hi:[1,0,0]
	v_pk_fma_f32 v[178:179], v[170:171], s[22:23], v[150:151] op_sel_hi:[1,0,0] neg_lo:[1,0,0] neg_hi:[1,0,0]
	v_pk_fma_f32 v[180:181], v[172:173], s[22:23], v[150:151] op_sel_hi:[1,0,0] neg_lo:[1,0,0] neg_hi:[1,0,0]
	v_pk_fma_f32 v[182:183], v[174:175], s[22:23], v[150:151] op_sel_hi:[1,0,0] neg_lo:[1,0,0] neg_hi:[1,0,0]
	v_pk_fma_f32 v[176:177], v[168:169], v[176:177], s[26:27] op_sel_hi:[1,1,0]
	v_pk_fma_f32 v[178:179], v[170:171], v[178:179], s[26:27] op_sel_hi:[1,1,0]
	v_pk_fma_f32 v[180:181], v[172:173], v[180:181], s[26:27] op_sel_hi:[1,1,0]
	v_pk_fma_f32 v[182:183], v[174:175], v[182:183], s[26:27] op_sel_hi:[1,1,0]
	v_pk_fma_f32 v[176:177], v[168:169], v[176:177], s[28:29] op_sel_hi:[1,1,0]
	v_pk_fma_f32 v[178:179], v[170:171], v[178:179], s[28:29] op_sel_hi:[1,1,0]
	v_pk_fma_f32 v[180:181], v[172:173], v[180:181], s[28:29] op_sel_hi:[1,1,0]
	v_pk_fma_f32 v[182:183], v[174:175], v[182:183], s[28:29] op_sel_hi:[1,1,0]
	v_pk_fma_f32 v[176:177], v[168:169], v[176:177], s[30:31] op_sel_hi:[1,1,0]
	v_pk_fma_f32 v[178:179], v[170:171], v[178:179], s[30:31] op_sel_hi:[1,1,0]
	v_pk_fma_f32 v[180:181], v[172:173], v[180:181], s[30:31] op_sel_hi:[1,1,0]
	v_pk_fma_f32 v[182:183], v[174:175], v[182:183], s[30:31] op_sel_hi:[1,1,0]
	v_pk_fma_f32 v[176:177], v[168:169], v[176:177], s[34:35] op_sel_hi:[1,1,0]
	v_pk_fma_f32 v[178:179], v[170:171], v[178:179], s[34:35] op_sel_hi:[1,1,0]
	v_pk_fma_f32 v[180:181], v[172:173], v[180:181], s[34:35] op_sel_hi:[1,1,0]
	v_pk_fma_f32 v[182:183], v[174:175], v[182:183], s[34:35] op_sel_hi:[1,1,0]
	v_pk_fma_f32 v[176:177], v[168:169], v[176:177], s[36:37] op_sel_hi:[1,1,0]
	v_pk_fma_f32 v[178:179], v[170:171], v[178:179], s[36:37] op_sel_hi:[1,1,0]
	v_pk_fma_f32 v[180:181], v[172:173], v[180:181], s[36:37] op_sel_hi:[1,1,0]
	v_pk_fma_f32 v[182:183], v[174:175], v[182:183], s[36:37] op_sel_hi:[1,1,0]
	v_pk_fma_f32 v[176:177], v[168:169], v[176:177], s[38:39] op_sel_hi:[1,1,0]
	v_pk_fma_f32 v[178:179], v[170:171], v[178:179], s[38:39] op_sel_hi:[1,1,0]
	v_pk_fma_f32 v[180:181], v[172:173], v[180:181], s[38:39] op_sel_hi:[1,1,0]
	v_pk_fma_f32 v[182:183], v[174:175], v[182:183], s[38:39] op_sel_hi:[1,1,0]
	v_pk_fma_f32 v[176:177], v[168:169], v[176:177], s[40:41] op_sel_hi:[1,1,0]
	v_pk_fma_f32 v[178:179], v[170:171], v[178:179], s[40:41] op_sel_hi:[1,1,0]
	v_pk_fma_f32 v[180:181], v[172:173], v[180:181], s[40:41] op_sel_hi:[1,1,0]
	v_pk_fma_f32 v[182:183], v[174:175], v[182:183], s[40:41] op_sel_hi:[1,1,0]
	v_pk_fma_f32 v[176:177], v[168:169], v[176:177], s[42:43] op_sel_hi:[1,1,0]
	v_pk_fma_f32 v[178:179], v[170:171], v[178:179], s[42:43] op_sel_hi:[1,1,0]
	v_pk_fma_f32 v[180:181], v[172:173], v[180:181], s[42:43] op_sel_hi:[1,1,0]
	v_pk_fma_f32 v[182:183], v[174:175], v[182:183], s[42:43] op_sel_hi:[1,1,0]
	v_pk_fma_f32 v[176:177], v[168:169], v[176:177], s[44:45] op_sel_hi:[1,1,0]
	v_pk_fma_f32 v[178:179], v[170:171], v[178:179], s[44:45] op_sel_hi:[1,1,0]
	v_pk_fma_f32 v[180:181], v[172:173], v[180:181], s[44:45] op_sel_hi:[1,1,0]
	v_pk_fma_f32 v[182:183], v[174:175], v[182:183], s[44:45] op_sel_hi:[1,1,0]
	v_pk_fma_f32 v[168:169], v[168:169], v[176:177], s[48:49] op_sel_hi:[1,1,0]
	v_pk_fma_f32 v[170:171], v[170:171], v[178:179], s[48:49] op_sel_hi:[1,1,0]
	v_pk_fma_f32 v[172:173], v[172:173], v[180:181], s[48:49] op_sel_hi:[1,1,0]
	v_pk_fma_f32 v[174:175], v[174:175], v[182:183], s[48:49] op_sel_hi:[1,1,0]
	v_pk_fma_f32 v[160:161], v[160:161], v[168:169], 0.5 op_sel_hi:[1,1,0]
	v_pk_fma_f32 v[162:163], v[162:163], v[170:171], 0.5 op_sel_hi:[1,1,0]
	v_pk_fma_f32 v[164:165], v[164:165], v[172:173], 0.5 op_sel_hi:[1,1,0]
	v_pk_fma_f32 v[166:167], v[166:167], v[174:175], 0.5 op_sel_hi:[1,1,0]
	v_pk_mul_f32 v[20:21], v[20:21], v[160:161]
	v_pk_mul_f32 v[22:23], v[22:23], v[162:163]
	v_pk_mul_f32 v[16:17], v[16:17], v[164:165]
	v_pk_mul_f32 v[18:19], v[18:19], v[166:167]
	v_cvt_pk_bf16_f32 v188, v20, v21
	v_cvt_pk_bf16_f32 v189, v22, v23
	v_cvt_pk_bf16_f32 v190, v16, v17
	v_cvt_pk_bf16_f32 v191, v18, v19
	global_store_dwordx4 v[196:197], v[188:191], off offset:256
	s_and_b64 vcc, exec, s[70:71]
	s_cbranch_vccz .Lg9_nostat_6
	v_pk_mul_f32 v[168:169], v[28:29], v[28:29]
	v_pk_mul_f32 v[170:171], v[30:31], v[30:31]
	v_pk_mul_f32 v[172:173], v[24:25], v[24:25]
	v_pk_mul_f32 v[174:175], v[26:27], v[26:27]
	v_pk_mul_f32 v[176:177], v[20:21], v[20:21]
	v_pk_mul_f32 v[178:179], v[22:23], v[22:23]
	v_pk_mul_f32 v[180:181], v[16:17], v[16:17]
	v_pk_mul_f32 v[182:183], v[18:19], v[18:19]
	v_add_f32_e32 v160, v28, v29
	v_add_f32_e32 v161, v30, v31
	v_add_f32_e32 v162, v24, v25
	v_add_f32_e32 v163, v26, v27
	v_add_f32_e32 v164, v20, v21
	v_add_f32_e32 v165, v22, v23
	v_add_f32_e32 v166, v16, v17
	v_add_f32_e32 v167, v18, v19
	v_add_f32_e32 v160, v160, v161
	v_add_f32_e32 v164, v164, v165
	v_add_f32_e32 v160, v160, v162
	v_add_f32_e32 v164, v164, v166
	v_add_f32_e32 v160, v160, v163
	v_add_f32_e32 v164, v164, v167
	v_add_f32_e32 v168, v168, v169
	v_add_f32_e32 v170, v170, v171
	v_add_f32_e32 v172, v172, v173
	v_add_f32_e32 v174, v174, v175
	v_add_f32_e32 v176, v176, v177
	v_add_f32_e32 v178, v178, v179
	v_add_f32_e32 v180, v180, v181
	v_add_f32_e32 v182, v182, v183
	v_add_f32_e32 v198, v160, v164
	v_add_f32_e32 v168, v168, v170
	v_add_f32_e32 v176, v176, v178
	v_mov_b32_e32 v199, v198
	v_add_f32_e32 v168, v168, v172
	v_add_f32_e32 v176, v176, v180
	s_nop 1
	v_permlane16_swap_b32 v199, v198
	s_nop 1
	v_add_f32_e32 v168, v168, v174
	v_add_f32_e32 v176, v176, v182
	v_add_f32_e32 v198, v199, v198
	v_add_f32_e32 v200, v168, v176
	v_mov_b32_e32 v202, v198
	v_mov_b32_e32 v201, v200
	s_nop 1
	v_permlane32_swap_b32 v202, v198
	s_nop 1
	s_nop 1
	v_permlane16_swap_b32 v201, v200
	s_nop 1
	v_add_f32_e32 v199, v201, v200
	v_mov_b32_e32 v203, v199
	s_nop 1
	v_permlane32_swap_b32 v203, v199
	s_nop 1
	s_and_saveexec_b64 s[4:5], s[6:7]
	v_lshlrev_b64 v[194:195], 8, v[192:193]
	v_lshl_add_u64 v[194:195], s[16:17], 0, v[194:195]
	v_lshl_add_u64 v[194:195], s[68:69], 3, v[194:195]
	v_pk_add_f32 v[200:201], v[202:203], v[198:199]
	global_store_dwordx2 v[194:195], v[200:201], off
	s_or_b64 exec, exec, s[4:5]
.Lg9_nostat_6:
	v_add_u32_e32 v192, 0xb0, v148
	v_ashrrev_i32_e32 v193, 31, v192
	v_lshlrev_b64 v[194:195], 12, v[192:193]
	v_lshl_add_u64 v[196:197], v[146:147], 0, v[194:195]
	v_pk_add_f32 v[12:13], v[12:13], v[76:77]
	v_pk_add_f32 v[14:15], v[14:15], v[78:79]
	v_pk_add_f32 v[8:9], v[8:9], v[68:69]
	v_pk_add_f32 v[10:11], v[10:11], v[70:71]
	v_med3_f32 v160, v12, s78, v158
	v_med3_f32 v161, v13, s78, v158
	v_med3_f32 v162, v14, s78, v158
	v_med3_f32 v163, v15, s78, v158
	v_med3_f32 v164, v8, s78, v158
	v_med3_f32 v165, v9, s78, v158
	v_med3_f32 v166, v10, s78, v158
	v_med3_f32 v167, v11, s78, v158
	v_pk_mul_f32 v[168:169], v[160:161], v[160:161]
	v_pk_mul_f32 v[170:171], v[162:163], v[162:163]
	v_pk_mul_f32 v[172:173], v[164:165], v[164:165]
	v_pk_mul_f32 v[174:175], v[166:167], v[166:167]
	v_pk_fma_f32 v[168:169], v[168:169], s[20:21], -1.0 op_sel_hi:[1,0,0]
	v_pk_fma_f32 v[170:171], v[170:171], s[20:21], -1.0 op_sel_hi:[1,0,0]
	v_pk_fma_f32 v[172:173], v[172:173], s[20:21], -1.0 op_sel_hi:[1,0,0]
	v_pk_fma_f32 v[174:175], v[174:175], s[20:21], -1.0 op_sel_hi:[1,0,0]
	v_pk_fma_f32 v[176:177], v[168:169], s[22:23], v[150:151] op_sel_hi:[1,0,0] neg_lo:[1,0,0] neg_hi:[1,0,0]
	v_pk_fma_f32 v[178:179], v[170:171], s[22:23], v[150:151] op_sel_hi:[1,0,0] neg_lo:[1,0,0] neg_hi:[1,0,0]
	v_pk_fma_f32 v[180:181], v[172:173], s[22:23], v[150:151] op_sel_hi:[1,0,0] neg_lo:[1,0,0] neg_hi:[1,0,0]
	v_pk_fma_f32 v[182:183], v[174:175], s[22:23], v[150:151] op_sel_hi:[1,0,0] neg_lo:[1,0,0] neg_hi:[1,0,0]
	v_pk_fma_f32 v[176:177], v[168:169], v[176:177], s[26:27] op_sel_hi:[1,1,0]
	v_pk_fma_f32 v[178:179], v[170:171], v[178:179], s[26:27] op_sel_hi:[1,1,0]
	v_pk_fma_f32 v[180:181], v[172:173], v[180:181], s[26:27] op_sel_hi:[1,1,0]
	v_pk_fma_f32 v[182:183], v[174:175], v[182:183], s[26:27] op_sel_hi:[1,1,0]
	v_pk_fma_f32 v[176:177], v[168:169], v[176:177], s[28:29] op_sel_hi:[1,1,0]
	v_pk_fma_f32 v[178:179], v[170:171], v[178:179], s[28:29] op_sel_hi:[1,1,0]
	v_pk_fma_f32 v[180:181], v[172:173], v[180:181], s[28:29] op_sel_hi:[1,1,0]
	v_pk_fma_f32 v[182:183], v[174:175], v[182:183], s[28:29] op_sel_hi:[1,1,0]
	v_pk_fma_f32 v[176:177], v[168:169], v[176:177], s[30:31] op_sel_hi:[1,1,0]
	v_pk_fma_f32 v[178:179], v[170:171], v[178:179], s[30:31] op_sel_hi:[1,1,0]
	v_pk_fma_f32 v[180:181], v[172:173], v[180:181], s[30:31] op_sel_hi:[1,1,0]
	v_pk_fma_f32 v[182:183], v[174:175], v[182:183], s[30:31] op_sel_hi:[1,1,0]
	v_pk_fma_f32 v[176:177], v[168:169], v[176:177], s[34:35] op_sel_hi:[1,1,0]
	v_pk_fma_f32 v[178:179], v[170:171], v[178:179], s[34:35] op_sel_hi:[1,1,0]
	v_pk_fma_f32 v[180:181], v[172:173], v[180:181], s[34:35] op_sel_hi:[1,1,0]
	v_pk_fma_f32 v[182:183], v[174:175], v[182:183], s[34:35] op_sel_hi:[1,1,0]
	v_pk_fma_f32 v[176:177], v[168:169], v[176:177], s[36:37] op_sel_hi:[1,1,0]
	v_pk_fma_f32 v[178:179], v[170:171], v[178:179], s[36:37] op_sel_hi:[1,1,0]
	v_pk_fma_f32 v[180:181], v[172:173], v[180:181], s[36:37] op_sel_hi:[1,1,0]
	v_pk_fma_f32 v[182:183], v[174:175], v[182:183], s[36:37] op_sel_hi:[1,1,0]
	v_pk_fma_f32 v[176:177], v[168:169], v[176:177], s[38:39] op_sel_hi:[1,1,0]
	v_pk_fma_f32 v[178:179], v[170:171], v[178:179], s[38:39] op_sel_hi:[1,1,0]
	v_pk_fma_f32 v[180:181], v[172:173], v[180:181], s[38:39] op_sel_hi:[1,1,0]
	v_pk_fma_f32 v[182:183], v[174:175], v[182:183], s[38:39] op_sel_hi:[1,1,0]
	v_pk_fma_f32 v[176:177], v[168:169], v[176:177], s[40:41] op_sel_hi:[1,1,0]
	v_pk_fma_f32 v[178:179], v[170:171], v[178:179], s[40:41] op_sel_hi:[1,1,0]
	v_pk_fma_f32 v[180:181], v[172:173], v[180:181], s[40:41] op_sel_hi:[1,1,0]
	v_pk_fma_f32 v[182:183], v[174:175], v[182:183], s[40:41] op_sel_hi:[1,1,0]
	v_pk_fma_f32 v[176:177], v[168:169], v[176:177], s[42:43] op_sel_hi:[1,1,0]
	v_pk_fma_f32 v[178:179], v[170:171], v[178:179], s[42:43] op_sel_hi:[1,1,0]
	v_pk_fma_f32 v[180:181], v[172:173], v[180:181], s[42:43] op_sel_hi:[1,1,0]
	v_pk_fma_f32 v[182:183], v[174:175], v[182:183], s[42:43] op_sel_hi:[1,1,0]
	v_pk_fma_f32 v[176:177], v[168:169], v[176:177], s[44:45] op_sel_hi:[1,1,0]
	v_pk_fma_f32 v[178:179], v[170:171], v[178:179], s[44:45] op_sel_hi:[1,1,0]
	v_pk_fma_f32 v[180:181], v[172:173], v[180:181], s[44:45] op_sel_hi:[1,1,0]
	v_pk_fma_f32 v[182:183], v[174:175], v[182:183], s[44:45] op_sel_hi:[1,1,0]
	v_pk_fma_f32 v[168:169], v[168:169], v[176:177], s[48:49] op_sel_hi:[1,1,0]
	v_pk_fma_f32 v[170:171], v[170:171], v[178:179], s[48:49] op_sel_hi:[1,1,0]
	v_pk_fma_f32 v[172:173], v[172:173], v[180:181], s[48:49] op_sel_hi:[1,1,0]
	v_pk_fma_f32 v[174:175], v[174:175], v[182:183], s[48:49] op_sel_hi:[1,1,0]
	v_pk_fma_f32 v[160:161], v[160:161], v[168:169], 0.5 op_sel_hi:[1,1,0]
	v_pk_fma_f32 v[162:163], v[162:163], v[170:171], 0.5 op_sel_hi:[1,1,0]
	v_pk_fma_f32 v[164:165], v[164:165], v[172:173], 0.5 op_sel_hi:[1,1,0]
	v_pk_fma_f32 v[166:167], v[166:167], v[174:175], 0.5 op_sel_hi:[1,1,0]
	v_pk_mul_f32 v[12:13], v[12:13], v[160:161]
	v_pk_mul_f32 v[14:15], v[14:15], v[162:163]
	v_pk_mul_f32 v[8:9], v[8:9], v[164:165]
	v_pk_mul_f32 v[10:11], v[10:11], v[166:167]
	v_cvt_pk_bf16_f32 v184, v12, v13
	v_cvt_pk_bf16_f32 v185, v14, v15
	v_cvt_pk_bf16_f32 v186, v8, v9
	v_cvt_pk_bf16_f32 v187, v10, v11
	global_store_dwordx4 v[196:197], v[184:187], off
	v_pk_add_f32 v[4:5], v[4:5], v[60:61]
	v_pk_add_f32 v[6:7], v[6:7], v[62:63]
	v_pk_add_f32 v[0:1], v[0:1], v[56:57]
	v_pk_add_f32 v[2:3], v[2:3], v[58:59]
	v_med3_f32 v160, v4, s78, v158
	v_med3_f32 v161, v5, s78, v158
	v_med3_f32 v162, v6, s78, v158
	v_med3_f32 v163, v7, s78, v158
	v_med3_f32 v164, v0, s78, v158
	v_med3_f32 v165, v1, s78, v158
	v_med3_f32 v166, v2, s78, v158
	v_med3_f32 v167, v3, s78, v158
	v_pk_mul_f32 v[168:169], v[160:161], v[160:161]
	v_pk_mul_f32 v[170:171], v[162:163], v[162:163]
	v_pk_mul_f32 v[172:173], v[164:165], v[164:165]
	v_pk_mul_f32 v[174:175], v[166:167], v[166:167]
	v_pk_fma_f32 v[168:169], v[168:169], s[20:21], -1.0 op_sel_hi:[1,0,0]
	v_pk_fma_f32 v[170:171], v[170:171], s[20:21], -1.0 op_sel_hi:[1,0,0]
	v_pk_fma_f32 v[172:173], v[172:173], s[20:21], -1.0 op_sel_hi:[1,0,0]
	v_pk_fma_f32 v[174:175], v[174:175], s[20:21], -1.0 op_sel_hi:[1,0,0]
	v_pk_fma_f32 v[176:177], v[168:169], s[22:23], v[150:151] op_sel_hi:[1,0,0] neg_lo:[1,0,0] neg_hi:[1,0,0]
	v_pk_fma_f32 v[178:179], v[170:171], s[22:23], v[150:151] op_sel_hi:[1,0,0] neg_lo:[1,0,0] neg_hi:[1,0,0]
	v_pk_fma_f32 v[180:181], v[172:173], s[22:23], v[150:151] op_sel_hi:[1,0,0] neg_lo:[1,0,0] neg_hi:[1,0,0]
	v_pk_fma_f32 v[182:183], v[174:175], s[22:23], v[150:151] op_sel_hi:[1,0,0] neg_lo:[1,0,0] neg_hi:[1,0,0]
	v_pk_fma_f32 v[176:177], v[168:169], v[176:177], s[26:27] op_sel_hi:[1,1,0]
	v_pk_fma_f32 v[178:179], v[170:171], v[178:179], s[26:27] op_sel_hi:[1,1,0]
	v_pk_fma_f32 v[180:181], v[172:173], v[180:181], s[26:27] op_sel_hi:[1,1,0]
	v_pk_fma_f32 v[182:183], v[174:175], v[182:183], s[26:27] op_sel_hi:[1,1,0]
	v_pk_fma_f32 v[176:177], v[168:169], v[176:177], s[28:29] op_sel_hi:[1,1,0]
	v_pk_fma_f32 v[178:179], v[170:171], v[178:179], s[28:29] op_sel_hi:[1,1,0]
	v_pk_fma_f32 v[180:181], v[172:173], v[180:181], s[28:29] op_sel_hi:[1,1,0]
	v_pk_fma_f32 v[182:183], v[174:175], v[182:183], s[28:29] op_sel_hi:[1,1,0]
	v_pk_fma_f32 v[176:177], v[168:169], v[176:177], s[30:31] op_sel_hi:[1,1,0]
	v_pk_fma_f32 v[178:179], v[170:171], v[178:179], s[30:31] op_sel_hi:[1,1,0]
	v_pk_fma_f32 v[180:181], v[172:173], v[180:181], s[30:31] op_sel_hi:[1,1,0]
	v_pk_fma_f32 v[182:183], v[174:175], v[182:183], s[30:31] op_sel_hi:[1,1,0]
	v_pk_fma_f32 v[176:177], v[168:169], v[176:177], s[34:35] op_sel_hi:[1,1,0]
	v_pk_fma_f32 v[178:179], v[170:171], v[178:179], s[34:35] op_sel_hi:[1,1,0]
	v_pk_fma_f32 v[180:181], v[172:173], v[180:181], s[34:35] op_sel_hi:[1,1,0]
	v_pk_fma_f32 v[182:183], v[174:175], v[182:183], s[34:35] op_sel_hi:[1,1,0]
	v_pk_fma_f32 v[176:177], v[168:169], v[176:177], s[36:37] op_sel_hi:[1,1,0]
	v_pk_fma_f32 v[178:179], v[170:171], v[178:179], s[36:37] op_sel_hi:[1,1,0]
	v_pk_fma_f32 v[180:181], v[172:173], v[180:181], s[36:37] op_sel_hi:[1,1,0]
	v_pk_fma_f32 v[182:183], v[174:175], v[182:183], s[36:37] op_sel_hi:[1,1,0]
	v_pk_fma_f32 v[176:177], v[168:169], v[176:177], s[38:39] op_sel_hi:[1,1,0]
	v_pk_fma_f32 v[178:179], v[170:171], v[178:179], s[38:39] op_sel_hi:[1,1,0]
	v_pk_fma_f32 v[180:181], v[172:173], v[180:181], s[38:39] op_sel_hi:[1,1,0]
	v_pk_fma_f32 v[182:183], v[174:175], v[182:183], s[38:39] op_sel_hi:[1,1,0]
	v_pk_fma_f32 v[176:177], v[168:169], v[176:177], s[40:41] op_sel_hi:[1,1,0]
	v_pk_fma_f32 v[178:179], v[170:171], v[178:179], s[40:41] op_sel_hi:[1,1,0]
	v_pk_fma_f32 v[180:181], v[172:173], v[180:181], s[40:41] op_sel_hi:[1,1,0]
	v_pk_fma_f32 v[182:183], v[174:175], v[182:183], s[40:41] op_sel_hi:[1,1,0]
	v_pk_fma_f32 v[176:177], v[168:169], v[176:177], s[42:43] op_sel_hi:[1,1,0]
	v_pk_fma_f32 v[178:179], v[170:171], v[178:179], s[42:43] op_sel_hi:[1,1,0]
	v_pk_fma_f32 v[180:181], v[172:173], v[180:181], s[42:43] op_sel_hi:[1,1,0]
	v_pk_fma_f32 v[182:183], v[174:175], v[182:183], s[42:43] op_sel_hi:[1,1,0]
	v_pk_fma_f32 v[176:177], v[168:169], v[176:177], s[44:45] op_sel_hi:[1,1,0]
	v_pk_fma_f32 v[178:179], v[170:171], v[178:179], s[44:45] op_sel_hi:[1,1,0]
	v_pk_fma_f32 v[180:181], v[172:173], v[180:181], s[44:45] op_sel_hi:[1,1,0]
	v_pk_fma_f32 v[182:183], v[174:175], v[182:183], s[44:45] op_sel_hi:[1,1,0]
	v_pk_fma_f32 v[168:169], v[168:169], v[176:177], s[48:49] op_sel_hi:[1,1,0]
	v_pk_fma_f32 v[170:171], v[170:171], v[178:179], s[48:49] op_sel_hi:[1,1,0]
	v_pk_fma_f32 v[172:173], v[172:173], v[180:181], s[48:49] op_sel_hi:[1,1,0]
	v_pk_fma_f32 v[174:175], v[174:175], v[182:183], s[48:49] op_sel_hi:[1,1,0]
	v_pk_fma_f32 v[160:161], v[160:161], v[168:169], 0.5 op_sel_hi:[1,1,0]
	v_pk_fma_f32 v[162:163], v[162:163], v[170:171], 0.5 op_sel_hi:[1,1,0]
	v_pk_fma_f32 v[164:165], v[164:165], v[172:173], 0.5 op_sel_hi:[1,1,0]
	v_pk_fma_f32 v[166:167], v[166:167], v[174:175], 0.5 op_sel_hi:[1,1,0]
	v_pk_mul_f32 v[4:5], v[4:5], v[160:161]
	v_pk_mul_f32 v[6:7], v[6:7], v[162:163]
	v_pk_mul_f32 v[0:1], v[0:1], v[164:165]
	v_pk_mul_f32 v[2:3], v[2:3], v[166:167]
	v_cvt_pk_bf16_f32 v188, v4, v5
	v_cvt_pk_bf16_f32 v189, v6, v7
	v_cvt_pk_bf16_f32 v190, v0, v1
	v_cvt_pk_bf16_f32 v191, v2, v3
	global_store_dwordx4 v[196:197], v[188:191], off offset:256
	s_and_b64 vcc, exec, s[70:71]
	s_cbranch_vccz .Lg9_nostat_7
	v_pk_mul_f32 v[168:169], v[12:13], v[12:13]
	v_pk_mul_f32 v[170:171], v[14:15], v[14:15]
	v_pk_mul_f32 v[172:173], v[8:9], v[8:9]
	v_pk_mul_f32 v[174:175], v[10:11], v[10:11]
	v_pk_mul_f32 v[176:177], v[4:5], v[4:5]
	v_pk_mul_f32 v[178:179], v[6:7], v[6:7]
	v_pk_mul_f32 v[180:181], v[0:1], v[0:1]
	v_pk_mul_f32 v[182:183], v[2:3], v[2:3]
	v_add_f32_e32 v160, v12, v13
	v_add_f32_e32 v161, v14, v15
	v_add_f32_e32 v162, v8, v9
	v_add_f32_e32 v163, v10, v11
	v_add_f32_e32 v164, v4, v5
	v_add_f32_e32 v165, v6, v7
	v_add_f32_e32 v166, v0, v1
	v_add_f32_e32 v167, v2, v3
	v_add_f32_e32 v160, v160, v161
	v_add_f32_e32 v164, v164, v165
	v_add_f32_e32 v160, v160, v162
	v_add_f32_e32 v164, v164, v166
	v_add_f32_e32 v160, v160, v163
	v_add_f32_e32 v164, v164, v167
	v_add_f32_e32 v168, v168, v169
	v_add_f32_e32 v170, v170, v171
	v_add_f32_e32 v172, v172, v173
	v_add_f32_e32 v174, v174, v175
	v_add_f32_e32 v176, v176, v177
	v_add_f32_e32 v178, v178, v179
	v_add_f32_e32 v180, v180, v181
	v_add_f32_e32 v182, v182, v183
	v_add_f32_e32 v198, v160, v164
	v_add_f32_e32 v168, v168, v170
	v_add_f32_e32 v176, v176, v178
	v_mov_b32_e32 v199, v198
	v_add_f32_e32 v168, v168, v172
	v_add_f32_e32 v176, v176, v180
	s_nop 1
	v_permlane16_swap_b32 v199, v198
	s_nop 1
	v_add_f32_e32 v168, v168, v174
	v_add_f32_e32 v176, v176, v182
	v_add_f32_e32 v198, v199, v198
	v_add_f32_e32 v200, v168, v176
	v_mov_b32_e32 v202, v198
	v_mov_b32_e32 v201, v200
	s_nop 1
	v_permlane32_swap_b32 v202, v198
	s_nop 1
	s_nop 1
	v_permlane16_swap_b32 v201, v200
	s_nop 1
	v_add_f32_e32 v199, v201, v200
	v_mov_b32_e32 v203, v199
	s_nop 1
	v_permlane32_swap_b32 v203, v199
	s_nop 1
	s_and_saveexec_b64 s[4:5], s[6:7]
	v_lshlrev_b64 v[194:195], 8, v[192:193]
	v_lshl_add_u64 v[194:195], s[16:17], 0, v[194:195]
	v_lshl_add_u64 v[194:195], s[68:69], 3, v[194:195]
	v_pk_add_f32 v[200:201], v[202:203], v[198:199]
	global_store_dwordx2 v[194:195], v[200:201], off
	s_or_b64 exec, exec, s[4:5]
.Lg9_nostat_7:
.LBB0_1804:
	s_and_b64 vcc, exec, s[0:1]
	s_mov_b64 s[0:1], -1
	s_cbranch_vccnz .LBB0_1761
	s_andn2_b64 vcc, exec, s[12:13]
	s_cbranch_vccnz .LBB0_1760
	s_barrier
	s_branch .LBB0_1760

.LBB0_2099:
	global_load_dword v2, v1, s[4:5] sc1
	s_add_i32 s3, s3, 1
	s_mov_b64 s[12:13], -1
	s_waitcnt vmcnt(0)
	v_cmp_ge_u32_e64 s[10:11], v2, v0
	s_branch .LBB0_2096

.LBB0_2140:
	s_mov_b32 s19, 0
	v_mbcnt_lo_u32_b32 v162, -1, 0
	v_mbcnt_hi_u32_b32 v162, -1, v162
	s_lshl_b32 s19, s64, 8
	v_readlane_b32 s64, v249, 35
	v_lshrrev_b32_e32 v8, 1, v162
	v_and_or_b32 v8, v8, 24, s19
	s_lshr_b32 s19, s26, 5
	s_mul_i32 s28, s19, 0x1800
	s_ashr_i32 s29, s28, 31
	v_or_b32_e32 v8, s52, v8
	s_lshl_b64 s[28:29], s[28:29], 2
	s_add_u32 s30, s48, s28
	v_ashrrev_i32_e32 v9, 31, v8
	s_addc_u32 s31, s49, s29
	v_lshlrev_b64 v[14:15], 2, v[8:9]
	v_lshl_add_u64 v[146:147], s[30:31], 0, v[14:15]
	s_add_u32 s30, s44, s28
	s_addc_u32 s31, s45, s29
	s_add_u32 s28, s30, 0x1000
	s_addc_u32 s29, s31, 0
	v_lshl_add_u64 v[148:149], s[28:29], 0, v[14:15]
	s_lshl_b32 s19, s26, 8
	global_load_dwordx4 v[10:13], v[146:147], off
	global_load_dwordx4 v[136:139], v[146:147], off offset:16
	global_load_dwordx4 v[140:143], v[148:149], off
	global_load_dwordx4 v[150:153], v[148:149], off offset:16
	s_add_i32 s19, s19, s51
	v_and_or_b32 v148, v162, 15, s19
	v_ashrrev_i32_e32 v149, 31, v148
	v_lshlrev_b64 v[162:163], 10, v[148:149]
	v_lshl_add_u64 v[162:163], v[162:163], 0, v[8:9]
	v_lshl_add_u64 v[200:201], s[30:31], 0, v[14:15]
	v_lshlrev_b64 v[212:213], 1, v[162:163]
	v_readlane_b32 s70, v249, 41
	v_readlane_b32 s71, v249, 42
	global_load_dwordx4 v[154:157], v[200:201], off offset:16
	global_load_dwordx4 v[158:161], v[200:201], off
	v_lshl_add_u64 v[214:215], s[90:91], 0, v[212:213]
	v_mov_b32_e32 v246, v212
	v_lshl_add_u64 v[14:15], s[70:71], 0, v[14:15]
	global_load_dwordx4 v[162:165], v[214:215], off
	global_load_dwordx4 v[230:233], v246, s[90:91] offset:256
	v_add_u32_e32 v247, 0x8000, v246
	global_load_dwordx4 v[234:237], v247, s[90:91]
	v_add_u32_e32 v247, 0x8000, v246
	global_load_dwordx4 v[238:241], v247, s[90:91] offset:256
	v_add_u32_e32 v247, 0x10000, v246
	global_load_dwordx4 v[242:245], v247, s[90:91]
	v_add_u32_e32 v247, 0x10000, v246
	global_load_dwordx4 v[226:229], v247, s[90:91] offset:256
	global_load_dwordx4 v[166:169], v[14:15], off
	global_load_dwordx4 v[170:173], v[14:15], off offset:16
	global_load_dwordx4 v[180:183], v[14:15], off offset:528
	global_load_dwordx4 v[184:187], v[14:15], off offset:512
	global_load_dwordx4 v[188:191], v[146:147], off offset:528
	global_load_dwordx4 v[192:195], v[146:147], off offset:512
	global_load_dwordx4 v[196:199], v[200:201], off offset:528
	s_nop 0
	global_load_dwordx4 v[200:203], v[200:201], off offset:512
	v_or_b32_e32 v204, 0x80, v8
	v_ashrrev_i32_e32 v205, 31, v204
	v_lshl_add_u64 v[14:15], v[204:205], 2, s[28:29]
	global_load_dwordx4 v[204:207], v[14:15], off offset:16
	global_load_dwordx4 v[208:211], v[14:15], off
	v_readlane_b32 s72, v249, 43
	v_readlane_b32 s73, v249, 44
	v_readlane_b32 s74, v249, 45
	v_readlane_b32 s75, v249, 46
	v_readlane_b32 s76, v249, 47
	v_readlane_b32 s77, v249, 48
	v_readlane_b32 s78, v249, 49
	v_readlane_b32 s79, v249, 50
	v_readlane_b32 s72, v249, 55
	v_readlane_b32 s76, v249, 59
	v_readlane_b32 s77, v249, 60
	v_readlane_b32 s73, v249, 56
	v_readlane_b32 s74, v249, 57
	v_readlane_b32 s75, v249, 58
	v_readlane_b32 s78, v249, 61
	v_readlane_b32 s79, v249, 62
	s_and_b64 vcc, exec, s[0:1]
	s_mov_b64 s[0:1], -1
	v_readlane_b32 s65, v249, 36
	v_readlane_b32 s66, v249, 37
	v_readlane_b32 s67, v249, 38
	v_readlane_b32 s68, v249, 39
	v_readlane_b32 s69, v249, 40
	s_waitcnt vmcnt(0)
	v_pk_add_f32 v[216:217], v[12:13], 1.0 op_sel_hi:[1,0]
	v_pk_add_f32 v[220:221], v[138:139], 1.0 op_sel_hi:[1,0]
	v_add_f32_e32 v138, 1.0, v140
	v_add_f32_e32 v139, 1.0, v141
	v_add_f32_e32 v140, 1.0, v142
	v_add_f32_e32 v141, 1.0, v143
	v_add_f32_e32 v142, 1.0, v150
	v_add_f32_e32 v143, 1.0, v151
	v_add_f32_e32 v146, 1.0, v152
	v_add_f32_e32 v147, 1.0, v153
	v_rcp_f32_e32 v138, v138
	v_rcp_f32_e32 v139, v139
	v_rcp_f32_e32 v140, v140
	v_rcp_f32_e32 v141, v141
	v_rcp_f32_e32 v142, v142
	v_rcp_f32_e32 v143, v143
	v_rcp_f32_e32 v146, v146
	v_rcp_f32_e32 v147, v147
	v_pk_mul_f32 v[138:139], v[138:139], s[14:15] op_sel_hi:[1,0]
	v_pk_mul_f32 v[140:141], v[140:141], s[14:15] op_sel_hi:[1,0]
	v_pk_mul_f32 v[142:143], v[142:143], s[14:15] op_sel_hi:[1,0]
	v_pk_mul_f32 v[146:147], v[146:147], s[14:15] op_sel_hi:[1,0]
	v_pk_add_f32 v[218:219], v[10:11], 1.0 op_sel_hi:[1,0]
	v_pk_add_f32 v[222:223], v[136:137], 1.0 op_sel_hi:[1,0]
	v_pk_mul_f32 v[150:151], v[160:161], v[140:141]
	v_pk_mul_f32 v[152:153], v[158:159], v[138:139]
	v_pk_mul_f32 v[156:157], v[156:157], v[146:147]
	v_pk_mul_f32 v[158:159], v[154:155], v[142:143]
	v_lshlrev_b32_e32 v160, 16, v162
	v_and_b32_e32 v161, 0xffff0000, v162
	v_lshlrev_b32_e32 v162, 16, v163
	v_and_b32_e32 v163, 0xffff0000, v163
	v_lshlrev_b32_e32 v224, 16, v164
	v_and_b32_e32 v225, 0xffff0000, v164
	v_lshlrev_b32_e32 v164, 16, v165
	v_and_b32_e32 v165, 0xffff0000, v165
	v_pk_fma_f32 v[150:151], v[168:169], v[216:217], v[150:151] neg_lo:[0,0,1] neg_hi:[0,0,1]
	v_pk_fma_f32 v[154:155], v[166:167], v[218:219], v[152:153] neg_lo:[0,0,1] neg_hi:[0,0,1]
	v_pk_fma_f32 v[152:153], v[172:173], v[220:221], v[156:157] neg_lo:[0,0,1] neg_hi:[0,0,1]
	v_pk_fma_f32 v[156:157], v[170:171], v[222:223], v[158:159] neg_lo:[0,0,1] neg_hi:[0,0,1]
	v_pk_mul_f32 v[10:11], v[216:217], s[16:17] op_sel_hi:[1,0]
	v_pk_mul_f32 v[14:15], v[218:219], s[16:17] op_sel_hi:[1,0]
	v_pk_mul_f32 v[12:13], v[220:221], s[16:17] op_sel_hi:[1,0]
	v_pk_mul_f32 v[136:137], v[222:223], s[16:17] op_sel_hi:[1,0]
	v_pk_fma_f32 v[158:159], v[138:139], v[160:161], v[154:155]
	v_pk_fma_f32 v[160:161], v[140:141], v[162:163], v[150:151]
	v_pk_fma_f32 v[162:163], v[142:143], v[224:225], v[156:157]
	v_pk_fma_f32 v[164:165], v[146:147], v[164:165], v[152:153]
	v_pk_fma_f32 v[132:133], v[132:133], v[14:15], v[158:159]
	v_pk_fma_f32 v[134:135], v[134:135], v[10:11], v[160:161]
	v_pk_fma_f32 v[158:159], v[128:129], v[136:137], v[162:163]
	v_pk_fma_f32 v[160:161], v[130:131], v[12:13], v[164:165]
	v_cvt_pk_bf16_f32 v128, v132, v133
	v_cvt_pk_bf16_f32 v129, v134, v135
	v_cvt_pk_bf16_f32 v130, v158, v159
	v_cvt_pk_bf16_f32 v131, v160, v161
	v_lshl_add_u64 v[216:217], s[76:77], 0, v[212:213]
	global_store_dwordx4 v[216:217], v[128:131], off
	v_add_f32_e32 v149, 1.0, v208
	v_add_f32_e32 v159, 1.0, v209
	v_add_f32_e32 v160, 1.0, v210
	v_add_f32_e32 v161, 1.0, v211
	v_add_f32_e32 v164, 1.0, v204
	v_add_f32_e32 v165, 1.0, v205
	v_add_f32_e32 v166, 1.0, v206
	v_add_f32_e32 v167, 1.0, v207
	v_rcp_f32_e32 v158, v149
	v_rcp_f32_e32 v159, v159
	v_rcp_f32_e32 v160, v160
	v_rcp_f32_e32 v161, v161
	v_rcp_f32_e32 v170, v164
	v_rcp_f32_e32 v171, v165
	v_rcp_f32_e32 v172, v166
	v_rcp_f32_e32 v173, v167
	v_or_b32_e32 v128, 16, v148
	v_ashrrev_i32_e32 v129, 31, v128
	v_pk_mul_f32 v[166:167], v[158:159], s[14:15] op_sel_hi:[1,0]
	v_pk_mul_f32 v[164:165], v[160:161], s[14:15] op_sel_hi:[1,0]
	v_pk_mul_f32 v[160:161], v[170:171], s[14:15] op_sel_hi:[1,0]
	v_pk_mul_f32 v[158:159], v[172:173], s[14:15] op_sel_hi:[1,0]
	v_lshlrev_b64 v[128:129], 10, v[128:129]
	v_pk_add_f32 v[162:163], v[194:195], 1.0 op_sel_hi:[1,0]
	v_pk_add_f32 v[168:169], v[192:193], 1.0 op_sel_hi:[1,0]
	v_pk_add_f32 v[190:191], v[190:191], 1.0 op_sel_hi:[1,0]
	v_pk_add_f32 v[188:189], v[188:189], 1.0 op_sel_hi:[1,0]
	v_pk_mul_f32 v[170:171], v[202:203], v[164:165]
	v_pk_mul_f32 v[172:173], v[200:201], v[166:167]
	v_pk_mul_f32 v[192:193], v[198:199], v[158:159]
	v_pk_mul_f32 v[194:195], v[196:197], v[160:161]
	v_lshl_add_u64 v[128:129], v[128:129], 0, v[8:9]
	v_pk_mul_f32 v[130:131], v[162:163], s[16:17] op_sel_hi:[1,0]
	v_pk_mul_f32 v[132:133], v[168:169], s[16:17] op_sel_hi:[1,0]
	v_pk_fma_f32 v[170:171], v[186:187], v[162:163], v[170:171] neg_lo:[0,0,1] neg_hi:[0,0,1]
	v_pk_fma_f32 v[172:173], v[184:185], v[168:169], v[172:173] neg_lo:[0,0,1] neg_hi:[0,0,1]
	v_pk_fma_f32 v[162:163], v[182:183], v[190:191], v[192:193] neg_lo:[0,0,1] neg_hi:[0,0,1]
	v_pk_fma_f32 v[168:169], v[180:181], v[188:189], v[194:195] neg_lo:[0,0,1] neg_hi:[0,0,1]
	v_lshlrev_b64 v[218:219], 1, v[128:129]
	v_pk_mul_f32 v[128:129], v[190:191], s[16:17] op_sel_hi:[1,0]
	v_pk_mul_f32 v[134:135], v[188:189], s[16:17] op_sel_hi:[1,0]
	v_lshl_add_u64 v[220:221], s[90:91], 0, v[218:219]
	s_waitcnt vmcnt(9)
	v_mov_b32_e32 v212, v230
	v_mov_b32_e32 v213, v231
	v_mov_b32_e32 v214, v232
	v_mov_b32_e32 v215, v233
	v_add_u32_e32 v247, 0x18000, v246
	global_load_dwordx4 v[230:233], v247, s[90:91]
	v_lshlrev_b32_e32 v180, 16, v212
	v_and_b32_e32 v181, 0xffff0000, v212
	v_lshlrev_b32_e32 v182, 16, v213
	v_and_b32_e32 v183, 0xffff0000, v213
	v_lshlrev_b32_e32 v184, 16, v214
	v_and_b32_e32 v185, 0xffff0000, v214
	v_lshlrev_b32_e32 v186, 16, v215
	v_and_b32_e32 v187, 0xffff0000, v215
	v_pk_fma_f32 v[180:181], v[166:167], v[180:181], v[172:173]
	v_pk_fma_f32 v[182:183], v[164:165], v[182:183], v[170:171]
	v_pk_fma_f32 v[184:185], v[160:161], v[184:185], v[168:169]
	v_pk_fma_f32 v[186:187], v[158:159], v[186:187], v[162:163]
	v_pk_fma_f32 v[124:125], v[124:125], v[132:133], v[180:181]
	v_pk_fma_f32 v[126:127], v[126:127], v[130:131], v[182:183]
	v_pk_fma_f32 v[180:181], v[120:121], v[134:135], v[184:185]
	v_pk_fma_f32 v[182:183], v[122:123], v[128:129], v[186:187]
	v_cvt_pk_bf16_f32 v120, v124, v125
	v_cvt_pk_bf16_f32 v121, v126, v127
	v_cvt_pk_bf16_f32 v122, v180, v181
	v_cvt_pk_bf16_f32 v123, v182, v183
	global_store_dwordx4 v[216:217], v[120:123], off offset:256
	v_lshl_add_u64 v[124:125], s[76:77], 0, v[218:219]
	s_waitcnt vmcnt(9)
	v_mov_b32_e32 v120, v234
	v_mov_b32_e32 v121, v235
	v_mov_b32_e32 v122, v236
	v_mov_b32_e32 v123, v237
	v_add_u32_e32 v247, 0x18000, v246
	global_load_dwordx4 v[234:237], v247, s[90:91] offset:256
	v_lshlrev_b32_e32 v126, 16, v120
	v_and_b32_e32 v127, 0xffff0000, v120
	v_lshlrev_b32_e32 v120, 16, v121
	v_and_b32_e32 v121, 0xffff0000, v121
	v_lshlrev_b32_e32 v180, 16, v122
	v_and_b32_e32 v181, 0xffff0000, v122
	v_lshlrev_b32_e32 v122, 16, v123
	v_and_b32_e32 v123, 0xffff0000, v123
	v_pk_fma_f32 v[126:127], v[138:139], v[126:127], v[154:155]
	v_pk_fma_f32 v[120:121], v[140:141], v[120:121], v[150:151]
	v_pk_fma_f32 v[180:181], v[142:143], v[180:181], v[156:157]
	v_pk_fma_f32 v[122:123], v[146:147], v[122:123], v[152:153]
	v_pk_fma_f32 v[116:117], v[116:117], v[14:15], v[126:127]
	v_pk_fma_f32 v[118:119], v[118:119], v[10:11], v[120:121]
	v_pk_fma_f32 v[120:121], v[112:113], v[136:137], v[180:181]
	v_pk_fma_f32 v[122:123], v[114:115], v[12:13], v[122:123]
	v_cvt_pk_bf16_f32 v112, v116, v117
	v_cvt_pk_bf16_f32 v113, v118, v119
	v_cvt_pk_bf16_f32 v114, v120, v121
	v_cvt_pk_bf16_f32 v115, v122, v123
	global_store_dwordx4 v[124:125], v[112:115], off
	v_or_b32_e32 v116, 32, v148
	v_ashrrev_i32_e32 v117, 31, v116
	v_lshlrev_b64 v[116:117], 10, v[116:117]
	v_lshl_add_u64 v[116:117], v[116:117], 0, v[8:9]
	v_lshlrev_b64 v[116:117], 1, v[116:117]
	v_lshl_add_u64 v[118:119], s[90:91], 0, v[116:117]
	s_waitcnt vmcnt(9)
	v_mov_b32_e32 v112, v238
	v_mov_b32_e32 v113, v239
	v_mov_b32_e32 v114, v240
	v_mov_b32_e32 v115, v241
	v_add_u32_e32 v247, 0x40000, v246
	global_load_dwordx4 v[238:241], v247, s[90:91]
	v_lshlrev_b32_e32 v120, 16, v112
	v_and_b32_e32 v121, 0xffff0000, v112
	v_lshlrev_b32_e32 v112, 16, v113
	v_and_b32_e32 v113, 0xffff0000, v113
	v_lshlrev_b32_e32 v122, 16, v114
	v_and_b32_e32 v123, 0xffff0000, v114
	v_lshlrev_b32_e32 v114, 16, v115
	v_and_b32_e32 v115, 0xffff0000, v115
	v_pk_fma_f32 v[120:121], v[166:167], v[120:121], v[172:173]
	v_pk_fma_f32 v[112:113], v[164:165], v[112:113], v[170:171]
	v_pk_fma_f32 v[122:123], v[160:161], v[122:123], v[168:169]
	v_pk_fma_f32 v[114:115], v[158:159], v[114:115], v[162:163]
	v_pk_fma_f32 v[108:109], v[108:109], v[132:133], v[120:121]
	v_pk_fma_f32 v[110:111], v[110:111], v[130:131], v[112:113]
	v_pk_fma_f32 v[112:113], v[104:105], v[134:135], v[122:123]
	v_pk_fma_f32 v[114:115], v[106:107], v[128:129], v[114:115]
	v_cvt_pk_bf16_f32 v104, v108, v109
	v_cvt_pk_bf16_f32 v105, v110, v111
	v_cvt_pk_bf16_f32 v106, v112, v113
	v_cvt_pk_bf16_f32 v107, v114, v115
	global_store_dwordx4 v[124:125], v[104:107], off offset:256
	v_lshl_add_u64 v[108:109], s[76:77], 0, v[116:117]
	s_waitcnt vmcnt(9)
	v_mov_b32_e32 v104, v242
	v_mov_b32_e32 v105, v243
	v_mov_b32_e32 v106, v244
	v_mov_b32_e32 v107, v245
	v_add_u32_e32 v247, 0x40000, v246
	global_load_dwordx4 v[242:245], v247, s[90:91] offset:256
	v_lshlrev_b32_e32 v110, 16, v104
	v_and_b32_e32 v111, 0xffff0000, v104
	v_lshlrev_b32_e32 v104, 16, v105
	v_and_b32_e32 v105, 0xffff0000, v105
	v_lshlrev_b32_e32 v112, 16, v106
	v_and_b32_e32 v113, 0xffff0000, v106
	v_lshlrev_b32_e32 v106, 16, v107
	v_and_b32_e32 v107, 0xffff0000, v107
	v_pk_fma_f32 v[110:111], v[138:139], v[110:111], v[154:155]
	v_pk_fma_f32 v[104:105], v[140:141], v[104:105], v[150:151]
	v_pk_fma_f32 v[112:113], v[142:143], v[112:113], v[156:157]
	v_pk_fma_f32 v[106:107], v[146:147], v[106:107], v[152:153]
	v_pk_fma_f32 v[100:101], v[100:101], v[14:15], v[110:111]
	v_pk_fma_f32 v[102:103], v[102:103], v[10:11], v[104:105]
	v_pk_fma_f32 v[104:105], v[96:97], v[136:137], v[112:113]
	v_pk_fma_f32 v[106:107], v[98:99], v[12:13], v[106:107]
	v_cvt_pk_bf16_f32 v96, v100, v101
	v_cvt_pk_bf16_f32 v97, v102, v103
	v_cvt_pk_bf16_f32 v98, v104, v105
	v_cvt_pk_bf16_f32 v99, v106, v107
	global_store_dwordx4 v[108:109], v[96:99], off
	v_or_b32_e32 v100, 48, v148
	v_ashrrev_i32_e32 v101, 31, v100
	v_lshlrev_b64 v[100:101], 10, v[100:101]
	v_lshl_add_u64 v[100:101], v[100:101], 0, v[8:9]
	v_lshlrev_b64 v[100:101], 1, v[100:101]
	v_lshl_add_u64 v[102:103], s[90:91], 0, v[100:101]
	s_waitcnt vmcnt(9)
	v_mov_b32_e32 v96, v226
	v_mov_b32_e32 v97, v227
	v_mov_b32_e32 v98, v228
	v_mov_b32_e32 v99, v229
	v_add_u32_e32 v247, 0x48000, v246
	global_load_dwordx4 v[226:229], v247, s[90:91]
	v_lshlrev_b32_e32 v104, 16, v96
	v_and_b32_e32 v105, 0xffff0000, v96
	v_lshlrev_b32_e32 v96, 16, v97
	v_and_b32_e32 v97, 0xffff0000, v97
	v_lshlrev_b32_e32 v106, 16, v98
	v_and_b32_e32 v107, 0xffff0000, v98
	v_lshlrev_b32_e32 v98, 16, v99
	v_and_b32_e32 v99, 0xffff0000, v99
	v_pk_fma_f32 v[104:105], v[166:167], v[104:105], v[172:173]
	v_pk_fma_f32 v[96:97], v[164:165], v[96:97], v[170:171]
	v_pk_fma_f32 v[106:107], v[160:161], v[106:107], v[168:169]
	v_pk_fma_f32 v[98:99], v[158:159], v[98:99], v[162:163]
	v_pk_fma_f32 v[92:93], v[92:93], v[132:133], v[104:105]
	v_pk_fma_f32 v[94:95], v[94:95], v[130:131], v[96:97]
	v_pk_fma_f32 v[96:97], v[88:89], v[134:135], v[106:107]
	v_pk_fma_f32 v[98:99], v[90:91], v[128:129], v[98:99]
	v_cvt_pk_bf16_f32 v88, v92, v93
	v_cvt_pk_bf16_f32 v89, v94, v95
	v_cvt_pk_bf16_f32 v90, v96, v97
	v_cvt_pk_bf16_f32 v91, v98, v99
	global_store_dwordx4 v[108:109], v[88:91], off offset:256
	v_lshl_add_u64 v[92:93], s[76:77], 0, v[100:101]
	s_waitcnt vmcnt(9)
	v_mov_b32_e32 v88, v230
	v_mov_b32_e32 v89, v231
	v_mov_b32_e32 v90, v232
	v_mov_b32_e32 v91, v233
	v_add_u32_e32 v247, 0x48000, v246
	global_load_dwordx4 v[230:233], v247, s[90:91] offset:256
	v_lshlrev_b32_e32 v94, 16, v88
	v_and_b32_e32 v95, 0xffff0000, v88
	v_lshlrev_b32_e32 v88, 16, v89
	v_and_b32_e32 v89, 0xffff0000, v89
	v_lshlrev_b32_e32 v96, 16, v90
	v_and_b32_e32 v97, 0xffff0000, v90
	v_lshlrev_b32_e32 v90, 16, v91
	v_and_b32_e32 v91, 0xffff0000, v91
	v_pk_fma_f32 v[94:95], v[138:139], v[94:95], v[154:155]
	v_pk_fma_f32 v[88:89], v[140:141], v[88:89], v[150:151]
	v_pk_fma_f32 v[96:97], v[142:143], v[96:97], v[156:157]
	v_pk_fma_f32 v[90:91], v[146:147], v[90:91], v[152:153]
	v_pk_fma_f32 v[84:85], v[84:85], v[14:15], v[94:95]
	v_pk_fma_f32 v[86:87], v[86:87], v[10:11], v[88:89]
	v_pk_fma_f32 v[88:89], v[80:81], v[136:137], v[96:97]
	v_pk_fma_f32 v[90:91], v[82:83], v[12:13], v[90:91]
	v_cvt_pk_bf16_f32 v80, v84, v85
	v_cvt_pk_bf16_f32 v81, v86, v87
	v_cvt_pk_bf16_f32 v82, v88, v89
	v_cvt_pk_bf16_f32 v83, v90, v91
	global_store_dwordx4 v[92:93], v[80:83], off
	v_add_u32_e32 v84, 0x80, v148
	v_ashrrev_i32_e32 v85, 31, v84
	v_lshlrev_b64 v[84:85], 10, v[84:85]
	v_lshl_add_u64 v[84:85], v[84:85], 0, v[8:9]
	v_lshlrev_b64 v[84:85], 1, v[84:85]
	v_lshl_add_u64 v[86:87], s[90:91], 0, v[84:85]
	s_waitcnt vmcnt(9)
	v_mov_b32_e32 v80, v234
	v_mov_b32_e32 v81, v235
	v_mov_b32_e32 v82, v236
	v_mov_b32_e32 v83, v237
	v_add_u32_e32 v247, 0x50000, v246
	global_load_dwordx4 v[234:237], v247, s[90:91]
	v_lshlrev_b32_e32 v88, 16, v80
	v_and_b32_e32 v89, 0xffff0000, v80
	v_lshlrev_b32_e32 v80, 16, v81
	v_and_b32_e32 v81, 0xffff0000, v81
	v_lshlrev_b32_e32 v90, 16, v82
	v_and_b32_e32 v91, 0xffff0000, v82
	v_lshlrev_b32_e32 v82, 16, v83
	v_and_b32_e32 v83, 0xffff0000, v83
	v_pk_fma_f32 v[88:89], v[166:167], v[88:89], v[172:173]
	v_pk_fma_f32 v[80:81], v[164:165], v[80:81], v[170:171]
	v_pk_fma_f32 v[90:91], v[160:161], v[90:91], v[168:169]
	v_pk_fma_f32 v[82:83], v[158:159], v[82:83], v[162:163]
	v_pk_fma_f32 v[76:77], v[76:77], v[132:133], v[88:89]
	v_pk_fma_f32 v[78:79], v[78:79], v[130:131], v[80:81]
	v_pk_fma_f32 v[80:81], v[72:73], v[134:135], v[90:91]
	v_pk_fma_f32 v[82:83], v[74:75], v[128:129], v[82:83]
	v_cvt_pk_bf16_f32 v72, v76, v77
	v_cvt_pk_bf16_f32 v73, v78, v79
	v_cvt_pk_bf16_f32 v74, v80, v81
	v_cvt_pk_bf16_f32 v75, v82, v83
	global_store_dwordx4 v[92:93], v[72:75], off offset:256
	v_lshl_add_u64 v[76:77], s[76:77], 0, v[84:85]
	s_waitcnt vmcnt(9)
	v_mov_b32_e32 v72, v238
	v_mov_b32_e32 v73, v239
	v_mov_b32_e32 v74, v240
	v_mov_b32_e32 v75, v241
	v_add_u32_e32 v247, 0x50000, v246
	global_load_dwordx4 v[238:241], v247, s[90:91] offset:256
	v_lshlrev_b32_e32 v78, 16, v72
	v_and_b32_e32 v79, 0xffff0000, v72
	v_lshlrev_b32_e32 v72, 16, v73
	v_and_b32_e32 v73, 0xffff0000, v73
	v_lshlrev_b32_e32 v80, 16, v74
	v_and_b32_e32 v81, 0xffff0000, v74
	v_lshlrev_b32_e32 v74, 16, v75
	v_and_b32_e32 v75, 0xffff0000, v75
	v_pk_fma_f32 v[78:79], v[138:139], v[78:79], v[154:155]
	v_pk_fma_f32 v[72:73], v[140:141], v[72:73], v[150:151]
	v_pk_fma_f32 v[80:81], v[142:143], v[80:81], v[156:157]
	v_pk_fma_f32 v[74:75], v[146:147], v[74:75], v[152:153]
	v_pk_fma_f32 v[68:69], v[68:69], v[14:15], v[78:79]
	v_pk_fma_f32 v[70:71], v[70:71], v[10:11], v[72:73]
	v_pk_fma_f32 v[72:73], v[64:65], v[136:137], v[80:81]
	v_pk_fma_f32 v[74:75], v[66:67], v[12:13], v[74:75]
	v_cvt_pk_bf16_f32 v64, v68, v69
	v_cvt_pk_bf16_f32 v65, v70, v71
	v_cvt_pk_bf16_f32 v66, v72, v73
	v_cvt_pk_bf16_f32 v67, v74, v75
	global_store_dwordx4 v[76:77], v[64:67], off
	v_add_u32_e32 v68, 0x90, v148
	v_ashrrev_i32_e32 v69, 31, v68
	v_lshlrev_b64 v[68:69], 10, v[68:69]
	v_lshl_add_u64 v[68:69], v[68:69], 0, v[8:9]
	v_lshlrev_b64 v[68:69], 1, v[68:69]
	v_lshl_add_u64 v[70:71], s[90:91], 0, v[68:69]
	s_waitcnt vmcnt(9)
	v_mov_b32_e32 v64, v242
	v_mov_b32_e32 v65, v243
	v_mov_b32_e32 v66, v244
	v_mov_b32_e32 v67, v245
	v_add_u32_e32 v247, 0x58000, v246
	global_load_dwordx4 v[242:245], v247, s[90:91]
	v_lshlrev_b32_e32 v72, 16, v64
	v_and_b32_e32 v73, 0xffff0000, v64
	v_lshlrev_b32_e32 v64, 16, v65
	v_and_b32_e32 v65, 0xffff0000, v65
	v_lshlrev_b32_e32 v74, 16, v66
	v_and_b32_e32 v75, 0xffff0000, v66
	v_lshlrev_b32_e32 v66, 16, v67
	v_and_b32_e32 v67, 0xffff0000, v67
	v_pk_fma_f32 v[72:73], v[166:167], v[72:73], v[172:173]
	v_pk_fma_f32 v[64:65], v[164:165], v[64:65], v[170:171]
	v_pk_fma_f32 v[74:75], v[160:161], v[74:75], v[168:169]
	v_pk_fma_f32 v[66:67], v[158:159], v[66:67], v[162:163]
	v_pk_fma_f32 v[60:61], v[60:61], v[132:133], v[72:73]
	v_pk_fma_f32 v[62:63], v[62:63], v[130:131], v[64:65]
	v_pk_fma_f32 v[64:65], v[56:57], v[134:135], v[74:75]
	v_pk_fma_f32 v[66:67], v[58:59], v[128:129], v[66:67]
	v_cvt_pk_bf16_f32 v56, v60, v61
	v_cvt_pk_bf16_f32 v57, v62, v63
	v_cvt_pk_bf16_f32 v58, v64, v65
	v_cvt_pk_bf16_f32 v59, v66, v67
	global_store_dwordx4 v[76:77], v[56:59], off offset:256
	v_lshl_add_u64 v[60:61], s[76:77], 0, v[68:69]
	s_waitcnt vmcnt(9)
	v_mov_b32_e32 v56, v226
	v_mov_b32_e32 v57, v227
	v_mov_b32_e32 v58, v228
	v_mov_b32_e32 v59, v229
	v_add_u32_e32 v247, 0x58000, v246
	global_load_dwordx4 v[226:229], v247, s[90:91] offset:256
	v_lshlrev_b32_e32 v62, 16, v56
	v_and_b32_e32 v63, 0xffff0000, v56
	v_lshlrev_b32_e32 v56, 16, v57
	v_and_b32_e32 v57, 0xffff0000, v57
	v_lshlrev_b32_e32 v64, 16, v58
	v_and_b32_e32 v65, 0xffff0000, v58
	v_lshlrev_b32_e32 v58, 16, v59
	v_and_b32_e32 v59, 0xffff0000, v59
	v_pk_fma_f32 v[62:63], v[138:139], v[62:63], v[154:155]
	v_pk_fma_f32 v[56:57], v[140:141], v[56:57], v[150:151]
	v_pk_fma_f32 v[64:65], v[142:143], v[64:65], v[156:157]
	v_pk_fma_f32 v[58:59], v[146:147], v[58:59], v[152:153]
	v_pk_fma_f32 v[52:53], v[52:53], v[14:15], v[62:63]
	v_pk_fma_f32 v[54:55], v[54:55], v[10:11], v[56:57]
	v_pk_fma_f32 v[56:57], v[48:49], v[136:137], v[64:65]
	v_pk_fma_f32 v[58:59], v[50:51], v[12:13], v[58:59]
	v_cvt_pk_bf16_f32 v48, v52, v53
	v_cvt_pk_bf16_f32 v49, v54, v55
	v_cvt_pk_bf16_f32 v50, v56, v57
	v_cvt_pk_bf16_f32 v51, v58, v59
	global_store_dwordx4 v[60:61], v[48:51], off
	v_add_u32_e32 v52, 0xa0, v148
	v_ashrrev_i32_e32 v53, 31, v52
	v_lshlrev_b64 v[52:53], 10, v[52:53]
	v_lshl_add_u64 v[52:53], v[52:53], 0, v[8:9]
	v_lshlrev_b64 v[52:53], 1, v[52:53]
	v_lshl_add_u64 v[54:55], s[90:91], 0, v[52:53]
	s_waitcnt vmcnt(9)
	v_mov_b32_e32 v48, v230
	v_mov_b32_e32 v49, v231
	v_mov_b32_e32 v50, v232
	v_mov_b32_e32 v51, v233
	v_lshlrev_b32_e32 v56, 16, v48
	v_and_b32_e32 v57, 0xffff0000, v48
	v_lshlrev_b32_e32 v48, 16, v49
	v_and_b32_e32 v49, 0xffff0000, v49
	v_lshlrev_b32_e32 v58, 16, v50
	v_and_b32_e32 v59, 0xffff0000, v50
	v_lshlrev_b32_e32 v50, 16, v51
	v_and_b32_e32 v51, 0xffff0000, v51
	v_pk_fma_f32 v[56:57], v[166:167], v[56:57], v[172:173]
	v_pk_fma_f32 v[48:49], v[164:165], v[48:49], v[170:171]
	v_pk_fma_f32 v[58:59], v[160:161], v[58:59], v[168:169]
	v_pk_fma_f32 v[50:51], v[158:159], v[50:51], v[162:163]
	v_pk_fma_f32 v[44:45], v[44:45], v[132:133], v[56:57]
	v_pk_fma_f32 v[46:47], v[46:47], v[130:131], v[48:49]
	v_pk_fma_f32 v[48:49], v[40:41], v[134:135], v[58:59]
	v_pk_fma_f32 v[50:51], v[42:43], v[128:129], v[50:51]
	v_cvt_pk_bf16_f32 v40, v44, v45
	v_cvt_pk_bf16_f32 v41, v46, v47
	v_cvt_pk_bf16_f32 v42, v48, v49
	v_cvt_pk_bf16_f32 v43, v50, v51
	global_store_dwordx4 v[60:61], v[40:43], off offset:256
	v_lshl_add_u64 v[44:45], s[76:77], 0, v[52:53]
	s_waitcnt vmcnt(8)
	v_mov_b32_e32 v40, v234
	v_mov_b32_e32 v41, v235
	v_mov_b32_e32 v42, v236
	v_mov_b32_e32 v43, v237
	v_lshlrev_b32_e32 v46, 16, v40
	v_and_b32_e32 v47, 0xffff0000, v40
	v_lshlrev_b32_e32 v40, 16, v41
	v_and_b32_e32 v41, 0xffff0000, v41
	v_lshlrev_b32_e32 v48, 16, v42
	v_and_b32_e32 v49, 0xffff0000, v42
	v_lshlrev_b32_e32 v42, 16, v43
	v_and_b32_e32 v43, 0xffff0000, v43
	v_pk_fma_f32 v[46:47], v[138:139], v[46:47], v[154:155]
	v_pk_fma_f32 v[40:41], v[140:141], v[40:41], v[150:151]
	v_pk_fma_f32 v[48:49], v[142:143], v[48:49], v[156:157]
	v_pk_fma_f32 v[42:43], v[146:147], v[42:43], v[152:153]
	v_pk_fma_f32 v[36:37], v[36:37], v[14:15], v[46:47]
	v_pk_fma_f32 v[38:39], v[38:39], v[10:11], v[40:41]
	v_pk_fma_f32 v[40:41], v[32:33], v[136:137], v[48:49]
	v_pk_fma_f32 v[42:43], v[34:35], v[12:13], v[42:43]
	v_cvt_pk_bf16_f32 v32, v36, v37
	v_cvt_pk_bf16_f32 v33, v38, v39
	v_cvt_pk_bf16_f32 v34, v40, v41
	v_cvt_pk_bf16_f32 v35, v42, v43
	global_store_dwordx4 v[44:45], v[32:35], off
	v_add_u32_e32 v36, 0xb0, v148
	v_ashrrev_i32_e32 v37, 31, v36
	v_lshlrev_b64 v[36:37], 10, v[36:37]
	v_lshl_add_u64 v[8:9], v[36:37], 0, v[8:9]
	v_lshlrev_b64 v[8:9], 1, v[8:9]
	v_lshl_add_u64 v[36:37], s[90:91], 0, v[8:9]
	s_waitcnt vmcnt(7)
	v_mov_b32_e32 v32, v238
	v_mov_b32_e32 v33, v239
	v_mov_b32_e32 v34, v240
	v_mov_b32_e32 v35, v241
	v_lshlrev_b32_e32 v38, 16, v32
	v_and_b32_e32 v39, 0xffff0000, v32
	v_lshlrev_b32_e32 v32, 16, v33
	v_and_b32_e32 v33, 0xffff0000, v33
	v_lshlrev_b32_e32 v40, 16, v34
	v_and_b32_e32 v41, 0xffff0000, v34
	v_lshlrev_b32_e32 v34, 16, v35
	v_and_b32_e32 v35, 0xffff0000, v35
	v_pk_fma_f32 v[38:39], v[166:167], v[38:39], v[172:173]
	v_pk_fma_f32 v[32:33], v[164:165], v[32:33], v[170:171]
	v_pk_fma_f32 v[40:41], v[160:161], v[40:41], v[168:169]
	v_pk_fma_f32 v[34:35], v[158:159], v[34:35], v[162:163]
	v_pk_fma_f32 v[28:29], v[28:29], v[132:133], v[38:39]
	v_pk_fma_f32 v[30:31], v[30:31], v[130:131], v[32:33]
	v_pk_fma_f32 v[32:33], v[24:25], v[134:135], v[40:41]
	v_pk_fma_f32 v[34:35], v[26:27], v[128:129], v[34:35]
	v_cvt_pk_bf16_f32 v24, v28, v29
	v_cvt_pk_bf16_f32 v25, v30, v31
	v_cvt_pk_bf16_f32 v26, v32, v33
	v_cvt_pk_bf16_f32 v27, v34, v35
	global_store_dwordx4 v[44:45], v[24:27], off offset:256
	v_lshl_add_u64 v[28:29], s[76:77], 0, v[8:9]
	s_waitcnt vmcnt(6)
	v_mov_b32_e32 v24, v242
	v_mov_b32_e32 v25, v243
	v_mov_b32_e32 v26, v244
	v_mov_b32_e32 v27, v245
	v_lshlrev_b32_e32 v8, 16, v24
	v_and_b32_e32 v9, 0xffff0000, v24
	v_lshlrev_b32_e32 v24, 16, v25
	v_and_b32_e32 v25, 0xffff0000, v25
	v_lshlrev_b32_e32 v30, 16, v26
	v_and_b32_e32 v31, 0xffff0000, v26
	v_lshlrev_b32_e32 v26, 16, v27
	v_and_b32_e32 v27, 0xffff0000, v27
	v_pk_fma_f32 v[8:9], v[138:139], v[8:9], v[154:155]
	v_pk_fma_f32 v[24:25], v[140:141], v[24:25], v[150:151]
	v_pk_fma_f32 v[30:31], v[142:143], v[30:31], v[156:157]
	v_pk_fma_f32 v[26:27], v[146:147], v[26:27], v[152:153]
	v_pk_fma_f32 v[8:9], v[20:21], v[14:15], v[8:9]
	v_pk_fma_f32 v[10:11], v[22:23], v[10:11], v[24:25]
	v_pk_fma_f32 v[14:15], v[16:17], v[136:137], v[30:31]
	v_pk_fma_f32 v[12:13], v[18:19], v[12:13], v[26:27]
	v_cvt_pk_bf16_f32 v8, v8, v9
	v_cvt_pk_bf16_f32 v9, v10, v11
	v_cvt_pk_bf16_f32 v10, v14, v15
	v_cvt_pk_bf16_f32 v11, v12, v13
	global_store_dwordx4 v[28:29], v[8:11], off
	s_waitcnt vmcnt(5)
	v_mov_b32_e32 v8, v226
	v_mov_b32_e32 v9, v227
	v_mov_b32_e32 v10, v228
	v_mov_b32_e32 v11, v229
	v_lshlrev_b32_e32 v12, 16, v8
	v_and_b32_e32 v13, 0xffff0000, v8
	v_lshlrev_b32_e32 v8, 16, v9
	v_and_b32_e32 v9, 0xffff0000, v9
	v_lshlrev_b32_e32 v14, 16, v10
	v_and_b32_e32 v15, 0xffff0000, v10
	v_lshlrev_b32_e32 v10, 16, v11
	v_and_b32_e32 v11, 0xffff0000, v11
	v_pk_fma_f32 v[12:13], v[166:167], v[12:13], v[172:173]
	v_pk_fma_f32 v[8:9], v[164:165], v[8:9], v[170:171]
	v_pk_fma_f32 v[14:15], v[160:161], v[14:15], v[168:169]
	v_pk_fma_f32 v[10:11], v[158:159], v[10:11], v[162:163]
	v_pk_fma_f32 v[4:5], v[4:5], v[132:133], v[12:13]
	v_pk_fma_f32 v[6:7], v[6:7], v[130:131], v[8:9]
	v_pk_fma_f32 v[8:9], v[0:1], v[134:135], v[14:15]
	v_pk_fma_f32 v[10:11], v[2:3], v[128:129], v[10:11]
	v_cvt_pk_bf16_f32 v0, v4, v5
	v_cvt_pk_bf16_f32 v1, v6, v7
	v_cvt_pk_bf16_f32 v2, v8, v9
	v_cvt_pk_bf16_f32 v3, v10, v11
	global_store_dwordx4 v[28:29], v[0:3], off offset:256
	s_cbranch_vccnz .LBB0_2129
	s_andn2_b64 vcc, exec, s[6:7]
	s_cbranch_vccnz .LBB0_2128
	s_barrier
	s_branch .LBB0_2128

.LBB0_2276:
	global_load_dword v2, v1, s[6:7] sc1
	s_add_i32 s3, s3, 1
	s_mov_b64 s[14:15], -1
	s_waitcnt vmcnt(0)
	v_cmp_ge_u32_e64 s[10:11], v2, v0
	s_branch .LBB0_2273

.LBB0_2895:
	s_or_b64 exec, exec, s[2:3]
	s_getreg_b32 s0, hwreg(HW_REG_HW_ID, 0, 6)
	s_lshl_b32 s0, s0, 2
	s_and_b32 s0, s0, 0xfc
	s_add_i32 s0, s0, 0
	s_add_i32 s0, s0, 0x25c00
	v_mov_b32_e32 v0, s0
	ds_read_b32 v0, v0
	s_waitcnt lgkmcnt(0)
	v_readfirstlane_b32 s0, v0
	v_mbcnt_lo_u32_b32 v0, -1, 0
	v_mbcnt_hi_u32_b32 v0, -1, v0
	s_nop 1
	v_lshl_add_u32 v0, s0, 6, v0
	s_nop 0
	v_cmp_eq_u32_e32 vcc, 0, v0
	s_and_saveexec_b64 s[0:1], vcc
	s_cbranch_execz .LBB0_2925
	s_add_i32 s2, 0, 0x24808
	v_mov_b32_e32 v0, s2
	s_add_i32 s2, 0, 0x2480c
	v_mov_b32_e32 v1, s2
	ds_read_b32 v0, v0
	ds_read_b32 v1, v1
	s_waitcnt lgkmcnt(0)
	v_cmp_eq_u32_e32 vcc, 0, v1
	s_cbranch_vccnz .LBB0_2906
	v_mov_b32_e32 v1, 0x3000
	s_add_i32 s2, 0, 0x24804
	v_mov_b32_e32 v3, s2
	ds_read_b32 v3, v3
	global_load_dword v1, v1, s[94:95] offset:1024 sc1
	s_waitcnt lgkmcnt(0)
	v_mul_lo_u32 v0, v0, v3
	s_add_u32 s2, s94, 0x3400
	s_addc_u32 s3, s95, 0
	s_waitcnt vmcnt(0)
	v_cmp_ge_u32_e32 vcc, v1, v0
	s_cbranch_vccnz .LBB0_2911
	s_mov_b32 s10, 1
	v_mov_b32_e32 v1, 0
	s_branch .LBB0_2900

.LBB0_2902:
	global_load_dword v2, v1, s[2:3] sc1
	s_add_i32 s10, s10, 1
	s_mov_b64 s[6:7], -1
	s_waitcnt vmcnt(0)
	v_cmp_ge_u32_e64 s[4:5], v2, v0
	s_branch .LBB0_2899
